# late offset-restoring barrier for the trailing half in P1/P3/P6/P7 K-loop entry + P6 next-unit gather ids loaded early + P6/P7 bias loads hoisted above the align barrier
# speedup vs baseline: 1.0225x; 1.0011x over previous
.LBB0_93:
	v_lshrrev_b32_e32 v2, 4, v0
	v_lshrrev_b32_e32 v168, 3, v0
	v_and_b32_e32 v3, 7, v0
	v_and_b32_e32 v4, 4, v2
	v_lshrrev_b32_e32 v5, 5, v0
	v_and_b32_e32 v6, 2, v168
	v_lshrrev_b32_e32 v8, 2, v0
	v_and_b32_e32 v5, 4, v5
	v_bitop3_b32 v6, v6, v3, v4 bitop3:0x36
	v_and_b32_e32 v7, 35, v168
	v_and_b32_e32 v8, 24, v8
	v_or3_b32 v7, v7, v8, v5
	v_lshlrev_b32_e32 v169, 4, v6
	v_lshl_or_b32 v142, v7, 12, v169
	v_bitop3_b32 v7, v168, 2, 64 bitop3:0xc8
	s_movk_i32 s0, 0x63
	v_bitop3_b32 v3, v7, v3, v4 bitop3:0x36
	v_bitop3_b32 v4, v168, s0, 64 bitop3:0xc8
	v_or3_b32 v4, v4, v8, v5
	v_lshlrev_b32_e32 v171, 4, v3
	v_or_b32_e32 v170, 64, v168
	v_lshl_or_b32 v144, v4, 12, v171
	v_lshlrev_b32_e32 v4, 11, v168
	v_lshl_or_b32 v172, v6, 3, v4
	v_lshlrev_b32_e32 v4, 11, v170
	s_lshr_b32 s0, s14, 6
	v_lshl_or_b32 v173, v3, 3, v4
	s_lshl_b32 s76, s0, 10
	v_mov_b32_e32 v3, 0x7f7f7f7f
	s_lshl_b32 s8, s10, 19
	s_lshl_b32 s9, s10, 8
	s_add_i32 s77, s76, 0
	v_or_b32_e32 v3, s8, v172
	s_bitset1_b32 s9, 7
	s_add_i32 m0, s77, 0x10000
	s_lshr_b32 s1, s14, 8
	v_lshlrev_b32_e32 v146, 1, v3
	v_or_b32_e32 v3, s9, v168
	global_load_lds_dwordx4 v142, s[66:67]
	s_add_i32 m0, s77, 0x12000
	v_lshl_or_b32 v132, v3, 12, v169
	v_or_b32_e32 v3, s8, v173
	s_add_u32 s8, s66, 0x80000
	v_lshlrev_b32_e32 v130, 1, v3
	v_or_b32_e32 v3, s9, v170
	global_load_lds_dwordx4 v144, s[66:67]
	s_addc_u32 s9, s67, 0
	s_add_i32 m0, s77, 0x14000
	s_add_i32 s78, s77, 0x2000
	global_load_lds_dwordx4 v142, s[8:9]
	s_add_i32 m0, s77, 0x16000
	v_mov_b32_e32 v147, 0
	global_load_lds_dwordx4 v144, s[8:9]
	s_mov_b32 m0, s77
	s_add_i32 s79, s77, 0x4000
	global_load_lds_dwordx4 v146, s[64:65]
	s_mov_b32 m0, s78
	v_mov_b32_e32 v143, v147
	global_load_lds_dwordx4 v130, s[64:65]
	s_mov_b32 m0, s79
	s_add_i32 s80, s77, 0x6000
	v_lshl_or_b32 v134, v3, 12, v171
	v_lshl_add_u64 v[4:5], s[66:67], 0, v[142:143]
	global_load_lds_dwordx4 v132, s[64:65]
	s_mov_b32 m0, s80
	s_mov_b64 s[8:9], 0x80
	v_mov_b32_e32 v145, v147
	global_load_lds_dwordx4 v134, s[64:65]
	s_add_i32 m0, s77, 0x18000
	v_lshl_add_u64 v[4:5], v[4:5], 0, s[8:9]
	v_lshl_add_u64 v[6:7], s[66:67], 0, v[144:145]
	global_load_lds_dwordx4 v[4:5], off
	s_add_i32 m0, s77, 0x1a000
	v_lshl_add_u64 v[4:5], v[6:7], 0, s[8:9]
	s_add_u32 s12, s66, 0x80080
	v_writelane_b32 v254, s13, 24
	global_load_lds_dwordx4 v[4:5], off
	s_addc_u32 s13, s67, 0
	s_add_i32 m0, s77, 0x1c000
	v_writelane_b32 v254, s92, 26
	global_load_lds_dwordx4 v142, s[12:13]
	s_add_i32 m0, s77, 0x1e000
	v_writelane_b32 v254, s96, 27
	global_load_lds_dwordx4 v144, s[12:13]
	s_waitcnt vmcnt(6)
	s_nop 0
	v_writelane_b32 v254, s97, 28
	s_cmp_eq_u32 s1, 1
	v_writelane_b32 v254, s95, 29
	s_mov_b32 s11, 0
	s_cselect_b64 s[12:13], -1, 0
	s_cmp_lg_u32 s1, 1
	s_barrier
	s_cbranch_scc1 .LBB0_95
.LBB0_95:
	s_ashr_i32 s81, s94, 31
	s_ashr_i32 s82, s69, 31
	s_add_u32 s16, s24, 0x1000
	s_addc_u32 s17, s25, 0
	v_writelane_b32 v254, s16, 30
	v_lshrrev_b32_e32 v5, 1, v0
	v_and_b32_e32 v3, 15, v0
	v_writelane_b32 v254, s17, 31
	s_add_u32 s16, s24, 0x1200
	s_addc_u32 s17, s25, 0
	s_lshl_b32 s0, s0, 5
	s_and_b32 s0, s0, 0x60
	s_add_u32 s83, s2, 0x54800000
	s_addc_u32 s84, s3, 0
	s_add_u32 s18, s2, 0x58800000
	s_addc_u32 s19, s3, 0
	s_add_u32 s85, s2, 0x5a800000
	s_addc_u32 s86, s3, 0
	s_add_u32 s20, s2, 0x5c800000
	s_addc_u32 s21, s3, 0
	s_add_u32 s22, s2, 0x62800000
	s_addc_u32 s23, s3, 0
	s_add_u32 s26, s2, 0x62c00000
	s_addc_u32 s27, s3, 0
	s_add_u32 s34, s2, 0x5e800000
	v_and_b32_e32 v2, 3, v2
	v_and_b32_e32 v4, 2, v0
	v_and_b32_e32 v5, 4, v5
	s_addc_u32 s35, s3, 0
	v_bitop3_b32 v4, v5, v2, v4 bitop3:0x36
	v_lshl_or_b32 v174, s1, 6, v3
	s_add_u32 s36, s2, 0x100000
	v_lshlrev_b32_e32 v4, 4, v4
	v_lshlrev_b32_e32 v5, 7, v174
	v_or_b32_e32 v3, s0, v3
	s_addc_u32 s37, s3, 0
	v_or_b32_e32 v6, v5, v4
	v_lshlrev_b32_e32 v3, 7, v3
	v_bitop3_b32 v5, v5, 64, v4 bitop3:0x36
	s_cmpk_lt_u32 s14, 0x100
	v_or_b32_e32 v175, v3, v4
	v_bitop3_b32 v176, v3, 64, v4 bitop3:0x36
	s_cselect_b64 s[38:39], -1, 0
	v_lshl_or_b32 v177, v2, 3, s0
	v_mov_b64_e32 v[148:149], 0x53f
	s_add_i32 s87, 0, 0x10000
	s_add_i32 s88, 0, 0x10800
	s_add_i32 s89, 0, 0x14000
	s_add_i32 s90, 0, 0x14800
	v_add_u32_e32 v178, 0, v6
	v_add_u32_e32 v179, 0, v5
	s_add_i32 s92, 0, 0x18000
	s_add_i32 s93, 0, 0x18800
	s_add_i32 s94, 0, 0x1c000
	s_add_i32 s95, 0, 0x1c800
	s_mov_b32 s40, 0x3e000000
	s_mov_b32 s96, 0x40000
	s_mov_b32 s97, 0x48000
	s_mov_b32 s41, 0x50000
	s_mov_b32 s91, 0
	s_mov_b64 s[44:45], s[66:67]
	s_mov_b64 s[46:47], s[64:65]
	s_branch .LBB0_98

.LBB0_100:
	s_lshl_b32 s15, s14, 19
	s_lshl_b32 s43, s14, 8
	v_or_b32_e32 v2, s15, v172
	s_bitset1_b32 s43, 7
	v_lshlrev_b32_e32 v136, 1, v2
	v_or_b32_e32 v2, s43, v168
	v_lshl_or_b32 v138, v2, 12, v169
	v_or_b32_e32 v2, s15, v173
	s_add_u32 s68, s64, 0x80
	v_lshlrev_b32_e32 v140, 1, v2
	v_or_b32_e32 v2, s43, v170
	s_addc_u32 s69, s65, 0
	v_lshl_or_b32 v150, v2, 12, v171
	v_mov_b32_e32 v131, v147
	v_mov_b32_e32 v133, v147
	v_mov_b32_e32 v135, v147
	s_add_u32 s15, s66, 0x100
	v_mov_b32_e32 v2, 0
	v_mov_b32_e32 v137, v147
	v_mov_b32_e32 v141, v147
	v_mov_b32_e32 v139, v147
	v_mov_b32_e32 v151, v147
	v_lshl_add_u64 v[152:153], s[68:69], 0, v[134:135]
	v_lshl_add_u64 v[154:155], s[68:69], 0, v[132:133]
	v_lshl_add_u64 v[156:157], s[68:69], 0, v[130:131]
	v_lshl_add_u64 v[158:159], s[68:69], 0, v[146:147]
	s_addc_u32 s43, s67, 0
	s_mov_b32 s72, -2
	s_mov_b64 s[66:67], 0
	v_mov_b32_e32 v3, v2
	v_mov_b32_e32 v4, v2
	v_mov_b32_e32 v5, v2
	v_mov_b32_e32 v6, v2
	v_mov_b32_e32 v7, v2
	v_mov_b32_e32 v8, v2
	v_mov_b32_e32 v9, v2
	v_mov_b32_e32 v10, v2
	v_mov_b32_e32 v11, v2
	v_mov_b32_e32 v12, v2
	v_mov_b32_e32 v13, v2
	v_mov_b32_e32 v14, v2
	v_mov_b32_e32 v15, v2
	v_mov_b32_e32 v16, v2
	v_mov_b32_e32 v17, v2
	v_mov_b32_e32 v18, v2
	v_mov_b32_e32 v19, v2
	v_mov_b32_e32 v20, v2
	v_mov_b32_e32 v21, v2
	v_mov_b32_e32 v22, v2
	v_mov_b32_e32 v23, v2
	v_mov_b32_e32 v24, v2
	v_mov_b32_e32 v25, v2
	v_mov_b32_e32 v26, v2
	v_mov_b32_e32 v27, v2
	v_mov_b32_e32 v28, v2
	v_mov_b32_e32 v29, v2
	v_mov_b32_e32 v30, v2
	v_mov_b32_e32 v31, v2
	v_mov_b32_e32 v32, v2
	v_mov_b32_e32 v33, v2
	v_mov_b32_e32 v66, v2
	v_mov_b32_e32 v67, v2
	v_mov_b32_e32 v68, v2
	v_mov_b32_e32 v69, v2
	v_mov_b32_e32 v70, v2
	v_mov_b32_e32 v71, v2
	v_mov_b32_e32 v72, v2
	v_mov_b32_e32 v73, v2
	v_mov_b32_e32 v74, v2
	v_mov_b32_e32 v75, v2
	v_mov_b32_e32 v76, v2
	v_mov_b32_e32 v77, v2
	v_mov_b32_e32 v78, v2
	v_mov_b32_e32 v79, v2
	v_mov_b32_e32 v80, v2
	v_mov_b32_e32 v81, v2
	v_mov_b32_e32 v82, v2
	v_mov_b32_e32 v83, v2
	v_mov_b32_e32 v84, v2
	v_mov_b32_e32 v85, v2
	v_mov_b32_e32 v86, v2
	v_mov_b32_e32 v87, v2
	v_mov_b32_e32 v88, v2
	v_mov_b32_e32 v89, v2
	v_mov_b32_e32 v90, v2
	v_mov_b32_e32 v91, v2
	v_mov_b32_e32 v92, v2
	v_mov_b32_e32 v93, v2
	v_mov_b32_e32 v94, v2
	v_mov_b32_e32 v95, v2
	v_mov_b32_e32 v96, v2
	v_mov_b32_e32 v97, v2
	v_mov_b32_e32 v34, v2
	v_mov_b32_e32 v35, v2
	v_mov_b32_e32 v36, v2
	v_mov_b32_e32 v37, v2
	v_mov_b32_e32 v38, v2
	v_mov_b32_e32 v39, v2
	v_mov_b32_e32 v40, v2
	v_mov_b32_e32 v41, v2
	v_mov_b32_e32 v42, v2
	v_mov_b32_e32 v43, v2
	v_mov_b32_e32 v44, v2
	v_mov_b32_e32 v45, v2
	v_mov_b32_e32 v46, v2
	v_mov_b32_e32 v47, v2
	v_mov_b32_e32 v48, v2
	v_mov_b32_e32 v49, v2
	v_mov_b32_e32 v50, v2
	v_mov_b32_e32 v51, v2
	v_mov_b32_e32 v52, v2
	v_mov_b32_e32 v53, v2
	v_mov_b32_e32 v54, v2
	v_mov_b32_e32 v55, v2
	v_mov_b32_e32 v56, v2
	v_mov_b32_e32 v57, v2
	v_mov_b32_e32 v58, v2
	v_mov_b32_e32 v59, v2
	v_mov_b32_e32 v60, v2
	v_mov_b32_e32 v61, v2
	v_mov_b32_e32 v62, v2
	v_mov_b32_e32 v63, v2
	v_mov_b32_e32 v64, v2
	v_mov_b32_e32 v65, v2
	v_mov_b32_e32 v98, v2
	v_mov_b32_e32 v99, v2
	v_mov_b32_e32 v100, v2
	v_mov_b32_e32 v101, v2
	v_mov_b32_e32 v102, v2
	v_mov_b32_e32 v103, v2
	v_mov_b32_e32 v104, v2
	v_mov_b32_e32 v105, v2
	v_mov_b32_e32 v106, v2
	v_mov_b32_e32 v107, v2
	v_mov_b32_e32 v108, v2
	v_mov_b32_e32 v109, v2
	v_mov_b32_e32 v110, v2
	v_mov_b32_e32 v111, v2
	v_mov_b32_e32 v112, v2
	v_mov_b32_e32 v113, v2
	v_mov_b32_e32 v114, v2
	v_mov_b32_e32 v115, v2
	v_mov_b32_e32 v116, v2
	v_mov_b32_e32 v117, v2
	v_mov_b32_e32 v118, v2
	v_mov_b32_e32 v119, v2
	v_mov_b32_e32 v120, v2
	v_mov_b32_e32 v121, v2
	v_mov_b32_e32 v122, v2
	v_mov_b32_e32 v123, v2
	v_mov_b32_e32 v124, v2
	v_mov_b32_e32 v125, v2
	v_mov_b32_e32 v126, v2
	v_mov_b32_e32 v127, v2
	v_mov_b32_e32 v128, v2
	v_mov_b32_e32 v129, v2
	s_andn2_b64 vcc, exec, s[12:13]
	s_cbranch_vccnz .Lp1_entry
	s_barrier
.Lp1_entry:
	s_branch .LBB0_102
.LBB0_101:
	s_add_u32 s70, s64, s66
	s_addc_u32 s71, s65, s67
	s_add_u32 s73, s70, 0x100
	v_add_u32_e32 v184, s87, v175
	v_add_u32_e32 v188, s87, v176
	v_add_u32_e32 v192, s88, v175
	v_add_u32_e32 v196, s88, v176
	v_add_u32_e32 v200, s89, v175
	v_add_u32_e32 v204, s89, v176
	v_add_u32_e32 v208, s90, v175
	v_add_u32_e32 v212, s90, v176
	s_addc_u32 vcc_lo, s71, 0
	ds_read_b128 v[184:187], v184
	ds_read_b128 v[188:191], v188
	ds_read_b128 v[192:195], v192
	ds_read_b128 v[196:199], v196
	ds_read_b128 v[200:203], v200
	ds_read_b128 v[204:207], v204
	ds_read_b128 v[208:211], v208
	ds_read_b128 v[212:215], v212
	s_and_b64 s[70:71], s[68:69], exec
	s_cselect_b32 s71, s47, vcc_lo
	s_cselect_b32 s70, s46, s73
	s_add_u32 s73, s15, s66
	s_addc_u32 vcc_lo, s43, s67
	s_and_b64 s[68:69], s[68:69], exec
	s_cselect_b32 s69, s45, vcc_lo
	s_cselect_b32 s68, s44, s73
	v_lshl_add_u64 v[248:249], v[158:159], 0, s[66:67]
	s_add_i32 m0, s77, 0x8000
	ds_read_b128 v[216:219], v178
	ds_read_b128 v[220:223], v178 offset:2048
	ds_read_b128 v[224:227], v179
	ds_read_b128 v[228:231], v179 offset:2048
	ds_read_b128 v[232:235], v178 offset:4096
	ds_read_b128 v[236:239], v178 offset:6144
	ds_read_b128 v[240:243], v179 offset:4096
	ds_read_b128 v[244:247], v179 offset:6144
	global_load_lds_dwordx4 v[248:249], off
	v_lshl_add_u64 v[248:249], v[156:157], 0, s[66:67]
	s_add_i32 m0, s77, 0xa000
	s_nop 0
	global_load_lds_dwordx4 v[248:249], off
	v_lshl_add_u64 v[248:249], v[154:155], 0, s[66:67]
	s_add_i32 m0, s77, 0xc000
	s_nop 0
	global_load_lds_dwordx4 v[248:249], off
	v_lshl_add_u64 v[248:249], v[152:153], 0, s[66:67]
	s_add_i32 m0, s77, 0xe000
	s_nop 0
	global_load_lds_dwordx4 v[248:249], off
	s_waitcnt vmcnt(8)
	s_waitcnt lgkmcnt(0)
	s_barrier
	s_setprio 1
	s_waitcnt lgkmcnt(0)
	v_mfma_f32_16x16x32_bf16 v[126:129], v[184:187], v[216:219], v[126:129]
	v_mfma_f32_16x16x32_bf16 v[122:125], v[192:195], v[216:219], v[122:125]
	v_mfma_f32_16x16x32_bf16 v[118:121], v[184:187], v[220:223], v[118:121]
	v_mfma_f32_16x16x32_bf16 v[114:117], v[192:195], v[220:223], v[114:117]
	v_mfma_f32_16x16x32_bf16 v[110:113], v[184:187], v[232:235], v[110:113]
	v_mfma_f32_16x16x32_bf16 v[106:109], v[192:195], v[232:235], v[106:109]
	v_mfma_f32_16x16x32_bf16 v[102:105], v[184:187], v[236:239], v[102:105]
	v_mfma_f32_16x16x32_bf16 v[98:101], v[192:195], v[236:239], v[98:101]
	v_mfma_f32_16x16x32_bf16 v[126:129], v[188:191], v[224:227], v[126:129]
	v_mfma_f32_16x16x32_bf16 v[122:125], v[196:199], v[224:227], v[122:125]
	v_mfma_f32_16x16x32_bf16 v[118:121], v[188:191], v[228:231], v[118:121]
	v_mfma_f32_16x16x32_bf16 v[114:117], v[196:199], v[228:231], v[114:117]
	v_mfma_f32_16x16x32_bf16 v[110:113], v[188:191], v[240:243], v[110:113]
	v_mfma_f32_16x16x32_bf16 v[106:109], v[196:199], v[240:243], v[106:109]
	v_mfma_f32_16x16x32_bf16 v[102:105], v[188:191], v[244:247], v[102:105]
	v_mfma_f32_16x16x32_bf16 v[98:101], v[196:199], v[244:247], v[98:101]
	s_setprio 0
	s_setprio 1
	v_mfma_f32_16x16x32_bf16 v[62:65], v[200:203], v[216:219], v[62:65]
	v_mfma_f32_16x16x32_bf16 v[58:61], v[208:211], v[216:219], v[58:61]
	v_mfma_f32_16x16x32_bf16 v[54:57], v[200:203], v[220:223], v[54:57]
	v_mfma_f32_16x16x32_bf16 v[50:53], v[208:211], v[220:223], v[50:53]
	v_mfma_f32_16x16x32_bf16 v[46:49], v[200:203], v[232:235], v[46:49]
	v_mfma_f32_16x16x32_bf16 v[42:45], v[208:211], v[232:235], v[42:45]
	v_mfma_f32_16x16x32_bf16 v[38:41], v[200:203], v[236:239], v[38:41]
	v_mfma_f32_16x16x32_bf16 v[34:37], v[208:211], v[236:239], v[34:37]
	v_mfma_f32_16x16x32_bf16 v[62:65], v[204:207], v[224:227], v[62:65]
	v_mfma_f32_16x16x32_bf16 v[58:61], v[212:215], v[224:227], v[58:61]
	v_mfma_f32_16x16x32_bf16 v[54:57], v[204:207], v[228:231], v[54:57]
	v_mfma_f32_16x16x32_bf16 v[50:53], v[212:215], v[228:231], v[50:53]
	v_mfma_f32_16x16x32_bf16 v[46:49], v[204:207], v[240:243], v[46:49]
	v_mfma_f32_16x16x32_bf16 v[42:45], v[212:215], v[240:243], v[42:45]
	v_mfma_f32_16x16x32_bf16 v[38:41], v[204:207], v[244:247], v[38:41]
	v_mfma_f32_16x16x32_bf16 v[34:37], v[212:215], v[244:247], v[34:37]
	s_setprio 0
	s_barrier
	s_add_i32 s73, s87, s76
	v_lshl_add_u64 v[248:249], s[68:69], 0, v[142:143]
	s_mov_b32 m0, s73
	ds_read_b128 v[216:219], v178 offset:16384
	ds_read_b128 v[220:223], v178 offset:18432
	ds_read_b128 v[224:227], v179 offset:16384
	ds_read_b128 v[228:231], v179 offset:18432
	ds_read_b128 v[232:235], v178 offset:20480
	ds_read_b128 v[236:239], v178 offset:22528
	ds_read_b128 v[240:243], v179 offset:20480
	ds_read_b128 v[244:247], v179 offset:22528
	global_load_lds_dwordx4 v[248:249], off
	s_add_i32 m0, s73, 0x2000
	s_add_u32 vcc_lo, s68, 0x80000
	v_lshl_add_u64 v[250:251], s[68:69], 0, v[144:145]
	s_addc_u32 vcc_hi, s69, 0
	s_add_i32 s73, s89, s76
	global_load_lds_dwordx4 v[250:251], off
	v_lshl_add_u64 v[252:253], vcc, 0, v[142:143]
	s_mov_b32 m0, s73
	s_nop 0
	global_load_lds_dwordx4 v[252:253], off
	v_lshl_add_u64 v[252:253], vcc, 0, v[144:145]
	s_add_i32 m0, s73, 0x2000
	s_nop 0
	global_load_lds_dwordx4 v[252:253], off
	s_waitcnt vmcnt(6)
	s_waitcnt lgkmcnt(0)
	s_barrier
	s_setprio 1
	s_waitcnt lgkmcnt(0)
	v_mfma_f32_16x16x32_bf16 v[94:97], v[184:187], v[216:219], v[94:97]
	v_mfma_f32_16x16x32_bf16 v[90:93], v[192:195], v[216:219], v[90:93]
	v_mfma_f32_16x16x32_bf16 v[86:89], v[184:187], v[220:223], v[86:89]
	v_mfma_f32_16x16x32_bf16 v[82:85], v[192:195], v[220:223], v[82:85]
	v_mfma_f32_16x16x32_bf16 v[78:81], v[184:187], v[232:235], v[78:81]
	v_mfma_f32_16x16x32_bf16 v[74:77], v[192:195], v[232:235], v[74:77]
	v_mfma_f32_16x16x32_bf16 v[70:73], v[184:187], v[236:239], v[70:73]
	v_mfma_f32_16x16x32_bf16 v[66:69], v[192:195], v[236:239], v[66:69]
	v_mfma_f32_16x16x32_bf16 v[94:97], v[188:191], v[224:227], v[94:97]
	v_mfma_f32_16x16x32_bf16 v[90:93], v[196:199], v[224:227], v[90:93]
	v_mfma_f32_16x16x32_bf16 v[86:89], v[188:191], v[228:231], v[86:89]
	v_mfma_f32_16x16x32_bf16 v[82:85], v[196:199], v[228:231], v[82:85]
	v_mfma_f32_16x16x32_bf16 v[78:81], v[188:191], v[240:243], v[78:81]
	v_mfma_f32_16x16x32_bf16 v[74:77], v[196:199], v[240:243], v[74:77]
	v_mfma_f32_16x16x32_bf16 v[70:73], v[188:191], v[244:247], v[70:73]
	v_mfma_f32_16x16x32_bf16 v[66:69], v[196:199], v[244:247], v[66:69]
	s_setprio 0
	s_setprio 1
	v_mfma_f32_16x16x32_bf16 v[30:33], v[200:203], v[216:219], v[30:33]
	v_mfma_f32_16x16x32_bf16 v[26:29], v[208:211], v[216:219], v[26:29]
	v_mfma_f32_16x16x32_bf16 v[22:25], v[200:203], v[220:223], v[22:25]
	v_mfma_f32_16x16x32_bf16 v[18:21], v[208:211], v[220:223], v[18:21]
	v_mfma_f32_16x16x32_bf16 v[14:17], v[200:203], v[232:235], v[14:17]
	v_mfma_f32_16x16x32_bf16 v[10:13], v[208:211], v[232:235], v[10:13]
	v_mfma_f32_16x16x32_bf16 v[6:9], v[200:203], v[236:239], v[6:9]
	v_mfma_f32_16x16x32_bf16 v[2:5], v[208:211], v[236:239], v[2:5]
	v_mfma_f32_16x16x32_bf16 v[30:33], v[204:207], v[224:227], v[30:33]
	v_mfma_f32_16x16x32_bf16 v[26:29], v[212:215], v[224:227], v[26:29]
	v_mfma_f32_16x16x32_bf16 v[22:25], v[204:207], v[228:231], v[22:25]
	v_mfma_f32_16x16x32_bf16 v[18:21], v[212:215], v[228:231], v[18:21]
	v_mfma_f32_16x16x32_bf16 v[14:17], v[204:207], v[240:243], v[14:17]
	v_mfma_f32_16x16x32_bf16 v[10:13], v[212:215], v[240:243], v[10:13]
	v_mfma_f32_16x16x32_bf16 v[6:9], v[204:207], v[244:247], v[6:9]
	v_mfma_f32_16x16x32_bf16 v[2:5], v[212:215], v[244:247], v[2:5]
	s_setprio 0
	s_barrier
	v_add_u32_e32 v184, s92, v175
	v_add_u32_e32 v188, s92, v176
	v_add_u32_e32 v192, s93, v175
	v_add_u32_e32 v196, s93, v176
	v_add_u32_e32 v200, s94, v175
	v_add_u32_e32 v204, s94, v176
	v_add_u32_e32 v208, s95, v175
	v_add_u32_e32 v212, s95, v176
	ds_read_b128 v[184:187], v184
	ds_read_b128 v[188:191], v188
	ds_read_b128 v[192:195], v192
	ds_read_b128 v[196:199], v196
	ds_read_b128 v[200:203], v200
	ds_read_b128 v[204:207], v204
	ds_read_b128 v[208:211], v208
	ds_read_b128 v[212:215], v212
	s_mov_b32 m0, s77
	v_lshl_add_u64 v[166:167], s[70:71], 0, v[166:167]
	ds_read_b128 v[216:219], v178 offset:32768
	ds_read_b128 v[220:223], v178 offset:34816
	ds_read_b128 v[224:227], v179 offset:32768
	ds_read_b128 v[228:231], v179 offset:34816
	ds_read_b128 v[232:235], v178 offset:36864
	ds_read_b128 v[236:239], v178 offset:38912
	ds_read_b128 v[240:243], v179 offset:36864
	ds_read_b128 v[244:247], v179 offset:38912
	global_load_lds_dwordx4 v[166:167], off
	v_lshl_add_u64 v[164:165], s[70:71], 0, v[164:165]
	s_mov_b32 m0, s78
	v_lshl_add_u64 v[162:163], s[70:71], 0, v[162:163]
	global_load_lds_dwordx4 v[164:165], off
	s_mov_b32 m0, s79
	v_lshl_add_u64 v[160:161], s[70:71], 0, v[160:161]
	global_load_lds_dwordx4 v[162:163], off
	s_mov_b32 m0, s80
	s_nop 0
	global_load_lds_dwordx4 v[160:161], off
	s_waitcnt vmcnt(8)
	s_waitcnt lgkmcnt(0)
	s_barrier
	s_setprio 1
	s_waitcnt lgkmcnt(0)
	v_mfma_f32_16x16x32_bf16 v[126:129], v[184:187], v[216:219], v[126:129]
	v_mfma_f32_16x16x32_bf16 v[122:125], v[192:195], v[216:219], v[122:125]
	v_mfma_f32_16x16x32_bf16 v[118:121], v[184:187], v[220:223], v[118:121]
	v_mfma_f32_16x16x32_bf16 v[114:117], v[192:195], v[220:223], v[114:117]
	v_mfma_f32_16x16x32_bf16 v[110:113], v[184:187], v[232:235], v[110:113]
	v_mfma_f32_16x16x32_bf16 v[106:109], v[192:195], v[232:235], v[106:109]
	v_mfma_f32_16x16x32_bf16 v[102:105], v[184:187], v[236:239], v[102:105]
	v_mfma_f32_16x16x32_bf16 v[98:101], v[192:195], v[236:239], v[98:101]
	v_mfma_f32_16x16x32_bf16 v[126:129], v[188:191], v[224:227], v[126:129]
	v_mfma_f32_16x16x32_bf16 v[122:125], v[196:199], v[224:227], v[122:125]
	v_mfma_f32_16x16x32_bf16 v[118:121], v[188:191], v[228:231], v[118:121]
	v_mfma_f32_16x16x32_bf16 v[114:117], v[196:199], v[228:231], v[114:117]
	v_mfma_f32_16x16x32_bf16 v[110:113], v[188:191], v[240:243], v[110:113]
	v_mfma_f32_16x16x32_bf16 v[106:109], v[196:199], v[240:243], v[106:109]
	v_mfma_f32_16x16x32_bf16 v[102:105], v[188:191], v[244:247], v[102:105]
	v_mfma_f32_16x16x32_bf16 v[98:101], v[196:199], v[244:247], v[98:101]
	s_setprio 0
	s_setprio 1
	v_mfma_f32_16x16x32_bf16 v[62:65], v[200:203], v[216:219], v[62:65]
	v_mfma_f32_16x16x32_bf16 v[58:61], v[208:211], v[216:219], v[58:61]
	v_mfma_f32_16x16x32_bf16 v[54:57], v[200:203], v[220:223], v[54:57]
	v_mfma_f32_16x16x32_bf16 v[50:53], v[208:211], v[220:223], v[50:53]
	v_mfma_f32_16x16x32_bf16 v[46:49], v[200:203], v[232:235], v[46:49]
	v_mfma_f32_16x16x32_bf16 v[42:45], v[208:211], v[232:235], v[42:45]
	v_mfma_f32_16x16x32_bf16 v[38:41], v[200:203], v[236:239], v[38:41]
	v_mfma_f32_16x16x32_bf16 v[34:37], v[208:211], v[236:239], v[34:37]
	v_mfma_f32_16x16x32_bf16 v[62:65], v[204:207], v[224:227], v[62:65]
	v_mfma_f32_16x16x32_bf16 v[58:61], v[212:215], v[224:227], v[58:61]
	v_mfma_f32_16x16x32_bf16 v[54:57], v[204:207], v[228:231], v[54:57]
	v_mfma_f32_16x16x32_bf16 v[50:53], v[212:215], v[228:231], v[50:53]
	v_mfma_f32_16x16x32_bf16 v[46:49], v[204:207], v[240:243], v[46:49]
	v_mfma_f32_16x16x32_bf16 v[42:45], v[212:215], v[240:243], v[42:45]
	v_mfma_f32_16x16x32_bf16 v[38:41], v[204:207], v[244:247], v[38:41]
	v_mfma_f32_16x16x32_bf16 v[34:37], v[212:215], v[244:247], v[34:37]
	s_setprio 0
	s_barrier
	s_add_i32 s70, s92, s76
	v_lshl_add_u64 v[240:241], v[248:249], 0, s[8:9]
	s_mov_b32 m0, s70
	ds_read_b128 v[160:163], v178 offset:49152
	ds_read_b128 v[164:167], v178 offset:51200
	ds_read_b128 v[216:219], v179 offset:49152
	ds_read_b128 v[220:223], v179 offset:51200
	ds_read_b128 v[224:227], v178 offset:53248
	ds_read_b128 v[228:231], v178 offset:55296
	ds_read_b128 v[232:235], v179 offset:53248
	ds_read_b128 v[236:239], v179 offset:55296
	global_load_lds_dwordx4 v[240:241], off
	s_add_i32 m0, s70, 0x2000
	s_add_u32 s68, s68, 0x80080
	v_lshl_add_u64 v[240:241], v[250:251], 0, s[8:9]
	s_addc_u32 s69, s69, 0
	s_add_i32 s70, s94, s76
	global_load_lds_dwordx4 v[240:241], off
	v_lshl_add_u64 v[240:241], s[68:69], 0, v[142:143]
	s_mov_b32 m0, s70
	s_nop 0
	global_load_lds_dwordx4 v[240:241], off
	v_lshl_add_u64 v[240:241], s[68:69], 0, v[144:145]
	s_add_i32 m0, s70, 0x2000
	s_nop 0
	global_load_lds_dwordx4 v[240:241], off
	s_waitcnt vmcnt(6)
	s_waitcnt lgkmcnt(0)
	s_barrier
	s_setprio 1
	s_waitcnt lgkmcnt(0)
	v_mfma_f32_16x16x32_bf16 v[94:97], v[184:187], v[160:163], v[94:97]
	v_mfma_f32_16x16x32_bf16 v[90:93], v[192:195], v[160:163], v[90:93]
	v_mfma_f32_16x16x32_bf16 v[86:89], v[184:187], v[164:167], v[86:89]
	v_mfma_f32_16x16x32_bf16 v[82:85], v[192:195], v[164:167], v[82:85]
	v_mfma_f32_16x16x32_bf16 v[78:81], v[184:187], v[224:227], v[78:81]
	v_mfma_f32_16x16x32_bf16 v[74:77], v[192:195], v[224:227], v[74:77]
	v_mfma_f32_16x16x32_bf16 v[70:73], v[184:187], v[228:231], v[70:73]
	v_mfma_f32_16x16x32_bf16 v[66:69], v[192:195], v[228:231], v[66:69]
	v_mfma_f32_16x16x32_bf16 v[94:97], v[188:191], v[216:219], v[94:97]
	v_mfma_f32_16x16x32_bf16 v[90:93], v[196:199], v[216:219], v[90:93]
	v_mfma_f32_16x16x32_bf16 v[86:89], v[188:191], v[220:223], v[86:89]
	v_mfma_f32_16x16x32_bf16 v[82:85], v[196:199], v[220:223], v[82:85]
	v_mfma_f32_16x16x32_bf16 v[78:81], v[188:191], v[232:235], v[78:81]
	v_mfma_f32_16x16x32_bf16 v[74:77], v[196:199], v[232:235], v[74:77]
	v_mfma_f32_16x16x32_bf16 v[70:73], v[188:191], v[236:239], v[70:73]
	v_mfma_f32_16x16x32_bf16 v[66:69], v[196:199], v[236:239], v[66:69]
	s_setprio 0
	s_setprio 1
	v_mfma_f32_16x16x32_bf16 v[30:33], v[200:203], v[160:163], v[30:33]
	v_mfma_f32_16x16x32_bf16 v[26:29], v[208:211], v[160:163], v[26:29]
	v_mfma_f32_16x16x32_bf16 v[22:25], v[200:203], v[164:167], v[22:25]
	v_mfma_f32_16x16x32_bf16 v[18:21], v[208:211], v[164:167], v[18:21]
	v_mfma_f32_16x16x32_bf16 v[14:17], v[200:203], v[224:227], v[14:17]
	v_mfma_f32_16x16x32_bf16 v[10:13], v[208:211], v[224:227], v[10:13]
	v_mfma_f32_16x16x32_bf16 v[6:9], v[200:203], v[228:231], v[6:9]
	v_mfma_f32_16x16x32_bf16 v[2:5], v[208:211], v[228:231], v[2:5]
	v_mfma_f32_16x16x32_bf16 v[30:33], v[204:207], v[216:219], v[30:33]
	v_mfma_f32_16x16x32_bf16 v[26:29], v[212:215], v[216:219], v[26:29]
	v_mfma_f32_16x16x32_bf16 v[22:25], v[204:207], v[220:223], v[22:25]
	v_mfma_f32_16x16x32_bf16 v[18:21], v[212:215], v[220:223], v[18:21]
	v_mfma_f32_16x16x32_bf16 v[14:17], v[204:207], v[232:235], v[14:17]
	v_mfma_f32_16x16x32_bf16 v[10:13], v[212:215], v[232:235], v[10:13]
	v_mfma_f32_16x16x32_bf16 v[6:9], v[204:207], v[236:239], v[6:9]
	v_mfma_f32_16x16x32_bf16 v[2:5], v[212:215], v[236:239], v[2:5]
	s_setprio 0
	s_barrier
	s_add_i32 s72, s72, 2
	s_add_u32 s66, s66, 0x100
	s_addc_u32 s67, s67, 0
	s_cmp_gt_u32 s72, 29
	s_cbranch_scc1 .LBB0_105

.LBB0_125:
	s_andn2_b64 vcc, exec, s[0:1]
	s_mov_b64 s[0:1], -1
	s_cbranch_vccnz .LBB0_97
	s_andn2_b64 vcc, exec, s[12:13]
	s_cbranch_vccnz .LBB0_96
	s_branch .LBB0_96

.LBB0_372:
	s_cmpk_lt_i32 s69, 0x200
	v_readfirstlane_b32 s1, v0
	s_cbranch_scc0 .LBB0_395
	v_lshrrev_b32_e32 v1, 5, v0
	s_lshr_b32 s12, s1, 6
	v_lshrrev_b32_e32 v2, 4, v0
	v_and_b32_e32 v5, 4, v1
	v_lshrrev_b32_e32 v1, 3, v0
	s_lshr_b32 s13, s1, 8
	s_lshl_b32 s33, s12, 10
	v_and_b32_e32 v3, 7, v0
	v_and_b32_e32 v4, 4, v2
	v_and_b32_e32 v6, 2, v1
	v_lshrrev_b32_e32 v8, 2, v0
	s_add_u32 s6, s2, 0x63000000
	v_bitop3_b32 v6, v6, v3, v4 bitop3:0x36
	v_and_b32_e32 v7, 35, v1
	v_and_b32_e32 v8, 24, v8
	s_addc_u32 s7, s3, 0
	v_or3_b32 v7, v7, v8, v5
	v_lshlrev_b32_e32 v168, 4, v6
	s_add_u32 s36, s2, 0x1e00000
	v_lshl_or_b32 v146, v7, 12, v168
	v_bitop3_b32 v7, v1, 2, 64 bitop3:0xc8
	s_movk_i32 s0, 0x63
	s_addc_u32 s37, s3, 0
	s_ashr_i32 s38, s69, 31
	v_bitop3_b32 v3, v7, v3, v4 bitop3:0x36
	v_bitop3_b32 v4, v1, s0, 64 bitop3:0xc8
	s_lshr_b32 s0, s38, 29
	s_add_i32 s0, s69, s0
	s_and_b32 s8, s0, -8
	s_sub_i32 s8, s69, s8
	s_lshl_b32 s10, s8, 6
	s_ashr_i32 s0, s0, 3
	s_mul_i32 s9, s8, 0x41
	s_cmp_lt_i32 s8, 0
	s_cselect_b32 s8, s9, s10
	s_add_i32 s0, s8, s0
	s_ashr_i32 s8, s0, 31
	s_lshr_b32 s8, s8, 26
	s_add_i32 s8, s0, s8
	s_ashr_i32 s9, s8, 6
	s_andn2_b32 s8, s8, 63
	s_sub_i32 s8, s0, s8
	s_bfe_i32 s0, s8, 0x80000
	s_bfe_u32 s0, s0, 0x3000c
	s_add_i32 s10, s8, s0
	s_bfe_i32 s0, s10, 0x80000
	s_and_b32 s10, s10, 0xf8
	s_sext_i32_i16 s0, s0
	s_sub_i32 s8, s8, s10
	s_lshl_b32 s9, s9, 3
	s_lshr_b32 s0, s0, 3
	s_sext_i32_i8 s8, s8
	v_or_b32_e32 v169, 64, v1
	s_add_i32 s73, s9, s8
	s_bfe_i64 s[8:9], s[0:1], 0x100000
	v_or3_b32 v4, v4, v8, v5
	v_lshlrev_b32_e32 v170, 4, v3
	v_lshlrev_b32_e32 v5, 11, v169
	s_lshl_b64 s[8:9], s[8:9], 20
	v_lshl_or_b32 v148, v4, 12, v170
	v_lshlrev_b32_e32 v4, 11, v1
	v_lshl_or_b32 v172, v3, 3, v5
	s_add_u32 s28, s36, s8
	v_mov_b32_e32 v3, 0x7f7f7f7f
	v_lshl_or_b32 v171, v6, 3, v4
	s_addc_u32 s29, s37, s9
	s_lshl_b32 s8, s73, 19
	s_lshl_b32 s9, s73, 8
	s_add_i32 s39, s33, 0
	v_or_b32_e32 v3, s8, v171
	s_bitset1_b32 s9, 7
	s_add_i32 m0, s39, 0x10000
	v_lshlrev_b32_e32 v150, 1, v3
	v_or_b32_e32 v3, s9, v1
	global_load_lds_dwordx4 v146, s[28:29]
	s_add_i32 m0, s39, 0x12000
	v_lshl_or_b32 v132, v3, 12, v168
	v_or_b32_e32 v3, s8, v172
	s_add_u32 s8, s28, 0x80000
	v_lshlrev_b32_e32 v130, 1, v3
	v_or_b32_e32 v3, s9, v169
	global_load_lds_dwordx4 v148, s[28:29]
	s_addc_u32 s9, s29, 0
	s_add_i32 m0, s39, 0x14000
	s_add_i32 s40, s39, 0x2000
	global_load_lds_dwordx4 v146, s[8:9]
	s_add_i32 m0, s39, 0x16000
	v_mov_b32_e32 v151, 0
	global_load_lds_dwordx4 v148, s[8:9]
	s_mov_b32 m0, s39
	s_add_i32 s41, s39, 0x4000
	global_load_lds_dwordx4 v150, s[6:7]
	s_mov_b32 m0, s40
	v_mov_b32_e32 v147, v151
	global_load_lds_dwordx4 v130, s[6:7]
	s_mov_b32 m0, s41
	s_add_i32 s42, s39, 0x6000
	v_lshl_or_b32 v134, v3, 12, v170
	v_lshl_add_u64 v[4:5], s[28:29], 0, v[146:147]
	global_load_lds_dwordx4 v132, s[6:7]
	s_mov_b32 m0, s42
	s_mov_b64 s[8:9], 0x80
	v_mov_b32_e32 v149, v151
	global_load_lds_dwordx4 v134, s[6:7]
	s_add_i32 m0, s39, 0x18000
	v_lshl_add_u64 v[4:5], v[4:5], 0, s[8:9]
	v_lshl_add_u64 v[6:7], s[28:29], 0, v[148:149]
	global_load_lds_dwordx4 v[4:5], off
	s_add_i32 m0, s39, 0x1a000
	v_lshl_add_u64 v[4:5], v[6:7], 0, s[8:9]
	s_add_u32 s10, s28, 0x80080
	global_load_lds_dwordx4 v[4:5], off
	s_addc_u32 s11, s29, 0
	s_add_i32 m0, s39, 0x1c000
	s_mov_b32 s43, 0
	global_load_lds_dwordx4 v146, s[10:11]
	s_add_i32 m0, s39, 0x1e000
	s_cmp_eq_u32 s13, 1
	global_load_lds_dwordx4 v148, s[10:11]
	s_waitcnt vmcnt(6)
	s_cselect_b64 s[10:11], -1, 0
	s_cmp_lg_u32 s13, 1
	s_barrier
	s_cbranch_scc1 .LBB0_375
.LBB0_375:
	s_sext_i32_i8 s74, s0
	s_lshl_b32 s0, s12, 5
	v_lshrrev_b32_e32 v5, 1, v0
	s_ashr_i32 s44, s94, 31
	s_and_b32 s0, s0, 0x60
	v_and_b32_e32 v3, 15, v0
	v_and_b32_e32 v2, 3, v2
	v_and_b32_e32 v4, 2, v0
	v_and_b32_e32 v5, 4, v5
	s_add_u32 s12, s2, 0x36800000
	v_bitop3_b32 v4, v5, v2, v4 bitop3:0x36
	v_lshl_or_b32 v173, s13, 6, v3
	s_addc_u32 s13, s3, 0
	v_lshlrev_b32_e32 v4, 4, v4
	v_lshlrev_b32_e32 v5, 7, v173
	v_or_b32_e32 v3, s0, v3
	s_cmpk_lt_u32 s1, 0x100
	v_or_b32_e32 v6, v5, v4
	v_lshlrev_b32_e32 v3, 7, v3
	v_bitop3_b32 v5, v5, 64, v4 bitop3:0x36
	s_cselect_b64 s[14:15], -1, 0
	s_add_u32 s16, s2, 0x63000080
	v_or_b32_e32 v174, v3, v4
	v_bitop3_b32 v175, v3, 64, v4 bitop3:0x36
	v_lshl_or_b32 v176, v2, 3, s0
	s_addc_u32 s17, s3, 0
	v_mov_b64_e32 v[152:153], 0x1ff
	s_add_i32 s45, 0, 0x10000
	s_add_i32 s46, 0, 0x10800
	s_add_i32 s47, 0, 0x14000
	s_add_i32 s64, 0, 0x14800
	v_add_u32_e32 v177, 0, v6
	v_add_u32_e32 v178, 0, v5
	s_add_i32 s65, 0, 0x18000
	s_add_i32 s66, 0, 0x18800
	s_add_i32 s67, 0, 0x1c000
	s_add_i32 s68, 0, 0x1c800
	s_mov_b64 s[18:19], 0x90000
	s_mov_b32 s69, 0x90000
	s_mov_b64 s[20:21], 0xa0000
	s_mov_b32 s70, 0xa0000
	s_mov_b64 s[22:23], 0xb0000
	s_mov_b32 s71, 0xb0000
	s_mov_b64 s[26:27], s[28:29]
	s_branch .LBB0_378

.LBB0_384:
	s_lshl_b32 s25, s72, 19
	s_lshl_b32 s30, s72, 8
	v_or_b32_e32 v2, s25, v171
	s_bitset1_b32 s30, 7
	v_lshlrev_b32_e32 v136, 1, v2
	v_or_b32_e32 v2, s30, v1
	v_lshl_or_b32 v138, v2, 12, v168
	v_or_b32_e32 v2, s25, v172
	v_lshlrev_b32_e32 v140, 1, v2
	v_or_b32_e32 v2, s30, v169
	v_lshl_or_b32 v142, v2, 12, v170
	v_mov_b32_e32 v131, v151
	v_mov_b32_e32 v133, v151
	v_mov_b32_e32 v135, v151
	s_add_u32 s25, s28, 0x100
	v_mov_b32_e32 v2, 0
	v_mov_b32_e32 v137, v151
	v_mov_b32_e32 v141, v151
	v_mov_b32_e32 v139, v151
	v_mov_b32_e32 v143, v151
	v_lshl_add_u64 v[144:145], s[16:17], 0, v[134:135]
	v_lshl_add_u64 v[154:155], s[16:17], 0, v[132:133]
	v_lshl_add_u64 v[156:157], s[16:17], 0, v[130:131]
	v_lshl_add_u64 v[158:159], s[16:17], 0, v[150:151]
	s_addc_u32 s75, s29, 0
	s_mov_b32 s76, -2
	s_mov_b64 s[28:29], 0
	v_mov_b32_e32 v3, v2
	v_mov_b32_e32 v4, v2
	v_mov_b32_e32 v5, v2
	v_mov_b32_e32 v6, v2
	v_mov_b32_e32 v7, v2
	v_mov_b32_e32 v8, v2
	v_mov_b32_e32 v9, v2
	v_mov_b32_e32 v14, v2
	v_mov_b32_e32 v15, v2
	v_mov_b32_e32 v16, v2
	v_mov_b32_e32 v17, v2
	v_mov_b32_e32 v22, v2
	v_mov_b32_e32 v23, v2
	v_mov_b32_e32 v24, v2
	v_mov_b32_e32 v25, v2
	v_mov_b32_e32 v30, v2
	v_mov_b32_e32 v31, v2
	v_mov_b32_e32 v32, v2
	v_mov_b32_e32 v33, v2
	v_mov_b32_e32 v38, v2
	v_mov_b32_e32 v39, v2
	v_mov_b32_e32 v40, v2
	v_mov_b32_e32 v41, v2
	v_mov_b32_e32 v46, v2
	v_mov_b32_e32 v47, v2
	v_mov_b32_e32 v48, v2
	v_mov_b32_e32 v49, v2
	v_mov_b32_e32 v54, v2
	v_mov_b32_e32 v55, v2
	v_mov_b32_e32 v56, v2
	v_mov_b32_e32 v57, v2
	v_mov_b32_e32 v10, v2
	v_mov_b32_e32 v11, v2
	v_mov_b32_e32 v12, v2
	v_mov_b32_e32 v13, v2
	v_mov_b32_e32 v18, v2
	v_mov_b32_e32 v19, v2
	v_mov_b32_e32 v20, v2
	v_mov_b32_e32 v21, v2
	v_mov_b32_e32 v26, v2
	v_mov_b32_e32 v27, v2
	v_mov_b32_e32 v28, v2
	v_mov_b32_e32 v29, v2
	v_mov_b32_e32 v34, v2
	v_mov_b32_e32 v35, v2
	v_mov_b32_e32 v36, v2
	v_mov_b32_e32 v37, v2
	v_mov_b32_e32 v42, v2
	v_mov_b32_e32 v43, v2
	v_mov_b32_e32 v44, v2
	v_mov_b32_e32 v45, v2
	v_mov_b32_e32 v50, v2
	v_mov_b32_e32 v51, v2
	v_mov_b32_e32 v52, v2
	v_mov_b32_e32 v53, v2
	v_mov_b32_e32 v58, v2
	v_mov_b32_e32 v59, v2
	v_mov_b32_e32 v60, v2
	v_mov_b32_e32 v61, v2
	v_mov_b32_e32 v62, v2
	v_mov_b32_e32 v63, v2
	v_mov_b32_e32 v64, v2
	v_mov_b32_e32 v65, v2
	v_mov_b32_e32 v66, v2
	v_mov_b32_e32 v67, v2
	v_mov_b32_e32 v68, v2
	v_mov_b32_e32 v69, v2
	v_mov_b32_e32 v70, v2
	v_mov_b32_e32 v71, v2
	v_mov_b32_e32 v72, v2
	v_mov_b32_e32 v73, v2
	v_mov_b32_e32 v74, v2
	v_mov_b32_e32 v75, v2
	v_mov_b32_e32 v76, v2
	v_mov_b32_e32 v77, v2
	v_mov_b32_e32 v78, v2
	v_mov_b32_e32 v79, v2
	v_mov_b32_e32 v80, v2
	v_mov_b32_e32 v81, v2
	v_mov_b32_e32 v82, v2
	v_mov_b32_e32 v83, v2
	v_mov_b32_e32 v84, v2
	v_mov_b32_e32 v85, v2
	v_mov_b32_e32 v90, v2
	v_mov_b32_e32 v91, v2
	v_mov_b32_e32 v92, v2
	v_mov_b32_e32 v93, v2
	v_mov_b32_e32 v98, v2
	v_mov_b32_e32 v99, v2
	v_mov_b32_e32 v100, v2
	v_mov_b32_e32 v101, v2
	v_mov_b32_e32 v106, v2
	v_mov_b32_e32 v107, v2
	v_mov_b32_e32 v108, v2
	v_mov_b32_e32 v109, v2
	v_mov_b32_e32 v86, v2
	v_mov_b32_e32 v87, v2
	v_mov_b32_e32 v88, v2
	v_mov_b32_e32 v89, v2
	v_mov_b32_e32 v94, v2
	v_mov_b32_e32 v95, v2
	v_mov_b32_e32 v96, v2
	v_mov_b32_e32 v97, v2
	v_mov_b32_e32 v102, v2
	v_mov_b32_e32 v103, v2
	v_mov_b32_e32 v104, v2
	v_mov_b32_e32 v105, v2
	v_mov_b32_e32 v110, v2
	v_mov_b32_e32 v111, v2
	v_mov_b32_e32 v112, v2
	v_mov_b32_e32 v113, v2
	v_mov_b32_e32 v114, v2
	v_mov_b32_e32 v115, v2
	v_mov_b32_e32 v116, v2
	v_mov_b32_e32 v117, v2
	v_mov_b32_e32 v118, v2
	v_mov_b32_e32 v119, v2
	v_mov_b32_e32 v120, v2
	v_mov_b32_e32 v121, v2
	v_mov_b32_e32 v122, v2
	v_mov_b32_e32 v123, v2
	v_mov_b32_e32 v124, v2
	v_mov_b32_e32 v125, v2
	v_mov_b32_e32 v126, v2
	v_mov_b32_e32 v127, v2
	v_mov_b32_e32 v128, v2
	v_mov_b32_e32 v129, v2
	s_andn2_b64 vcc, exec, s[10:11]
	s_cbranch_vccnz .Lp3_entry
	s_barrier
.Lp3_entry:
	s_branch .LBB0_386
.LBB0_385:
	v_add_u32_e32 v183, s45, v174
	v_add_u32_e32 v188, s45, v175
	s_add_u32 s34, s2, s28
	ds_read_b128 v[184:187], v183
	ds_read_b128 v[188:191], v188
	v_add_u32_e32 v183, s46, v174
	v_add_u32_e32 v196, s46, v175
	s_addc_u32 s35, s3, s29
	ds_read_b128 v[192:195], v183
	ds_read_b128 v[196:199], v196
	v_add_u32_e32 v183, s47, v174
	v_add_u32_e32 v204, s47, v175
	s_add_u32 s77, s34, 0x63000100
	ds_read_b128 v[200:203], v183
	ds_read_b128 v[204:207], v204
	v_add_u32_e32 v183, s64, v174
	v_add_u32_e32 v212, s64, v175
	s_addc_u32 s78, s35, 0
	ds_read_b128 v[208:211], v183
	ds_read_b128 v[212:215], v212
	s_and_b64 s[34:35], s[30:31], exec
	s_cselect_b32 s35, s7, s78
	s_cselect_b32 s34, s6, s77
	s_add_u32 s77, s25, s28
	s_addc_u32 s78, s75, s29
	s_and_b64 s[30:31], s[30:31], exec
	s_cselect_b32 s31, s27, s78
	s_cselect_b32 s30, s26, s77
	v_lshl_add_u64 v[248:249], v[158:159], 0, s[28:29]
	s_add_i32 m0, s39, 0x8000
	ds_read_b128 v[216:219], v177
	ds_read_b128 v[220:223], v177 offset:2048
	ds_read_b128 v[224:227], v178
	ds_read_b128 v[228:231], v178 offset:2048
	ds_read_b128 v[232:235], v177 offset:4096
	ds_read_b128 v[236:239], v177 offset:6144
	ds_read_b128 v[240:243], v178 offset:4096
	ds_read_b128 v[244:247], v178 offset:6144
	global_load_lds_dwordx4 v[248:249], off
	v_lshl_add_u64 v[248:249], v[156:157], 0, s[28:29]
	s_add_i32 m0, s39, 0xa000
	s_nop 0
	global_load_lds_dwordx4 v[248:249], off
	v_lshl_add_u64 v[248:249], v[154:155], 0, s[28:29]
	s_add_i32 m0, s39, 0xc000
	s_nop 0
	global_load_lds_dwordx4 v[248:249], off
	v_lshl_add_u64 v[248:249], v[144:145], 0, s[28:29]
	s_add_i32 m0, s39, 0xe000
	s_nop 0
	global_load_lds_dwordx4 v[248:249], off
	s_waitcnt vmcnt(8)
	s_waitcnt lgkmcnt(0)
	s_barrier
	s_setprio 1
	s_waitcnt lgkmcnt(0)
	v_mfma_f32_16x16x32_bf16 v[126:129], v[184:187], v[216:219], v[126:129]
	v_mfma_f32_16x16x32_bf16 v[122:125], v[192:195], v[216:219], v[122:125]
	v_mfma_f32_16x16x32_bf16 v[118:121], v[184:187], v[220:223], v[118:121]
	v_mfma_f32_16x16x32_bf16 v[114:117], v[192:195], v[220:223], v[114:117]
	v_mfma_f32_16x16x32_bf16 v[110:113], v[184:187], v[232:235], v[110:113]
	v_mfma_f32_16x16x32_bf16 v[102:105], v[192:195], v[232:235], v[102:105]
	v_mfma_f32_16x16x32_bf16 v[94:97], v[184:187], v[236:239], v[94:97]
	v_mfma_f32_16x16x32_bf16 v[86:89], v[192:195], v[236:239], v[86:89]
	v_mfma_f32_16x16x32_bf16 v[126:129], v[188:191], v[224:227], v[126:129]
	v_mfma_f32_16x16x32_bf16 v[122:125], v[196:199], v[224:227], v[122:125]
	v_mfma_f32_16x16x32_bf16 v[118:121], v[188:191], v[228:231], v[118:121]
	v_mfma_f32_16x16x32_bf16 v[114:117], v[196:199], v[228:231], v[114:117]
	v_mfma_f32_16x16x32_bf16 v[110:113], v[188:191], v[240:243], v[110:113]
	v_mfma_f32_16x16x32_bf16 v[102:105], v[196:199], v[240:243], v[102:105]
	v_mfma_f32_16x16x32_bf16 v[94:97], v[188:191], v[244:247], v[94:97]
	v_mfma_f32_16x16x32_bf16 v[86:89], v[196:199], v[244:247], v[86:89]
	s_setprio 0
	s_setprio 1
	v_mfma_f32_16x16x32_bf16 v[106:109], v[200:203], v[216:219], v[106:109]
	v_mfma_f32_16x16x32_bf16 v[98:101], v[208:211], v[216:219], v[98:101]
	v_mfma_f32_16x16x32_bf16 v[90:93], v[200:203], v[220:223], v[90:93]
	v_mfma_f32_16x16x32_bf16 v[82:85], v[208:211], v[220:223], v[82:85]
	v_mfma_f32_16x16x32_bf16 v[78:81], v[200:203], v[232:235], v[78:81]
	v_mfma_f32_16x16x32_bf16 v[74:77], v[208:211], v[232:235], v[74:77]
	v_mfma_f32_16x16x32_bf16 v[70:73], v[200:203], v[236:239], v[70:73]
	v_mfma_f32_16x16x32_bf16 v[66:69], v[208:211], v[236:239], v[66:69]
	v_mfma_f32_16x16x32_bf16 v[106:109], v[204:207], v[224:227], v[106:109]
	v_mfma_f32_16x16x32_bf16 v[98:101], v[212:215], v[224:227], v[98:101]
	v_mfma_f32_16x16x32_bf16 v[90:93], v[204:207], v[228:231], v[90:93]
	v_mfma_f32_16x16x32_bf16 v[82:85], v[212:215], v[228:231], v[82:85]
	v_mfma_f32_16x16x32_bf16 v[78:81], v[204:207], v[240:243], v[78:81]
	v_mfma_f32_16x16x32_bf16 v[74:77], v[212:215], v[240:243], v[74:77]
	v_mfma_f32_16x16x32_bf16 v[70:73], v[204:207], v[244:247], v[70:73]
	v_mfma_f32_16x16x32_bf16 v[66:69], v[212:215], v[244:247], v[66:69]
	s_setprio 0
	s_barrier
	s_add_i32 s77, s45, s33
	v_lshl_add_u64 v[248:249], s[30:31], 0, v[146:147]
	s_mov_b32 m0, s77
	ds_read_b128 v[216:219], v177 offset:16384
	ds_read_b128 v[220:223], v177 offset:18432
	ds_read_b128 v[224:227], v178 offset:16384
	ds_read_b128 v[228:231], v178 offset:18432
	ds_read_b128 v[232:235], v177 offset:20480
	ds_read_b128 v[236:239], v177 offset:22528
	ds_read_b128 v[240:243], v178 offset:20480
	ds_read_b128 v[244:247], v178 offset:22528
	global_load_lds_dwordx4 v[248:249], off
	s_add_i32 m0, s77, 0x2000
	s_add_u32 s78, s30, 0x80000
	v_lshl_add_u64 v[250:251], s[30:31], 0, v[148:149]
	s_addc_u32 s79, s31, 0
	s_add_i32 s77, s47, s33
	global_load_lds_dwordx4 v[250:251], off
	v_lshl_add_u64 v[252:253], s[78:79], 0, v[146:147]
	s_mov_b32 m0, s77
	s_nop 0
	global_load_lds_dwordx4 v[252:253], off
	v_lshl_add_u64 v[252:253], s[78:79], 0, v[148:149]
	s_add_i32 m0, s77, 0x2000
	s_nop 0
	global_load_lds_dwordx4 v[252:253], off
	s_waitcnt vmcnt(6)
	s_waitcnt lgkmcnt(0)
	s_barrier
	s_setprio 1
	s_waitcnt lgkmcnt(0)
	v_mfma_f32_16x16x32_bf16 v[62:65], v[184:187], v[216:219], v[62:65]
	v_mfma_f32_16x16x32_bf16 v[58:61], v[192:195], v[216:219], v[58:61]
	v_mfma_f32_16x16x32_bf16 v[50:53], v[184:187], v[220:223], v[50:53]
	v_mfma_f32_16x16x32_bf16 v[42:45], v[192:195], v[220:223], v[42:45]
	v_mfma_f32_16x16x32_bf16 v[34:37], v[184:187], v[232:235], v[34:37]
	v_mfma_f32_16x16x32_bf16 v[26:29], v[192:195], v[232:235], v[26:29]
	v_mfma_f32_16x16x32_bf16 v[18:21], v[184:187], v[236:239], v[18:21]
	v_mfma_f32_16x16x32_bf16 v[10:13], v[192:195], v[236:239], v[10:13]
	v_mfma_f32_16x16x32_bf16 v[62:65], v[188:191], v[224:227], v[62:65]
	v_mfma_f32_16x16x32_bf16 v[58:61], v[196:199], v[224:227], v[58:61]
	v_mfma_f32_16x16x32_bf16 v[50:53], v[188:191], v[228:231], v[50:53]
	v_mfma_f32_16x16x32_bf16 v[42:45], v[196:199], v[228:231], v[42:45]
	v_mfma_f32_16x16x32_bf16 v[34:37], v[188:191], v[240:243], v[34:37]
	v_mfma_f32_16x16x32_bf16 v[26:29], v[196:199], v[240:243], v[26:29]
	v_mfma_f32_16x16x32_bf16 v[18:21], v[188:191], v[244:247], v[18:21]
	v_mfma_f32_16x16x32_bf16 v[10:13], v[196:199], v[244:247], v[10:13]
	s_setprio 0
	s_setprio 1
	v_mfma_f32_16x16x32_bf16 v[54:57], v[200:203], v[216:219], v[54:57]
	v_mfma_f32_16x16x32_bf16 v[46:49], v[208:211], v[216:219], v[46:49]
	v_mfma_f32_16x16x32_bf16 v[38:41], v[200:203], v[220:223], v[38:41]
	v_mfma_f32_16x16x32_bf16 v[30:33], v[208:211], v[220:223], v[30:33]
	v_mfma_f32_16x16x32_bf16 v[22:25], v[200:203], v[232:235], v[22:25]
	v_mfma_f32_16x16x32_bf16 v[14:17], v[208:211], v[232:235], v[14:17]
	v_mfma_f32_16x16x32_bf16 v[6:9], v[200:203], v[236:239], v[6:9]
	v_mfma_f32_16x16x32_bf16 v[2:5], v[208:211], v[236:239], v[2:5]
	v_mfma_f32_16x16x32_bf16 v[54:57], v[204:207], v[224:227], v[54:57]
	v_mfma_f32_16x16x32_bf16 v[46:49], v[212:215], v[224:227], v[46:49]
	v_mfma_f32_16x16x32_bf16 v[38:41], v[204:207], v[228:231], v[38:41]
	v_mfma_f32_16x16x32_bf16 v[30:33], v[212:215], v[228:231], v[30:33]
	v_mfma_f32_16x16x32_bf16 v[22:25], v[204:207], v[240:243], v[22:25]
	v_mfma_f32_16x16x32_bf16 v[14:17], v[212:215], v[240:243], v[14:17]
	v_mfma_f32_16x16x32_bf16 v[6:9], v[204:207], v[244:247], v[6:9]
	v_mfma_f32_16x16x32_bf16 v[2:5], v[212:215], v[244:247], v[2:5]
	s_setprio 0
	s_barrier
	v_add_u32_e32 v183, s65, v174
	v_add_u32_e32 v188, s65, v175
	ds_read_b128 v[184:187], v183
	ds_read_b128 v[188:191], v188
	v_add_u32_e32 v183, s66, v174
	v_add_u32_e32 v196, s66, v175
	ds_read_b128 v[192:195], v183
	ds_read_b128 v[196:199], v196
	v_add_u32_e32 v183, s67, v174
	v_add_u32_e32 v204, s67, v175
	ds_read_b128 v[200:203], v183
	ds_read_b128 v[204:207], v204
	v_add_u32_e32 v183, s68, v174
	v_add_u32_e32 v212, s68, v175
	ds_read_b128 v[208:211], v183
	ds_read_b128 v[212:215], v212
	s_mov_b32 m0, s39
	v_lshl_add_u64 v[166:167], s[34:35], 0, v[166:167]
	ds_read_b128 v[216:219], v177 offset:32768
	ds_read_b128 v[220:223], v177 offset:34816
	ds_read_b128 v[224:227], v178 offset:32768
	ds_read_b128 v[228:231], v178 offset:34816
	ds_read_b128 v[232:235], v177 offset:36864
	ds_read_b128 v[236:239], v177 offset:38912
	ds_read_b128 v[240:243], v178 offset:36864
	ds_read_b128 v[244:247], v178 offset:38912
	global_load_lds_dwordx4 v[166:167], off
	v_lshl_add_u64 v[164:165], s[34:35], 0, v[164:165]
	s_mov_b32 m0, s40
	v_lshl_add_u64 v[162:163], s[34:35], 0, v[162:163]
	global_load_lds_dwordx4 v[164:165], off
	s_mov_b32 m0, s41
	v_lshl_add_u64 v[160:161], s[34:35], 0, v[160:161]
	global_load_lds_dwordx4 v[162:163], off
	s_mov_b32 m0, s42
	s_nop 0
	global_load_lds_dwordx4 v[160:161], off
	s_waitcnt vmcnt(8)
	s_waitcnt lgkmcnt(0)
	s_barrier
	s_setprio 1
	s_waitcnt lgkmcnt(0)
	v_mfma_f32_16x16x32_bf16 v[126:129], v[184:187], v[216:219], v[126:129]
	v_mfma_f32_16x16x32_bf16 v[122:125], v[192:195], v[216:219], v[122:125]
	v_mfma_f32_16x16x32_bf16 v[118:121], v[184:187], v[220:223], v[118:121]
	v_mfma_f32_16x16x32_bf16 v[114:117], v[192:195], v[220:223], v[114:117]
	v_mfma_f32_16x16x32_bf16 v[110:113], v[184:187], v[232:235], v[110:113]
	v_mfma_f32_16x16x32_bf16 v[102:105], v[192:195], v[232:235], v[102:105]
	v_mfma_f32_16x16x32_bf16 v[94:97], v[184:187], v[236:239], v[94:97]
	v_mfma_f32_16x16x32_bf16 v[86:89], v[192:195], v[236:239], v[86:89]
	v_mfma_f32_16x16x32_bf16 v[126:129], v[188:191], v[224:227], v[126:129]
	v_mfma_f32_16x16x32_bf16 v[122:125], v[196:199], v[224:227], v[122:125]
	v_mfma_f32_16x16x32_bf16 v[118:121], v[188:191], v[228:231], v[118:121]
	v_mfma_f32_16x16x32_bf16 v[114:117], v[196:199], v[228:231], v[114:117]
	v_mfma_f32_16x16x32_bf16 v[110:113], v[188:191], v[240:243], v[110:113]
	v_mfma_f32_16x16x32_bf16 v[102:105], v[196:199], v[240:243], v[102:105]
	v_mfma_f32_16x16x32_bf16 v[94:97], v[188:191], v[244:247], v[94:97]
	v_mfma_f32_16x16x32_bf16 v[86:89], v[196:199], v[244:247], v[86:89]
	s_setprio 0
	s_setprio 1
	v_mfma_f32_16x16x32_bf16 v[106:109], v[200:203], v[216:219], v[106:109]
	v_mfma_f32_16x16x32_bf16 v[98:101], v[208:211], v[216:219], v[98:101]
	v_mfma_f32_16x16x32_bf16 v[90:93], v[200:203], v[220:223], v[90:93]
	v_mfma_f32_16x16x32_bf16 v[82:85], v[208:211], v[220:223], v[82:85]
	v_mfma_f32_16x16x32_bf16 v[78:81], v[200:203], v[232:235], v[78:81]
	v_mfma_f32_16x16x32_bf16 v[74:77], v[208:211], v[232:235], v[74:77]
	v_mfma_f32_16x16x32_bf16 v[70:73], v[200:203], v[236:239], v[70:73]
	v_mfma_f32_16x16x32_bf16 v[66:69], v[208:211], v[236:239], v[66:69]
	v_mfma_f32_16x16x32_bf16 v[106:109], v[204:207], v[224:227], v[106:109]
	v_mfma_f32_16x16x32_bf16 v[98:101], v[212:215], v[224:227], v[98:101]
	v_mfma_f32_16x16x32_bf16 v[90:93], v[204:207], v[228:231], v[90:93]
	v_mfma_f32_16x16x32_bf16 v[82:85], v[212:215], v[228:231], v[82:85]
	v_mfma_f32_16x16x32_bf16 v[78:81], v[204:207], v[240:243], v[78:81]
	v_mfma_f32_16x16x32_bf16 v[74:77], v[212:215], v[240:243], v[74:77]
	v_mfma_f32_16x16x32_bf16 v[70:73], v[204:207], v[244:247], v[70:73]
	v_mfma_f32_16x16x32_bf16 v[66:69], v[212:215], v[244:247], v[66:69]
	s_setprio 0
	s_barrier
	s_add_i32 s34, s65, s33
	v_lshl_add_u64 v[240:241], v[248:249], 0, s[8:9]
	s_mov_b32 m0, s34
	ds_read_b128 v[160:163], v177 offset:49152
	ds_read_b128 v[164:167], v177 offset:51200
	ds_read_b128 v[216:219], v178 offset:49152
	ds_read_b128 v[220:223], v178 offset:51200
	ds_read_b128 v[224:227], v177 offset:53248
	ds_read_b128 v[228:231], v177 offset:55296
	ds_read_b128 v[232:235], v178 offset:53248
	ds_read_b128 v[236:239], v178 offset:55296
	global_load_lds_dwordx4 v[240:241], off
	s_add_i32 m0, s34, 0x2000
	s_add_u32 s30, s30, 0x80080
	v_lshl_add_u64 v[240:241], v[250:251], 0, s[8:9]
	s_addc_u32 s31, s31, 0
	s_add_i32 s34, s67, s33
	global_load_lds_dwordx4 v[240:241], off
	v_lshl_add_u64 v[240:241], s[30:31], 0, v[146:147]
	s_mov_b32 m0, s34
	s_nop 0
	global_load_lds_dwordx4 v[240:241], off
	v_lshl_add_u64 v[240:241], s[30:31], 0, v[148:149]
	s_add_i32 m0, s34, 0x2000
	s_nop 0
	global_load_lds_dwordx4 v[240:241], off
	s_waitcnt vmcnt(6)
	s_waitcnt lgkmcnt(0)
	s_barrier
	s_setprio 1
	s_waitcnt lgkmcnt(0)
	v_mfma_f32_16x16x32_bf16 v[62:65], v[184:187], v[160:163], v[62:65]
	v_mfma_f32_16x16x32_bf16 v[58:61], v[192:195], v[160:163], v[58:61]
	v_mfma_f32_16x16x32_bf16 v[50:53], v[184:187], v[164:167], v[50:53]
	v_mfma_f32_16x16x32_bf16 v[42:45], v[192:195], v[164:167], v[42:45]
	v_mfma_f32_16x16x32_bf16 v[34:37], v[184:187], v[224:227], v[34:37]
	v_mfma_f32_16x16x32_bf16 v[26:29], v[192:195], v[224:227], v[26:29]
	v_mfma_f32_16x16x32_bf16 v[18:21], v[184:187], v[228:231], v[18:21]
	v_mfma_f32_16x16x32_bf16 v[10:13], v[192:195], v[228:231], v[10:13]
	v_mfma_f32_16x16x32_bf16 v[62:65], v[188:191], v[216:219], v[62:65]
	v_mfma_f32_16x16x32_bf16 v[58:61], v[196:199], v[216:219], v[58:61]
	v_mfma_f32_16x16x32_bf16 v[50:53], v[188:191], v[220:223], v[50:53]
	v_mfma_f32_16x16x32_bf16 v[42:45], v[196:199], v[220:223], v[42:45]
	v_mfma_f32_16x16x32_bf16 v[34:37], v[188:191], v[232:235], v[34:37]
	v_mfma_f32_16x16x32_bf16 v[26:29], v[196:199], v[232:235], v[26:29]
	v_mfma_f32_16x16x32_bf16 v[18:21], v[188:191], v[236:239], v[18:21]
	v_mfma_f32_16x16x32_bf16 v[10:13], v[196:199], v[236:239], v[10:13]
	s_setprio 0
	s_setprio 1
	v_mfma_f32_16x16x32_bf16 v[54:57], v[200:203], v[160:163], v[54:57]
	v_mfma_f32_16x16x32_bf16 v[46:49], v[208:211], v[160:163], v[46:49]
	v_mfma_f32_16x16x32_bf16 v[38:41], v[200:203], v[164:167], v[38:41]
	v_mfma_f32_16x16x32_bf16 v[30:33], v[208:211], v[164:167], v[30:33]
	v_mfma_f32_16x16x32_bf16 v[22:25], v[200:203], v[224:227], v[22:25]
	v_mfma_f32_16x16x32_bf16 v[14:17], v[208:211], v[224:227], v[14:17]
	v_mfma_f32_16x16x32_bf16 v[6:9], v[200:203], v[228:231], v[6:9]
	v_mfma_f32_16x16x32_bf16 v[2:5], v[208:211], v[228:231], v[2:5]
	v_mfma_f32_16x16x32_bf16 v[54:57], v[204:207], v[216:219], v[54:57]
	v_mfma_f32_16x16x32_bf16 v[46:49], v[212:215], v[216:219], v[46:49]
	v_mfma_f32_16x16x32_bf16 v[38:41], v[204:207], v[220:223], v[38:41]
	v_mfma_f32_16x16x32_bf16 v[30:33], v[212:215], v[220:223], v[30:33]
	v_mfma_f32_16x16x32_bf16 v[22:25], v[204:207], v[232:235], v[22:25]
	v_mfma_f32_16x16x32_bf16 v[14:17], v[212:215], v[232:235], v[14:17]
	v_mfma_f32_16x16x32_bf16 v[6:9], v[204:207], v[236:239], v[6:9]
	v_mfma_f32_16x16x32_bf16 v[2:5], v[212:215], v[236:239], v[2:5]
	s_setprio 0
	s_barrier
	s_add_i32 s76, s76, 2
	s_add_u32 s28, s28, 0x100
	s_addc_u32 s29, s29, 0
	s_cmp_gt_u32 s76, 29
	s_cbranch_scc1 .LBB0_389

.LBB0_391:
	v_lshl_or_b32 v154, s74, 8, v176
	v_readlane_b32 s76, v254, 2
	v_ashrrev_i32_e32 v155, 31, v154
	v_readlane_b32 s80, v254, 6
	v_readlane_b32 s81, v254, 7
	v_lshl_add_u32 v156, s73, 8, v173
	v_ashrrev_i32_e32 v157, 31, v156
	v_lshl_add_u64 v[130:131], v[154:155], 2, s[80:81]
	global_load_dwordx4 v[142:145], v[130:131], off
	global_load_dwordx4 v[138:141], v[130:131], off offset:16
	global_load_dwordx4 v[134:137], v[130:131], off offset:512
	s_nop 0
	global_load_dwordx4 v[130:133], v[130:131], off offset:528
	v_or_b32_e32 v158, 16, v156
	v_or_b32_e32 v160, 32, v156
	v_or_b32_e32 v162, 48, v156
	v_lshlrev_b64 v[156:157], 12, v[156:157]
	v_ashrrev_i32_e32 v159, 31, v158
	v_ashrrev_i32_e32 v161, 31, v160
	v_ashrrev_i32_e32 v163, 31, v162
	v_lshlrev_b64 v[164:165], 1, v[154:155]
	v_lshl_add_u64 v[154:155], s[12:13], 0, v[156:157]
	v_lshlrev_b64 v[156:157], 12, v[158:159]
	v_lshlrev_b64 v[158:159], 12, v[160:161]
	v_lshlrev_b64 v[160:161], 12, v[162:163]
	v_lshl_add_u64 v[156:157], s[12:13], 0, v[156:157]
	v_lshl_add_u64 v[158:159], s[12:13], 0, v[158:159]
	v_lshl_add_u64 v[160:161], s[12:13], 0, v[160:161]
	v_lshl_add_u64 v[154:155], v[154:155], 0, v[164:165]
	v_lshl_add_u64 v[156:157], v[156:157], 0, v[164:165]
	v_lshl_add_u64 v[158:159], v[158:159], 0, v[164:165]
	v_lshl_add_u64 v[160:161], v[160:161], 0, v[164:165]
	s_mov_b32 s25, 0x80000
	s_mov_b64 s[28:29], 0x80000
	v_readlane_b32 s77, v254, 3
	v_readlane_b32 s78, v254, 4
	v_readlane_b32 s79, v254, 5
	v_readlane_b32 s82, v254, 8
	v_readlane_b32 s83, v254, 9
	v_readlane_b32 s84, v254, 10
	v_readlane_b32 s85, v254, 11
	v_readlane_b32 s86, v254, 12
	v_readlane_b32 s87, v254, 13
	v_readlane_b32 s88, v254, 14
	v_readlane_b32 s89, v254, 15
	v_readlane_b32 s90, v254, 16
	v_readlane_b32 s91, v254, 17
	s_waitcnt vmcnt(0)
	v_pk_add_f32 v[128:129], v[128:129], v[144:145]
	v_pk_add_f32 v[126:127], v[126:127], v[142:143]
	v_pk_add_f32 v[164:165], v[72:73], v[136:137]
	v_cvt_pk_bf16_f32 v72, v126, v127
	v_cvt_pk_bf16_f32 v73, v128, v129
	v_pk_add_f32 v[124:125], v[124:125], v[140:141]
	v_pk_add_f32 v[122:123], v[122:123], v[138:139]
	v_pk_add_f32 v[108:109], v[108:109], v[136:137]
	v_pk_add_f32 v[106:107], v[106:107], v[134:135]
	v_pk_add_f32 v[162:163], v[74:75], v[130:131]
	v_cvt_pk_bf16_f32 v74, v122, v123
	v_cvt_pk_bf16_f32 v75, v124, v125
	global_store_dwordx4 v[154:155], v[72:75], off
	v_pk_add_f32 v[100:101], v[100:101], v[132:133]
	v_pk_add_f32 v[98:99], v[98:99], v[130:131]
	v_cvt_pk_bf16_f32 v72, v106, v107
	v_cvt_pk_bf16_f32 v73, v108, v109
	v_pk_add_f32 v[120:121], v[120:121], v[144:145]
	v_pk_add_f32 v[118:119], v[118:119], v[142:143]
	v_cvt_pk_bf16_f32 v74, v98, v99
	v_cvt_pk_bf16_f32 v75, v100, v101
	global_store_dwordx4 v[154:155], v[72:75], off offset:256
	v_pk_add_f32 v[116:117], v[116:117], v[140:141]
	v_pk_add_f32 v[114:115], v[114:115], v[138:139]
	v_cvt_pk_bf16_f32 v72, v118, v119
	v_cvt_pk_bf16_f32 v73, v120, v121
	v_pk_add_f32 v[92:93], v[92:93], v[136:137]
	v_pk_add_f32 v[90:91], v[90:91], v[134:135]
	v_cvt_pk_bf16_f32 v74, v114, v115
	v_cvt_pk_bf16_f32 v75, v116, v117
	global_store_dwordx4 v[156:157], v[72:75], off
	v_pk_add_f32 v[84:85], v[84:85], v[132:133]
	v_pk_add_f32 v[82:83], v[82:83], v[130:131]
	v_cvt_pk_bf16_f32 v72, v90, v91
	v_cvt_pk_bf16_f32 v73, v92, v93
	v_pk_add_f32 v[112:113], v[112:113], v[144:145]
	v_pk_add_f32 v[110:111], v[110:111], v[142:143]
	v_cvt_pk_bf16_f32 v74, v82, v83
	v_cvt_pk_bf16_f32 v75, v84, v85
	global_store_dwordx4 v[156:157], v[72:75], off offset:256
	v_pk_add_f32 v[104:105], v[104:105], v[140:141]
	v_pk_add_f32 v[102:103], v[102:103], v[138:139]
	v_cvt_pk_bf16_f32 v72, v110, v111
	v_cvt_pk_bf16_f32 v73, v112, v113
	v_pk_add_f32 v[80:81], v[80:81], v[136:137]
	v_pk_add_f32 v[78:79], v[78:79], v[134:135]
	v_cvt_pk_bf16_f32 v74, v102, v103
	v_cvt_pk_bf16_f32 v75, v104, v105
	global_store_dwordx4 v[158:159], v[72:75], off
	v_pk_add_f32 v[76:77], v[76:77], v[132:133]
	v_pk_add_f32 v[96:97], v[96:97], v[144:145]
	v_cvt_pk_bf16_f32 v72, v78, v79
	v_cvt_pk_bf16_f32 v73, v80, v81
	v_pk_add_f32 v[94:95], v[94:95], v[142:143]
	v_cvt_pk_bf16_f32 v74, v162, v163
	v_cvt_pk_bf16_f32 v75, v76, v77
	global_store_dwordx4 v[158:159], v[72:75], off offset:256
	v_pk_add_f32 v[88:89], v[88:89], v[140:141]
	v_pk_add_f32 v[86:87], v[86:87], v[138:139]
	v_cvt_pk_bf16_f32 v72, v94, v95
	v_cvt_pk_bf16_f32 v73, v96, v97
	v_pk_add_f32 v[70:71], v[70:71], v[134:135]
	v_cvt_pk_bf16_f32 v74, v86, v87
	v_cvt_pk_bf16_f32 v75, v88, v89
	global_store_dwordx4 v[160:161], v[72:75], off
	v_pk_add_f32 v[64:65], v[64:65], v[144:145]
	v_pk_add_f32 v[62:63], v[62:63], v[142:143]
	v_pk_add_f32 v[72:73], v[68:69], v[132:133]
	v_pk_add_f32 v[68:69], v[66:67], v[130:131]
	v_cvt_pk_bf16_f32 v66, v70, v71
	v_cvt_pk_bf16_f32 v67, v164, v165
	v_pk_add_f32 v[56:57], v[56:57], v[136:137]
	v_cvt_pk_bf16_f32 v68, v68, v69
	v_cvt_pk_bf16_f32 v69, v72, v73
	global_store_dwordx4 v[160:161], v[66:69], off offset:256
	v_pk_add_f32 v[54:55], v[54:55], v[134:135]
	v_pk_add_f32 v[40:41], v[40:41], v[136:137]
	v_pk_add_f32 v[66:67], v[60:61], v[140:141]
	v_pk_add_f32 v[60:61], v[58:59], v[138:139]
	v_cvt_pk_bf16_f32 v58, v62, v63
	v_cvt_pk_bf16_f32 v59, v64, v65
	v_add_co_u32_e32 v64, vcc, s25, v154
	v_cvt_pk_bf16_f32 v60, v60, v61
	v_cvt_pk_bf16_f32 v61, v66, v67
	v_lshl_add_u64 v[62:63], v[154:155], 0, s[28:29]
	s_nop 0
	v_addc_co_u32_e32 v65, vcc, 0, v155, vcc
	global_store_dwordx4 v[64:65], v[58:61], off
	v_pk_add_f32 v[38:39], v[38:39], v[134:135]
	v_pk_add_f32 v[24:25], v[24:25], v[136:137]
	v_pk_add_f32 v[58:59], v[48:49], v[132:133]
	v_pk_add_f32 v[48:49], v[46:47], v[130:131]
	v_cvt_pk_bf16_f32 v46, v54, v55
	v_cvt_pk_bf16_f32 v47, v56, v57
	v_pk_add_f32 v[22:23], v[22:23], v[134:135]
	v_cvt_pk_bf16_f32 v48, v48, v49
	v_cvt_pk_bf16_f32 v49, v58, v59
	global_store_dwordx4 v[62:63], v[46:49], off offset:256
	v_pk_add_f32 v[8:9], v[8:9], v[136:137]
	v_pk_add_f32 v[6:7], v[6:7], v[134:135]
	v_pk_add_f32 v[48:49], v[50:51], v[142:143]
	v_pk_add_f32 v[50:51], v[44:45], v[140:141]
	v_pk_add_f32 v[44:45], v[42:43], v[138:139]
	v_cvt_pk_bf16_f32 v42, v48, v49
	v_add_co_u32_e32 v48, vcc, s69, v154
	v_pk_add_f32 v[46:47], v[52:53], v[144:145]
	s_nop 0
	v_addc_co_u32_e32 v49, vcc, 0, v155, vcc
	v_cvt_pk_bf16_f32 v43, v46, v47
	v_cvt_pk_bf16_f32 v44, v44, v45
	v_cvt_pk_bf16_f32 v45, v50, v51
	global_store_dwordx4 v[48:49], v[42:45], off
	v_lshl_add_u64 v[46:47], v[154:155], 0, s[18:19]
	s_nop 0
	v_pk_add_f32 v[42:43], v[32:33], v[132:133]
	v_pk_add_f32 v[32:33], v[30:31], v[130:131]
	v_cvt_pk_bf16_f32 v30, v38, v39
	v_cvt_pk_bf16_f32 v31, v40, v41
	s_nop 0
	v_cvt_pk_bf16_f32 v32, v32, v33
	v_cvt_pk_bf16_f32 v33, v42, v43
	global_store_dwordx4 v[46:47], v[30:33], off offset:256
	s_nop 1
	v_pk_add_f32 v[32:33], v[34:35], v[142:143]
	v_pk_add_f32 v[34:35], v[28:29], v[140:141]
	v_pk_add_f32 v[28:29], v[26:27], v[138:139]
	v_cvt_pk_bf16_f32 v26, v32, v33
	v_add_co_u32_e32 v32, vcc, s70, v154
	v_pk_add_f32 v[30:31], v[36:37], v[144:145]
	s_nop 0
	v_addc_co_u32_e32 v33, vcc, 0, v155, vcc
	v_cvt_pk_bf16_f32 v27, v30, v31
	v_cvt_pk_bf16_f32 v28, v28, v29
	v_cvt_pk_bf16_f32 v29, v34, v35
	global_store_dwordx4 v[32:33], v[26:29], off
	v_lshl_add_u64 v[30:31], v[154:155], 0, s[20:21]
	s_nop 0
	v_pk_add_f32 v[26:27], v[16:17], v[132:133]
	v_pk_add_f32 v[16:17], v[14:15], v[130:131]
	v_cvt_pk_bf16_f32 v14, v22, v23
	v_cvt_pk_bf16_f32 v15, v24, v25
	s_nop 0
	v_cvt_pk_bf16_f32 v16, v16, v17
	v_cvt_pk_bf16_f32 v17, v26, v27
	global_store_dwordx4 v[30:31], v[14:17], off offset:256
	s_nop 1
	v_pk_add_f32 v[16:17], v[18:19], v[142:143]
	v_pk_add_f32 v[18:19], v[12:13], v[140:141]
	v_pk_add_f32 v[12:13], v[10:11], v[138:139]
	v_cvt_pk_bf16_f32 v10, v16, v17
	v_add_co_u32_e32 v16, vcc, s71, v154
	v_pk_add_f32 v[14:15], v[20:21], v[144:145]
	s_nop 0
	v_addc_co_u32_e32 v17, vcc, 0, v155, vcc
	v_cvt_pk_bf16_f32 v11, v14, v15
	v_cvt_pk_bf16_f32 v12, v12, v13
	v_cvt_pk_bf16_f32 v13, v18, v19
	v_lshl_add_u64 v[14:15], v[154:155], 0, s[22:23]
	global_store_dwordx4 v[16:17], v[10:13], off
	s_andn2_b64 vcc, exec, s[0:1]
	s_mov_b64 s[0:1], -1
	v_pk_add_f32 v[10:11], v[4:5], v[132:133]
	v_pk_add_f32 v[4:5], v[2:3], v[130:131]
	v_cvt_pk_bf16_f32 v2, v6, v7
	v_cvt_pk_bf16_f32 v3, v8, v9
	s_nop 0
	v_cvt_pk_bf16_f32 v4, v4, v5
	v_cvt_pk_bf16_f32 v5, v10, v11
	global_store_dwordx4 v[14:15], v[2:5], off offset:256
	s_cbranch_vccnz .LBB0_377
	s_andn2_b64 vcc, exec, s[10:11]
	s_cbranch_vccnz .LBB0_376
	s_branch .LBB0_376

.LBB0_766:
	s_lshl_b32 s0, s21, 4
	s_cmp_lt_i32 s69, s0
	v_readfirstlane_b32 s16, v0
	s_cbranch_scc0 .LBB0_787
	s_lshl_b32 s23, s21, 1
	s_lshr_b32 s14, s16, 6
	s_or_b32 s25, s23, 1
	s_lshr_b32 s15, s16, 8
	s_lshl_b32 s33, s14, 10
	s_add_u32 s8, s2, 0x56800000
	s_addc_u32 s9, s3, 0
	s_add_u32 s46, s2, 0x2800000
	s_addc_u32 s47, s3, 0
	s_add_u32 s50, s2, 0x200000
	s_addc_u32 s51, s3, 0
	s_ashr_i32 s54, s69, 31
	s_lshr_b32 s1, s54, 29
	s_add_i32 s1, s69, s1
	s_ashr_i32 s10, s1, 3
	s_and_b32 s1, s1, -8
	s_sub_i32 s1, s69, s1
	s_cmp_lt_i32 s1, 0
	s_cselect_b32 s11, s25, s23
	s_mul_i32 s1, s11, s1
	s_add_i32 s1, s1, s10
	s_ashr_i32 s10, s1, 31
	s_lshr_b32 s10, s10, 25
	s_add_i32 s10, s1, s10
	s_ashr_i32 s10, s10, 7
	s_lshl_b32 s11, s10, 3
	s_sub_i32 s12, s21, s11
	s_min_i32 s12, s12, 8
	s_abs_i32 s13, s12
	v_cvt_f32_u32_e32 v1, s13
	s_sub_i32 s18, 0, s13
	s_lshl_b32 s10, s10, 7
	s_sub_i32 s1, s1, s10
	v_rcp_iflag_f32_e32 v1, v1
	s_abs_i32 s17, s1
	s_xor_b32 s10, s1, s12
	s_ashr_i32 s10, s10, 31
	v_mul_f32_e32 v1, 0x4f7ffffe, v1
	v_cvt_u32_f32_e32 v1, v1
	v_mov_b32_e32 v2, 0x7f7f7f7f
	v_mov_b32_e32 v163, 0
	v_mov_b32_e32 v165, v163
	v_readfirstlane_b32 s19, v1
	s_mul_i32 s18, s18, s19
	s_mul_hi_u32 s18, s19, s18
	s_add_i32 s19, s19, s18
	s_mul_hi_u32 s18, s17, s19
	s_mul_i32 s19, s18, s13
	s_sub_i32 s17, s17, s19
	s_add_i32 s19, s18, 1
	s_sub_i32 s20, s17, s13
	s_cmp_ge_u32 s17, s13
	s_cselect_b32 s18, s19, s18
	s_cselect_b32 s17, s20, s17
	s_add_i32 s19, s18, 1
	s_cmp_ge_u32 s17, s13
	s_cselect_b32 s13, s19, s18
	s_xor_b32 s13, s13, s10
	s_sub_i32 s34, s13, s10
	s_mul_i32 s10, s34, s12
	s_sub_i32 s1, s1, s10
	s_add_i32 s82, s11, s1
	s_add_i32 s1, s82, 0
	s_add_i32 s1, s1, 0x22200
	v_mov_b32_e32 v1, s1
	ds_read_u8 v1, v1
	v_mov_b32_e32 v167, v163
	s_mov_b64 s[88:89], s[70:71]
	s_mov_b32 s66, 0
	s_waitcnt lgkmcnt(0)
	v_readfirstlane_b32 s36, v1
	s_lshl_b32 s1, s36, 2
	s_add_i32 s1, s1, 0
	s_add_i32 s10, s1, 0x22040
	v_mov_b32_e32 v1, s10
	ds_read_b32 v1, v1
	s_ashr_i32 s37, s36, 31
	s_lshl_b64 s[10:11], s[36:37], 23
	s_waitcnt lgkmcnt(0)
	v_readfirstlane_b32 s12, v1
	s_sub_i32 s12, s82, s12
	s_add_u32 s13, s46, s10
	s_addc_u32 s17, s47, s11
	s_ashr_i32 s35, s34, 31
	s_lshl_b64 s[10:11], s[34:35], 19
	s_add_u32 s40, s13, s10
	s_addc_u32 s41, s17, s11
	s_add_i32 s1, s1, 0x22100
	v_mov_b32_e32 v1, s1
	ds_read_b32 v2, v1
	v_lshrrev_b32_e32 v1, 3, v0
	s_lshl_b32 s1, s12, 8
	v_or_b32_e32 v204, 64, v1
	v_or_b32_e32 v6, s1, v204
	s_waitcnt lgkmcnt(0)
	v_readfirstlane_b32 s12, v2
	v_or_b32_e32 v2, s1, v1
	v_or_b32_e32 v3, 0x80, v2
	v_cmp_gt_i32_e32 vcc, s12, v2
	v_or_b32_e32 v7, 0x80, v6
	s_lshl_b64 s[10:11], s[36:37], 16
	v_cndmask_b32_e32 v2, 0, v2, vcc
	v_cmp_gt_i32_e32 vcc, s12, v3
	s_add_u32 s10, s50, s10
	s_addc_u32 s11, s51, s11
	v_cndmask_b32_e32 v4, 0, v3, vcc
	v_cmp_gt_i32_e32 vcc, s12, v6
	v_ashrrev_i32_e32 v3, 31, v2
	v_lshl_add_u64 v[2:3], v[2:3], 2, s[10:11]
	v_cndmask_b32_e32 v6, 0, v6, vcc
	v_cmp_gt_i32_e32 vcc, s12, v7
	v_ashrrev_i32_e32 v5, 31, v4
	v_lshl_add_u64 v[4:5], v[4:5], 2, s[10:11]
	v_cndmask_b32_e32 v8, 0, v7, vcc
	v_ashrrev_i32_e32 v9, 31, v8
	v_ashrrev_i32_e32 v7, 31, v6
	v_lshl_add_u64 v[8:9], v[8:9], 2, s[10:11]
	v_lshl_add_u64 v[6:7], v[6:7], 2, s[10:11]
	global_load_dword v3, v[2:3], off
	s_nop 0
	global_load_dword v10, v[4:5], off
	global_load_dword v11, v[6:7], off
	s_nop 0
	global_load_dword v8, v[8:9], off
	v_lshrrev_b32_e32 v2, 4, v0
	v_and_b32_e32 v4, 7, v0
	v_lshrrev_b32_e32 v5, 5, v0
	v_lshrrev_b32_e32 v6, 2, v0
	v_and_b32_e32 v7, 4, v2
	v_and_b32_e32 v9, 2, v1
	v_and_b32_e32 v5, 4, v5
	v_and_b32_e32 v12, 35, v1
	v_and_b32_e32 v6, 24, v6
	v_bitop3_b32 v9, v9, v4, v7 bitop3:0x36
	s_movk_i32 s1, 0x63
	v_bitop3_b32 v13, v1, 2, 64 bitop3:0xc8
	v_or3_b32 v12, v12, v6, v5
	v_lshlrev_b32_e32 v205, 4, v9
	s_add_i32 s35, s33, 0
	v_bitop3_b32 v14, v1, s1, 64 bitop3:0xc8
	v_bitop3_b32 v4, v13, v4, v7 bitop3:0x36
	v_lshl_or_b32 v164, v12, 11, v205
	s_add_i32 m0, s35, 0x10000
	v_or3_b32 v5, v14, v6, v5
	v_lshlrev_b32_e32 v206, 4, v4
	global_load_lds_dwordx4 v164, s[40:41]
	s_add_i32 m0, s35, 0x12000
	v_lshl_or_b32 v166, v5, 11, v206
	s_add_u32 s10, s40, 0x40000
	global_load_lds_dwordx4 v166, s[40:41]
	s_addc_u32 s11, s41, 0
	s_add_i32 m0, s35, 0x14000
	s_add_i32 s55, s35, 0x2000
	global_load_lds_dwordx4 v164, s[10:11]
	s_add_i32 m0, s35, 0x16000
	s_add_i32 s64, s35, 0x4000
	global_load_lds_dwordx4 v166, s[10:11]
	s_mov_b32 m0, s35
	s_add_i32 s65, s35, 0x6000
	v_lshl_add_u64 v[4:5], s[40:41], 0, v[164:165]
	s_mov_b64 s[10:11], 0x80
	v_lshl_add_u64 v[4:5], v[4:5], 0, s[10:11]
	v_lshl_add_u64 v[6:7], s[40:41], 0, v[166:167]
	s_waitcnt vmcnt(0)
	v_lshl_or_b32 v176, v3, 11, v205
	global_load_lds_dwordx4 v176, s[8:9]
	v_lshl_or_b32 v178, v11, 11, v206
	s_mov_b32 m0, s55
	v_lshl_or_b32 v180, v10, 11, v205
	global_load_lds_dwordx4 v178, s[8:9]
	s_mov_b32 m0, s64
	v_lshl_or_b32 v182, v8, 11, v206
	global_load_lds_dwordx4 v180, s[8:9]
	s_mov_b32 m0, s65
	s_nop 0
	global_load_lds_dwordx4 v182, s[8:9]
	s_add_i32 m0, s35, 0x18000
	s_nop 0
	global_load_lds_dwordx4 v[4:5], off
	s_add_i32 m0, s35, 0x1a000
	v_lshl_add_u64 v[4:5], v[6:7], 0, s[10:11]
	s_add_u32 s12, s40, 0x40080
	global_load_lds_dwordx4 v[4:5], off
	s_addc_u32 s13, s41, 0
	s_add_i32 m0, s35, 0x1c000
	s_nop 0
	global_load_lds_dwordx4 v164, s[12:13]
	s_add_i32 m0, s35, 0x1e000
	s_cmp_eq_u32 s15, 1
	global_load_lds_dwordx4 v166, s[12:13]
	s_waitcnt vmcnt(6)
	s_cselect_b64 s[12:13], -1, 0
	s_cmp_lg_u32 s15, 1
	s_barrier
	s_cbranch_scc1 .LBB0_769
.LBB0_769:
	s_lshl_b32 s14, s14, 5
	v_lshrrev_b32_e32 v5, 1, v0
	s_ashr_i32 s67, s94, 31
	s_ashr_i32 s1, s0, 31
	s_and_b32 s18, s14, 0x60
	v_and_b32_e32 v3, 15, v0
	v_and_b32_e32 v2, 3, v2
	v_and_b32_e32 v4, 2, v0
	v_and_b32_e32 v5, 4, v5
	s_add_u32 s14, s2, 0x3e800000
	v_bitop3_b32 v4, v5, v2, v4 bitop3:0x36
	v_lshl_or_b32 v207, s15, 6, v3
	s_addc_u32 s15, s3, 0
	v_lshlrev_b32_e32 v4, 4, v4
	v_lshlrev_b32_e32 v5, 7, v207
	v_or_b32_e32 v3, s18, v3
	s_cmpk_lt_u32 s16, 0x100
	v_or_b32_e32 v6, v5, v4
	v_lshlrev_b32_e32 v3, 7, v3
	v_bitop3_b32 v5, v5, 64, v4 bitop3:0x36
	s_cselect_b64 s[16:17], -1, 0
	v_lshl_or_b32 v210, v2, 3, s18
	s_add_u32 s18, s2, 0x56800080
	v_or_b32_e32 v208, v3, v4
	v_bitop3_b32 v209, v3, 64, v4 bitop3:0x36
	s_addc_u32 s19, s3, 0
	v_mov_b64_e32 v[168:169], s[0:1]
	s_add_i32 s68, 0, 0x10000
	s_add_i32 s69, 0, 0x10800
	s_add_i32 s70, 0, 0x14000
	s_add_i32 s71, 0, 0x14800
	v_add_u32_e32 v211, 0, v6
	v_add_u32_e32 v212, 0, v5
	s_add_i32 s72, 0, 0x18000
	s_add_i32 s73, 0, 0x18800
	s_add_i32 s74, 0, 0x1c000
	s_add_i32 s75, 0, 0x1c800
	s_mov_b32 s20, 0x41000000
	s_mov_b32 s22, 0x39000000
	s_mov_b32 s24, 0x37800000
	s_mov_b32 s76, 0xc0c00000
	s_mov_b32 s77, 0x40000
	s_mov_b32 s78, 0x48000
	s_mov_b32 s79, 0x50000
	v_mov_b32_e32 v213, 0x41000000
	s_branch .LBB0_772

.LBB0_776:
	s_lshl_b32 s27, s81, 8
	v_or_b32_e32 v214, s27, v1
	v_or_b32_e32 v216, s27, v204
	s_lshl_b32 s27, s28, 2
	s_add_i32 s27, s27, 0
	s_lshl_b64 s[38:39], s[28:29], 16
	s_add_i32 s27, s27, 0x22100
	s_add_u32 s38, s50, s38
	s_addc_u32 s39, s51, s39
	v_mov_b32_e32 v177, v163
	v_mov_b32_e32 v179, v163
	v_mov_b32_e32 v181, v163
	v_mov_b32_e32 v183, v163
	s_add_u32 s29, s40, 0x100
	v_mov_b32_e32 v34, 0
	v_or_b32_e32 v215, 0x80, v214
	v_or_b32_e32 v217, 0x80, v216
	v_lshl_add_u64 v[184:185], s[18:19], 0, v[182:183]
	v_lshl_add_u64 v[186:187], s[18:19], 0, v[180:181]
	v_lshl_add_u64 v[188:189], s[18:19], 0, v[178:179]
	v_lshl_add_u64 v[190:191], s[18:19], 0, v[176:177]
	s_addc_u32 s37, s41, 0
	s_mov_b32 s83, -2
	s_mov_b64 s[40:41], 0
	v_mov_b32_e32 v35, v34
	v_mov_b32_e32 v36, v34
	v_mov_b32_e32 v37, v34
	v_mov_b32_e32 v38, v34
	v_mov_b32_e32 v39, v34
	v_mov_b32_e32 v40, v34
	v_mov_b32_e32 v41, v34
	v_mov_b32_e32 v50, v34
	v_mov_b32_e32 v51, v34
	v_mov_b32_e32 v52, v34
	v_mov_b32_e32 v53, v34
	v_mov_b32_e32 v54, v34
	v_mov_b32_e32 v55, v34
	v_mov_b32_e32 v56, v34
	v_mov_b32_e32 v57, v34
	v_mov_b32_e32 v66, v34
	v_mov_b32_e32 v67, v34
	v_mov_b32_e32 v68, v34
	v_mov_b32_e32 v69, v34
	v_mov_b32_e32 v70, v34
	v_mov_b32_e32 v71, v34
	v_mov_b32_e32 v72, v34
	v_mov_b32_e32 v73, v34
	v_mov_b32_e32 v82, v34
	v_mov_b32_e32 v83, v34
	v_mov_b32_e32 v84, v34
	v_mov_b32_e32 v85, v34
	v_mov_b32_e32 v86, v34
	v_mov_b32_e32 v87, v34
	v_mov_b32_e32 v88, v34
	v_mov_b32_e32 v89, v34
	v_mov_b32_e32 v42, v34
	v_mov_b32_e32 v43, v34
	v_mov_b32_e32 v44, v34
	v_mov_b32_e32 v45, v34
	v_mov_b32_e32 v46, v34
	v_mov_b32_e32 v47, v34
	v_mov_b32_e32 v48, v34
	v_mov_b32_e32 v49, v34
	v_mov_b32_e32 v58, v34
	v_mov_b32_e32 v59, v34
	v_mov_b32_e32 v60, v34
	v_mov_b32_e32 v61, v34
	v_mov_b32_e32 v62, v34
	v_mov_b32_e32 v63, v34
	v_mov_b32_e32 v64, v34
	v_mov_b32_e32 v65, v34
	v_mov_b32_e32 v74, v34
	v_mov_b32_e32 v75, v34
	v_mov_b32_e32 v76, v34
	v_mov_b32_e32 v77, v34
	v_mov_b32_e32 v78, v34
	v_mov_b32_e32 v79, v34
	v_mov_b32_e32 v80, v34
	v_mov_b32_e32 v81, v34
	v_mov_b32_e32 v90, v34
	v_mov_b32_e32 v91, v34
	v_mov_b32_e32 v92, v34
	v_mov_b32_e32 v93, v34
	v_mov_b32_e32 v94, v34
	v_mov_b32_e32 v95, v34
	v_mov_b32_e32 v96, v34
	v_mov_b32_e32 v97, v34
	v_mov_b32_e32 v98, v34
	v_mov_b32_e32 v99, v34
	v_mov_b32_e32 v100, v34
	v_mov_b32_e32 v101, v34
	v_mov_b32_e32 v102, v34
	v_mov_b32_e32 v103, v34
	v_mov_b32_e32 v104, v34
	v_mov_b32_e32 v105, v34
	v_mov_b32_e32 v114, v34
	v_mov_b32_e32 v115, v34
	v_mov_b32_e32 v116, v34
	v_mov_b32_e32 v117, v34
	v_mov_b32_e32 v118, v34
	v_mov_b32_e32 v119, v34
	v_mov_b32_e32 v120, v34
	v_mov_b32_e32 v121, v34
	v_mov_b32_e32 v130, v34
	v_mov_b32_e32 v131, v34
	v_mov_b32_e32 v132, v34
	v_mov_b32_e32 v133, v34
	v_mov_b32_e32 v134, v34
	v_mov_b32_e32 v135, v34
	v_mov_b32_e32 v136, v34
	v_mov_b32_e32 v137, v34
	v_mov_b32_e32 v138, v34
	v_mov_b32_e32 v139, v34
	v_mov_b32_e32 v140, v34
	v_mov_b32_e32 v141, v34
	v_mov_b32_e32 v142, v34
	v_mov_b32_e32 v143, v34
	v_mov_b32_e32 v144, v34
	v_mov_b32_e32 v145, v34
	v_mov_b32_e32 v106, v34
	v_mov_b32_e32 v107, v34
	v_mov_b32_e32 v108, v34
	v_mov_b32_e32 v109, v34
	v_mov_b32_e32 v110, v34
	v_mov_b32_e32 v111, v34
	v_mov_b32_e32 v112, v34
	v_mov_b32_e32 v113, v34
	v_mov_b32_e32 v122, v34
	v_mov_b32_e32 v123, v34
	v_mov_b32_e32 v124, v34
	v_mov_b32_e32 v125, v34
	v_mov_b32_e32 v126, v34
	v_mov_b32_e32 v127, v34
	v_mov_b32_e32 v128, v34
	v_mov_b32_e32 v129, v34
	v_mov_b32_e32 v146, v34
	v_mov_b32_e32 v147, v34
	v_mov_b32_e32 v148, v34
	v_mov_b32_e32 v149, v34
	v_mov_b32_e32 v150, v34
	v_mov_b32_e32 v151, v34
	v_mov_b32_e32 v152, v34
	v_mov_b32_e32 v153, v34
	v_mov_b32_e32 v154, v34
	v_mov_b32_e32 v155, v34
	v_mov_b32_e32 v156, v34
	v_mov_b32_e32 v157, v34
	v_mov_b32_e32 v158, v34
	v_mov_b32_e32 v159, v34
	v_mov_b32_e32 v160, v34
	v_mov_b32_e32 v161, v34
	s_andn2_b64 vcc, exec, s[12:13]
	s_cbranch_vccnz .Lp6_entry
	s_barrier
.Lp6_entry:
	s_branch .LBB0_778
.LBB0_777:
	s_add_u32 s44, s2, s40
	v_add_u32_e32 v2, s68, v208
	s_addc_u32 s45, s3, s41
	v_add_u32_e32 v3, s68, v209
	ds_read_b128 v[18:21], v2
	ds_read_b128 v[22:25], v3
	v_add_u32_e32 v2, s69, v208
	s_add_u32 s84, s44, 0x56800100
	v_add_u32_e32 v3, s69, v209
	ds_read_b128 v[26:29], v2
	ds_read_b128 v[30:33], v3
	v_add_u32_e32 v2, s70, v208
	v_add_u32_e32 v6, s70, v209
	v_add_u32_e32 v10, s71, v208
	v_add_u32_e32 v14, s71, v209
	s_addc_u32 s85, s45, 0
	ds_read_b128 v[2:5], v2
	ds_read_b128 v[6:9], v6
	ds_read_b128 v[10:13], v10
	ds_read_b128 v[14:17], v14
	s_and_b64 s[44:45], s[42:43], exec
	s_cselect_b32 s45, s9, s85
	s_cselect_b32 s44, s8, s84
	s_add_u32 s84, s29, s40
	s_addc_u32 s85, s37, s41
	s_and_b64 s[42:43], s[42:43], exec
	s_cselect_b32 s43, s31, s85
	s_cselect_b32 s42, s30, s84
	v_lshl_add_u64 v[200:201], v[190:191], 0, s[40:41]
	s_add_i32 m0, s35, 0x8000
	ds_read_b128 v[218:221], v211
	ds_read_b128 v[226:229], v211 offset:2048
	ds_read_b128 v[222:225], v212
	ds_read_b128 v[230:233], v212 offset:2048
	ds_read_b128 v[234:237], v211 offset:4096
	ds_read_b128 v[242:245], v211 offset:6144
	ds_read_b128 v[238:241], v212 offset:4096
	ds_read_b128 v[246:249], v212 offset:6144
	global_load_lds_dwordx4 v[200:201], off
	v_lshl_add_u64 v[200:201], v[188:189], 0, s[40:41]
	s_add_i32 m0, s35, 0xa000
	s_nop 0
	global_load_lds_dwordx4 v[200:201], off
	v_lshl_add_u64 v[200:201], v[186:187], 0, s[40:41]
	s_add_i32 m0, s35, 0xc000
	s_nop 0
	global_load_lds_dwordx4 v[200:201], off
	v_lshl_add_u64 v[200:201], v[184:185], 0, s[40:41]
	s_add_i32 m0, s35, 0xe000
	s_nop 0
	global_load_lds_dwordx4 v[200:201], off
	s_waitcnt vmcnt(8)
	s_waitcnt lgkmcnt(0)
	s_barrier
	s_setprio 1
	s_waitcnt lgkmcnt(0)
	v_mfma_f32_16x16x128_f8f6f4 v[158:161], v[18:25], v[218:225], v[158:161]
	v_mfma_f32_16x16x128_f8f6f4 v[154:157], v[26:33], v[218:225], v[154:157]
	v_mfma_f32_16x16x128_f8f6f4 v[150:153], v[18:25], v[226:233], v[150:153]
	v_mfma_f32_16x16x128_f8f6f4 v[146:149], v[26:33], v[226:233], v[146:149]
	v_mfma_f32_16x16x128_f8f6f4 v[126:129], v[18:25], v[234:241], v[126:129]
	v_mfma_f32_16x16x128_f8f6f4 v[122:125], v[26:33], v[234:241], v[122:125]
	v_mfma_f32_16x16x128_f8f6f4 v[110:113], v[18:25], v[242:249], v[110:113]
	v_mfma_f32_16x16x128_f8f6f4 v[106:109], v[26:33], v[242:249], v[106:109]
	s_setprio 0
	s_setprio 1
	v_mfma_f32_16x16x128_f8f6f4 v[142:145], v[2:9], v[218:225], v[142:145]
	v_mfma_f32_16x16x128_f8f6f4 v[138:141], v[10:17], v[218:225], v[138:141]
	v_mfma_f32_16x16x128_f8f6f4 v[134:137], v[2:9], v[226:233], v[134:137]
	v_mfma_f32_16x16x128_f8f6f4 v[130:133], v[10:17], v[226:233], v[130:133]
	v_mfma_f32_16x16x128_f8f6f4 v[118:121], v[2:9], v[234:241], v[118:121]
	v_mfma_f32_16x16x128_f8f6f4 v[114:117], v[10:17], v[234:241], v[114:117]
	v_mfma_f32_16x16x128_f8f6f4 v[102:105], v[2:9], v[242:249], v[102:105]
	v_mfma_f32_16x16x128_f8f6f4 v[98:101], v[10:17], v[242:249], v[98:101]
	s_setprio 0
	s_barrier
	s_add_i32 s84, s68, s33
	v_lshl_add_u64 v[200:201], s[42:43], 0, v[164:165]
	s_mov_b32 m0, s84
	ds_read_b128 v[218:221], v211 offset:16384
	ds_read_b128 v[226:229], v211 offset:18432
	ds_read_b128 v[222:225], v212 offset:16384
	ds_read_b128 v[230:233], v212 offset:18432
	ds_read_b128 v[234:237], v211 offset:20480
	ds_read_b128 v[242:245], v211 offset:22528
	ds_read_b128 v[238:241], v212 offset:20480
	ds_read_b128 v[246:249], v212 offset:22528
	global_load_lds_dwordx4 v[200:201], off
	s_add_i32 m0, s84, 0x2000
	s_add_u32 s84, s42, 0x40000
	v_lshl_add_u64 v[202:203], s[42:43], 0, v[166:167]
	s_addc_u32 s85, s43, 0
	s_add_i32 s86, s70, s33
	global_load_lds_dwordx4 v[202:203], off
	v_lshl_add_u64 v[250:251], s[84:85], 0, v[164:165]
	s_mov_b32 m0, s86
	s_nop 0
	global_load_lds_dwordx4 v[250:251], off
	v_lshl_add_u64 v[250:251], s[84:85], 0, v[166:167]
	s_add_i32 m0, s86, 0x2000
	s_nop 0
	global_load_lds_dwordx4 v[250:251], off
	s_waitcnt vmcnt(6)
	s_waitcnt lgkmcnt(0)
	s_barrier
	s_setprio 1
	s_waitcnt lgkmcnt(0)
	v_mfma_f32_16x16x128_f8f6f4 v[94:97], v[18:25], v[218:225], v[94:97]
	v_mfma_f32_16x16x128_f8f6f4 v[90:93], v[26:33], v[218:225], v[90:93]
	v_mfma_f32_16x16x128_f8f6f4 v[78:81], v[18:25], v[226:233], v[78:81]
	v_mfma_f32_16x16x128_f8f6f4 v[74:77], v[26:33], v[226:233], v[74:77]
	v_mfma_f32_16x16x128_f8f6f4 v[62:65], v[18:25], v[234:241], v[62:65]
	v_mfma_f32_16x16x128_f8f6f4 v[58:61], v[26:33], v[234:241], v[58:61]
	v_mfma_f32_16x16x128_f8f6f4 v[46:49], v[18:25], v[242:249], v[46:49]
	v_mfma_f32_16x16x128_f8f6f4 v[42:45], v[26:33], v[242:249], v[42:45]
	s_setprio 0
	s_setprio 1
	v_mfma_f32_16x16x128_f8f6f4 v[86:89], v[2:9], v[218:225], v[86:89]
	v_mfma_f32_16x16x128_f8f6f4 v[82:85], v[10:17], v[218:225], v[82:85]
	v_mfma_f32_16x16x128_f8f6f4 v[70:73], v[2:9], v[226:233], v[70:73]
	v_mfma_f32_16x16x128_f8f6f4 v[66:69], v[10:17], v[226:233], v[66:69]
	v_mfma_f32_16x16x128_f8f6f4 v[54:57], v[2:9], v[234:241], v[54:57]
	v_mfma_f32_16x16x128_f8f6f4 v[50:53], v[10:17], v[234:241], v[50:53]
	v_mfma_f32_16x16x128_f8f6f4 v[38:41], v[2:9], v[242:249], v[38:41]
	v_mfma_f32_16x16x128_f8f6f4 v[34:37], v[10:17], v[242:249], v[34:37]
	s_setprio 0
	s_barrier
	v_add_u32_e32 v2, s72, v208
	v_add_u32_e32 v6, s72, v209
	v_add_u32_e32 v10, s73, v208
	v_add_u32_e32 v14, s73, v209
	v_add_u32_e32 v18, s74, v208
	v_add_u32_e32 v22, s74, v209
	v_add_u32_e32 v26, s75, v208
	v_add_u32_e32 v30, s75, v209
	ds_read_b128 v[2:5], v2
	ds_read_b128 v[6:9], v6
	ds_read_b128 v[10:13], v10
	ds_read_b128 v[14:17], v14
	ds_read_b128 v[18:21], v18
	ds_read_b128 v[22:25], v22
	ds_read_b128 v[26:29], v26
	ds_read_b128 v[30:33], v30
	s_mov_b32 m0, s35
	v_lshl_add_u64 v[198:199], s[44:45], 0, v[198:199]
	ds_read_b128 v[218:221], v211 offset:32768
	ds_read_b128 v[226:229], v211 offset:34816
	ds_read_b128 v[222:225], v212 offset:32768
	ds_read_b128 v[230:233], v212 offset:34816
	ds_read_b128 v[234:237], v211 offset:36864
	ds_read_b128 v[242:245], v211 offset:38912
	ds_read_b128 v[238:241], v212 offset:36864
	ds_read_b128 v[246:249], v212 offset:38912
	global_load_lds_dwordx4 v[198:199], off
	v_lshl_add_u64 v[196:197], s[44:45], 0, v[196:197]
	s_mov_b32 m0, s55
	v_lshl_add_u64 v[194:195], s[44:45], 0, v[194:195]
	global_load_lds_dwordx4 v[196:197], off
	s_mov_b32 m0, s64
	v_lshl_add_u64 v[192:193], s[44:45], 0, v[192:193]
	global_load_lds_dwordx4 v[194:195], off
	s_mov_b32 m0, s65
	s_nop 0
	global_load_lds_dwordx4 v[192:193], off
	s_waitcnt vmcnt(8)
	s_waitcnt lgkmcnt(0)
	s_barrier
	s_setprio 1
	s_waitcnt lgkmcnt(0)
	v_mfma_f32_16x16x128_f8f6f4 v[158:161], v[2:9], v[218:225], v[158:161]
	v_mfma_f32_16x16x128_f8f6f4 v[154:157], v[10:17], v[218:225], v[154:157]
	v_mfma_f32_16x16x128_f8f6f4 v[150:153], v[2:9], v[226:233], v[150:153]
	v_mfma_f32_16x16x128_f8f6f4 v[146:149], v[10:17], v[226:233], v[146:149]
	v_mfma_f32_16x16x128_f8f6f4 v[126:129], v[2:9], v[234:241], v[126:129]
	v_mfma_f32_16x16x128_f8f6f4 v[122:125], v[10:17], v[234:241], v[122:125]
	v_mfma_f32_16x16x128_f8f6f4 v[110:113], v[2:9], v[242:249], v[110:113]
	v_mfma_f32_16x16x128_f8f6f4 v[106:109], v[10:17], v[242:249], v[106:109]
	s_setprio 0
	s_setprio 1
	v_mfma_f32_16x16x128_f8f6f4 v[142:145], v[18:25], v[218:225], v[142:145]
	v_mfma_f32_16x16x128_f8f6f4 v[138:141], v[26:33], v[218:225], v[138:141]
	v_mfma_f32_16x16x128_f8f6f4 v[134:137], v[18:25], v[226:233], v[134:137]
	v_mfma_f32_16x16x128_f8f6f4 v[130:133], v[26:33], v[226:233], v[130:133]
	v_mfma_f32_16x16x128_f8f6f4 v[118:121], v[18:25], v[234:241], v[118:121]
	v_mfma_f32_16x16x128_f8f6f4 v[114:117], v[26:33], v[234:241], v[114:117]
	v_mfma_f32_16x16x128_f8f6f4 v[102:105], v[18:25], v[242:249], v[102:105]
	v_mfma_f32_16x16x128_f8f6f4 v[98:101], v[26:33], v[242:249], v[98:101]
	s_setprio 0
	s_barrier
	s_add_i32 s44, s72, s33
	v_lshl_add_u64 v[200:201], v[200:201], 0, s[10:11]
	s_mov_b32 m0, s44
	ds_read_b128 v[192:195], v211 offset:49152
	ds_read_b128 v[218:221], v211 offset:51200
	ds_read_b128 v[196:199], v212 offset:49152
	ds_read_b128 v[222:225], v212 offset:51200
	ds_read_b128 v[226:229], v211 offset:53248
	ds_read_b128 v[234:237], v211 offset:55296
	ds_read_b128 v[230:233], v212 offset:53248
	ds_read_b128 v[238:241], v212 offset:55296
	global_load_lds_dwordx4 v[200:201], off
	s_add_i32 m0, s44, 0x2000
	s_add_u32 s42, s42, 0x40080
	v_lshl_add_u64 v[200:201], v[202:203], 0, s[10:11]
	s_addc_u32 s43, s43, 0
	s_add_i32 s44, s74, s33
	global_load_lds_dwordx4 v[200:201], off
	v_lshl_add_u64 v[200:201], s[42:43], 0, v[164:165]
	s_mov_b32 m0, s44
	s_nop 0
	global_load_lds_dwordx4 v[200:201], off
	v_lshl_add_u64 v[200:201], s[42:43], 0, v[166:167]
	s_add_i32 m0, s44, 0x2000
	s_nop 0
	global_load_lds_dwordx4 v[200:201], off
	s_waitcnt vmcnt(6)
	s_waitcnt lgkmcnt(0)
	s_barrier
	s_setprio 1
	s_waitcnt lgkmcnt(0)
	v_mfma_f32_16x16x128_f8f6f4 v[94:97], v[2:9], v[192:199], v[94:97]
	v_mfma_f32_16x16x128_f8f6f4 v[90:93], v[10:17], v[192:199], v[90:93]
	v_mfma_f32_16x16x128_f8f6f4 v[78:81], v[2:9], v[218:225], v[78:81]
	v_mfma_f32_16x16x128_f8f6f4 v[74:77], v[10:17], v[218:225], v[74:77]
	v_mfma_f32_16x16x128_f8f6f4 v[62:65], v[2:9], v[226:233], v[62:65]
	v_mfma_f32_16x16x128_f8f6f4 v[58:61], v[10:17], v[226:233], v[58:61]
	v_mfma_f32_16x16x128_f8f6f4 v[46:49], v[2:9], v[234:241], v[46:49]
	v_mfma_f32_16x16x128_f8f6f4 v[42:45], v[10:17], v[234:241], v[42:45]
	s_setprio 0
	s_setprio 1
	v_mfma_f32_16x16x128_f8f6f4 v[86:89], v[18:25], v[192:199], v[86:89]
	v_mfma_f32_16x16x128_f8f6f4 v[82:85], v[26:33], v[192:199], v[82:85]
	v_mfma_f32_16x16x128_f8f6f4 v[70:73], v[18:25], v[218:225], v[70:73]
	v_mfma_f32_16x16x128_f8f6f4 v[66:69], v[26:33], v[218:225], v[66:69]
	v_mfma_f32_16x16x128_f8f6f4 v[54:57], v[18:25], v[226:233], v[54:57]
	v_mfma_f32_16x16x128_f8f6f4 v[50:53], v[26:33], v[226:233], v[50:53]
	v_mfma_f32_16x16x128_f8f6f4 v[38:41], v[18:25], v[234:241], v[38:41]
	v_mfma_f32_16x16x128_f8f6f4 v[34:37], v[26:33], v[234:241], v[34:37]
	s_setprio 0
	s_barrier
	s_add_i32 s83, s83, 2
	s_add_u32 s40, s40, 0x100
	s_addc_u32 s41, s41, 0
	s_cmp_gt_u32 s83, 13
	s_cbranch_scc1 .LBB0_781
.LBB0_778:
	s_cmpk_eq_i32 s40, 0x700
	s_cselect_b64 s[42:43], -1, 0
	s_cmpk_lg_i32 s40, 0x700
	v_mov_b64_e32 v[192:193], v[182:183]
	v_mov_b64_e32 v[194:195], v[180:181]
	v_mov_b64_e32 v[196:197], v[178:179]
	v_mov_b64_e32 v[198:199], v[176:177]
	s_cbranch_scc1 .Lp6_idx_chk
	s_andn2_b64 vcc, exec, s[0:1]
	v_cndmask_b32_e32 v172, v172, v180, vcc
	v_cndmask_b32_e32 v174, v174, v182, vcc
	v_cndmask_b32_e32 v162, v162, v176, vcc
	v_cndmask_b32_e32 v170, v170, v178, vcc
	v_mov_b64_e32 v[198:199], v[176:177]
	v_mov_b64_e32 v[196:197], v[178:179]
	v_mov_b64_e32 v[194:195], v[180:181]
	v_mov_b64_e32 v[192:193], v[182:183]
	s_cbranch_vccnz .LBB0_777
	v_mov_b32_e32 v171, v163
	v_mov_b32_e32 v173, v163
	v_mov_b32_e32 v175, v163
	v_lshl_or_b32 v162, v162, 11, v205
	v_lshl_or_b32 v172, v172, 11, v205
	v_lshl_or_b32 v170, v170, 11, v206
	v_lshl_or_b32 v174, v174, 11, v206
	v_mov_b64_e32 v[198:199], v[162:163]
	v_mov_b64_e32 v[196:197], v[170:171]
	v_mov_b64_e32 v[194:195], v[172:173]
	v_mov_b64_e32 v[192:193], v[174:175]
	s_branch .LBB0_777
.Lp6_idx_chk:
	s_cmpk_lg_i32 s40, 0x300
	s_cbranch_scc1 .LBB0_777
	s_andn2_b64 vcc, exec, s[0:1]
	s_cbranch_vccnz .LBB0_777
	v_mov_b32_e32 v2, s27
	ds_read_b32 v2, v2
	s_waitcnt lgkmcnt(0)
	v_readfirstlane_b32 s44, v2
	s_nop 1
	v_cmp_gt_i32_e32 vcc, s44, v214
	s_nop 1
	v_cndmask_b32_e32 v2, 0, v214, vcc
	v_cmp_gt_i32_e32 vcc, s44, v215
	v_ashrrev_i32_e32 v3, 31, v2
	v_lshl_add_u64 v[2:3], v[2:3], 2, s[38:39]
	v_cndmask_b32_e32 v4, 0, v215, vcc
	v_cmp_gt_i32_e32 vcc, s44, v216
	v_ashrrev_i32_e32 v5, 31, v4
	v_lshl_add_u64 v[4:5], v[4:5], 2, s[38:39]
	v_cndmask_b32_e32 v6, 0, v216, vcc
	v_cmp_gt_i32_e32 vcc, s44, v217
	v_ashrrev_i32_e32 v7, 31, v6
	v_lshl_add_u64 v[6:7], v[6:7], 2, s[38:39]
	v_cndmask_b32_e32 v8, 0, v217, vcc
	v_ashrrev_i32_e32 v9, 31, v8
	v_lshl_add_u64 v[8:9], v[8:9], 2, s[38:39]
	global_load_dword v162, v[2:3], off
	s_nop 0
	global_load_dword v172, v[4:5], off
	s_nop 0
	global_load_dword v170, v[6:7], off
	global_load_dword v174, v[8:9], off
	s_branch .LBB0_777
.LBB0_781:
	s_ashr_i32 s37, s36, 31
	v_lshl_or_b32 v20, s34, 7, v210
	s_lshl_b64 s[36:37], s[36:37], 13
	s_add_u32 s38, s48, s36
	v_ashrrev_i32_e32 v21, 31, v20
	s_addc_u32 s39, s49, s37
	v_lshlrev_b64 v[2:3], 2, v[20:21]
	v_lshl_add_u64 v[8:9], s[38:39], 0, v[2:3]
	global_load_dwordx4 v[4:7], v[8:9], off
	global_load_dwordx4 v[12:15], v[8:9], off offset:16
	s_add_u32 s36, s52, s36
	s_addc_u32 s37, s53, s37
	v_lshl_add_u64 v[2:3], s[36:37], 0, v[2:3]
	global_load_dwordx4 v[24:27], v[2:3], off
	global_load_dwordx4 v[28:31], v[2:3], off offset:16
	s_and_b64 vcc, exec, s[16:17]
	s_cbranch_vccz .LBB0_783
	s_barrier
.LBB0_783:
	s_nop 15
	s_nop 15
	v_lshl_add_u32 v22, s82, 8, v207
	v_ashrrev_i32_e32 v23, 31, v22
	v_lshlrev_b64 v[2:3], 11, v[22:23]
	v_mov_b32_e32 v32, v163
	v_mov_b32_e32 v33, v163
	v_lshl_add_u64 v[2:3], s[14:15], 0, v[2:3]
	v_lshl_add_u64 v[2:3], v[2:3], 0, v[20:21]
	s_waitcnt vmcnt(0)
	v_pk_mul_f32 v[8:9], v[6:7], s[20:21] op_sel_hi:[1,0]
	v_pk_mul_f32 v[10:11], v[4:5], s[20:21] op_sel_hi:[1,0]
	v_pk_mul_f32 v[6:7], v[12:13], s[20:21] op_sel_hi:[1,0]
	v_pk_mul_f32 v[4:5], v[14:15], s[20:21] op_sel_hi:[1,0]
	v_pk_fma_f32 v[158:159], v[158:159], s[22:23], v[10:11] op_sel_hi:[1,0,1]
	v_pk_fma_f32 v[154:155], v[154:155], s[22:23], v[6:7] op_sel_hi:[1,0,1]
	v_pk_fma_f32 v[156:157], v[156:157], s[22:23], v[4:5] op_sel_hi:[1,0,1]
	v_pk_add_f32 v[16:17], v[26:27], 1.0 op_sel_hi:[1,0]
	v_pk_add_f32 v[18:19], v[24:25], 1.0 op_sel_hi:[1,0]
	v_min_f32_e32 v24, 0x42600000, v158
	v_min_f32_e32 v26, 0x42600000, v154
	v_min_f32_e32 v25, 0x42600000, v159
	v_min_f32_e32 v27, 0x42600000, v155
	v_pk_add_f32 v[12:13], v[30:31], 1.0 op_sel_hi:[1,0]
	v_min_f32_e32 v31, 0x42600000, v157
	v_mul_f32_e32 v23, 0xbe9d265f, v24
	v_mul_f32_e32 v155, 0xbe9d265f, v26
	v_mul_f32_e32 v157, 0xbe9d265f, v25
	v_mul_f32_e32 v158, 0xbe9d265f, v27
	v_min_f32_e32 v30, 0x42600000, v156
	v_exp_f32_e32 v154, v23
	v_exp_f32_e32 v156, v155
	v_exp_f32_e32 v155, v157
	v_exp_f32_e32 v157, v158
	v_pk_fma_f32 v[160:161], v[160:161], s[22:23], v[8:9] op_sel_hi:[1,0,1]
	v_pk_add_f32 v[14:15], v[28:29], 1.0 op_sel_hi:[1,0]
	v_min_f32_e32 v28, 0x42600000, v160
	v_min_f32_e32 v29, 0x42600000, v161
	v_pk_fma_f32 v[144:145], v[144:145], s[24:25], v[16:17] op_sel_hi:[1,0,1]
	v_pk_fma_f32 v[140:141], v[140:141], s[24:25], v[12:13] op_sel_hi:[1,0,1]
	v_mul_f32_e32 v159, 0xbe9d265f, v28
	v_mul_f32_e32 v160, 0xbe9d265f, v30
	v_mul_f32_e32 v161, 0xbe9d265f, v29
	v_mul_f32_e32 v171, 0xbe9d265f, v31
	v_med3_f32 v144, v144, s76, v213
	v_med3_f32 v140, v140, s76, v213
	v_med3_f32 v145, v145, s76, v213
	v_med3_f32 v141, v141, s76, v213
	v_exp_f32_e32 v158, v159
	v_exp_f32_e32 v160, v160
	v_exp_f32_e32 v159, v161
	v_exp_f32_e32 v161, v171
	v_pk_mul_f32 v[28:29], v[28:29], v[144:145]
	v_pk_mul_f32 v[30:31], v[30:31], v[140:141]
	v_pk_add_f32 v[140:141], v[154:155], 1.0 op_sel_hi:[1,0]
	v_pk_add_f32 v[144:145], v[156:157], 1.0 op_sel_hi:[1,0]
	v_rcp_f32_e32 v140, v140
	v_rcp_f32_e32 v144, v144
	v_rcp_f32_e32 v141, v141
	v_rcp_f32_e32 v145, v145
	v_pk_fma_f32 v[142:143], v[142:143], s[24:25], v[18:19] op_sel_hi:[1,0,1]
	v_pk_fma_f32 v[138:139], v[138:139], s[24:25], v[14:15] op_sel_hi:[1,0,1]
	v_med3_f32 v142, v142, s76, v213
	v_med3_f32 v138, v138, s76, v213
	v_med3_f32 v143, v143, s76, v213
	v_med3_f32 v139, v139, s76, v213
	v_pk_mul_f32 v[24:25], v[24:25], v[142:143]
	v_pk_mul_f32 v[26:27], v[26:27], v[138:139]
	v_pk_add_f32 v[138:139], v[158:159], 1.0 op_sel_hi:[1,0]
	v_pk_add_f32 v[142:143], v[160:161], 1.0 op_sel_hi:[1,0]
	v_rcp_f32_e32 v138, v138
	v_rcp_f32_e32 v142, v142
	v_rcp_f32_e32 v139, v139
	v_rcp_f32_e32 v143, v143
	v_pk_mul_f32 v[24:25], v[24:25], v[140:141]
	v_pk_mul_f32 v[26:27], v[26:27], v[144:145]
	v_cvt_pk_fp8_f32 v32, v24, v25
	v_cvt_pk_fp8_f32 v33, v26, v27
	v_pk_mul_f32 v[24:25], v[28:29], v[138:139]
	v_pk_mul_f32 v[26:27], v[30:31], v[142:143]
	v_cvt_pk_fp8_f32 v32, v24, v25 op_sel:[0,0,1]
	v_cvt_pk_fp8_f32 v33, v26, v27 op_sel:[0,0,1]
	v_pk_fma_f32 v[152:153], v[152:153], s[22:23], v[8:9] op_sel_hi:[1,0,1]
	v_pk_fma_f32 v[150:151], v[150:151], s[22:23], v[10:11] op_sel_hi:[1,0,1]
	v_pk_fma_f32 v[148:149], v[148:149], s[22:23], v[4:5] op_sel_hi:[1,0,1]
	v_pk_fma_f32 v[146:147], v[146:147], s[22:23], v[6:7] op_sel_hi:[1,0,1]
	v_min_f32_e32 v150, 0x42600000, v150
	v_pk_fma_f32 v[134:135], v[134:135], s[24:25], v[18:19] op_sel_hi:[1,0,1]
	v_min_f32_e32 v28, 0x42600000, v152
	v_min_f32_e32 v146, 0x42600000, v146
	v_pk_fma_f32 v[136:137], v[136:137], s[24:25], v[16:17] op_sel_hi:[1,0,1]
	v_pk_fma_f32 v[132:133], v[132:133], s[24:25], v[12:13] op_sel_hi:[1,0,1]
	v_med3_f32 v27, v135, s76, v213
	v_min_f32_e32 v30, 0x42600000, v148
	v_mul_f32_e32 v23, 0xbe9d265f, v150
	v_mul_f32_e32 v135, 0xbe9d265f, v28
	v_pk_fma_f32 v[24:25], v[130:131], s[24:25], v[14:15] op_sel_hi:[1,0,1]
	global_store_dwordx2 v[2:3], v[32:33], off
	v_min_f32_e32 v151, 0x42600000, v151
	v_med3_f32 v32, v136, s76, v213
	v_med3_f32 v130, v132, s76, v213
	v_min_f32_e32 v29, 0x42600000, v153
	v_exp_f32_e32 v132, v23
	v_mul_f32_e32 v23, 0xbe9d265f, v146
	v_exp_f32_e32 v136, v135
	v_mul_f32_e32 v135, 0xbe9d265f, v30
	v_med3_f32 v26, v134, s76, v213
	v_min_f32_e32 v147, 0x42600000, v147
	v_min_f32_e32 v31, 0x42600000, v149
	v_exp_f32_e32 v134, v23
	v_mul_f32_e32 v23, 0xbe9d265f, v151
	v_exp_f32_e32 v138, v135
	v_mul_f32_e32 v135, 0xbe9d265f, v29
	v_med3_f32 v33, v137, s76, v213
	v_med3_f32 v131, v133, s76, v213
	v_exp_f32_e32 v133, v23
	v_mul_f32_e32 v23, 0xbe9d265f, v147
	v_exp_f32_e32 v137, v135
	v_mul_f32_e32 v135, 0xbe9d265f, v31
	v_exp_f32_e32 v139, v135
	v_exp_f32_e32 v135, v23
	v_pk_add_f32 v[132:133], v[132:133], 1.0 op_sel_hi:[1,0]
	v_med3_f32 v24, v24, s76, v213
	v_rcp_f32_e32 v132, v132
	v_pk_add_f32 v[134:135], v[134:135], 1.0 op_sel_hi:[1,0]
	v_rcp_f32_e32 v133, v133
	v_rcp_f32_e32 v134, v134
	v_rcp_f32_e32 v135, v135
	v_med3_f32 v25, v25, s76, v213
	v_pk_add_f32 v[138:139], v[138:139], 1.0 op_sel_hi:[1,0]
	v_pk_mul_f32 v[24:25], v[146:147], v[24:25]
	v_pk_add_f32 v[136:137], v[136:137], 1.0 op_sel_hi:[1,0]
	v_rcp_f32_e32 v138, v138
	v_rcp_f32_e32 v139, v139
	v_pk_mul_f32 v[28:29], v[28:29], v[32:33]
	v_pk_mul_f32 v[26:27], v[150:151], v[26:27]
	v_pk_mul_f32 v[24:25], v[24:25], v[134:135]
	v_mov_b32_e32 v33, v163
	v_rcp_f32_e32 v136, v136
	v_rcp_f32_e32 v137, v137
	v_pk_mul_f32 v[26:27], v[26:27], v[132:133]
	v_mov_b32_e32 v32, v163
	v_cvt_pk_fp8_f32 v33, v24, v25
	v_cvt_pk_fp8_f32 v32, v26, v27
	v_pk_mul_f32 v[24:25], v[30:31], v[130:131]
	v_pk_mul_f32 v[28:29], v[28:29], v[136:137]
	v_pk_mul_f32 v[24:25], v[24:25], v[138:139]
	v_cvt_pk_fp8_f32 v32, v28, v29 op_sel:[0,0,1]
	v_cvt_pk_fp8_f32 v33, v24, v25 op_sel:[0,0,1]
	v_or_b32_e32 v24, 16, v22
	v_ashrrev_i32_e32 v25, 31, v24
	v_lshlrev_b64 v[24:25], 11, v[24:25]
	v_lshl_add_u64 v[24:25], s[14:15], 0, v[24:25]
	v_lshl_add_u64 v[24:25], v[24:25], 0, v[20:21]
	global_store_dwordx2 v[24:25], v[32:33], off
	v_pk_fma_f32 v[24:25], v[128:129], s[22:23], v[8:9] op_sel_hi:[1,0,1]
	v_pk_fma_f32 v[26:27], v[126:127], s[22:23], v[10:11] op_sel_hi:[1,0,1]
	v_pk_fma_f32 v[28:29], v[124:125], s[22:23], v[4:5] op_sel_hi:[1,0,1]
	v_pk_fma_f32 v[30:31], v[122:123], s[22:23], v[6:7] op_sel_hi:[1,0,1]
	v_min_f32_e32 v26, 0x42600000, v26
	v_min_f32_e32 v24, 0x42600000, v24
	v_min_f32_e32 v30, 0x42600000, v30
	v_min_f32_e32 v28, 0x42600000, v28
	v_mul_f32_e32 v23, 0xbe9d265f, v26
	v_mul_f32_e32 v123, 0xbe9d265f, v24
	v_pk_fma_f32 v[32:33], v[120:121], s[24:25], v[16:17] op_sel_hi:[1,0,1]
	v_min_f32_e32 v27, 0x42600000, v27
	v_min_f32_e32 v25, 0x42600000, v25
	v_exp_f32_e32 v120, v23
	v_mul_f32_e32 v23, 0xbe9d265f, v30
	v_exp_f32_e32 v124, v123
	v_mul_f32_e32 v123, 0xbe9d265f, v28
	v_min_f32_e32 v31, 0x42600000, v31
	v_min_f32_e32 v29, 0x42600000, v29
	v_exp_f32_e32 v122, v23
	v_mul_f32_e32 v23, 0xbe9d265f, v27
	v_exp_f32_e32 v126, v123
	v_mul_f32_e32 v123, 0xbe9d265f, v25
	v_exp_f32_e32 v121, v23
	v_mul_f32_e32 v23, 0xbe9d265f, v31
	v_exp_f32_e32 v125, v123
	v_mul_f32_e32 v123, 0xbe9d265f, v29
	v_exp_f32_e32 v127, v123
	v_exp_f32_e32 v123, v23
	v_pk_add_f32 v[120:121], v[120:121], 1.0 op_sel_hi:[1,0]
	v_pk_fma_f32 v[118:119], v[118:119], s[24:25], v[18:19] op_sel_hi:[1,0,1]
	v_rcp_f32_e32 v120, v120
	v_pk_add_f32 v[122:123], v[122:123], 1.0 op_sel_hi:[1,0]
	v_rcp_f32_e32 v121, v121
	v_rcp_f32_e32 v122, v122
	v_rcp_f32_e32 v123, v123
	v_pk_fma_f32 v[114:115], v[114:115], s[24:25], v[14:15] op_sel_hi:[1,0,1]
	v_med3_f32 v118, v118, s76, v213
	v_med3_f32 v119, v119, s76, v213
	v_med3_f32 v114, v114, s76, v213
	v_med3_f32 v115, v115, s76, v213
	v_med3_f32 v32, v32, s76, v213
	v_med3_f32 v33, v33, s76, v213
	v_pk_add_f32 v[124:125], v[124:125], 1.0 op_sel_hi:[1,0]
	v_pk_mul_f32 v[26:27], v[26:27], v[118:119]
	v_pk_add_f32 v[126:127], v[126:127], 1.0 op_sel_hi:[1,0]
	v_rcp_f32_e32 v124, v124
	v_rcp_f32_e32 v125, v125
	v_pk_mul_f32 v[24:25], v[24:25], v[32:33]
	v_pk_mul_f32 v[26:27], v[26:27], v[120:121]
	v_pk_mul_f32 v[30:31], v[30:31], v[114:115]
	v_mov_b32_e32 v32, v163
	v_rcp_f32_e32 v126, v126
	v_rcp_f32_e32 v127, v127
	v_pk_mul_f32 v[30:31], v[30:31], v[122:123]
	v_cvt_pk_fp8_f32 v32, v26, v27
	v_mov_b32_e32 v33, v163
	v_pk_fma_f32 v[116:117], v[116:117], s[24:25], v[12:13] op_sel_hi:[1,0,1]
	v_cvt_pk_fp8_f32 v33, v30, v31
	v_med3_f32 v116, v116, s76, v213
	v_med3_f32 v117, v117, s76, v213
	v_pk_mul_f32 v[24:25], v[24:25], v[124:125]
	v_pk_mul_f32 v[26:27], v[28:29], v[116:117]
	v_cvt_pk_fp8_f32 v32, v24, v25 op_sel:[0,0,1]
	v_pk_mul_f32 v[26:27], v[26:27], v[126:127]
	v_or_b32_e32 v24, 32, v22
	v_cvt_pk_fp8_f32 v33, v26, v27 op_sel:[0,0,1]
	v_ashrrev_i32_e32 v25, 31, v24
	v_lshlrev_b64 v[24:25], 11, v[24:25]
	v_lshl_add_u64 v[24:25], s[14:15], 0, v[24:25]
	v_lshl_add_u64 v[24:25], v[24:25], 0, v[20:21]
	global_store_dwordx2 v[24:25], v[32:33], off
	v_pk_fma_f32 v[24:25], v[112:113], s[22:23], v[8:9] op_sel_hi:[1,0,1]
	v_pk_fma_f32 v[26:27], v[110:111], s[22:23], v[10:11] op_sel_hi:[1,0,1]
	v_pk_fma_f32 v[28:29], v[108:109], s[22:23], v[4:5] op_sel_hi:[1,0,1]
	v_pk_fma_f32 v[30:31], v[106:107], s[22:23], v[6:7] op_sel_hi:[1,0,1]
	v_min_f32_e32 v26, 0x42600000, v26
	v_min_f32_e32 v24, 0x42600000, v24
	v_min_f32_e32 v30, 0x42600000, v30
	v_min_f32_e32 v28, 0x42600000, v28
	v_mul_f32_e32 v23, 0xbe9d265f, v26
	v_mul_f32_e32 v107, 0xbe9d265f, v24
	v_pk_fma_f32 v[32:33], v[104:105], s[24:25], v[16:17] op_sel_hi:[1,0,1]
	v_min_f32_e32 v27, 0x42600000, v27
	v_min_f32_e32 v25, 0x42600000, v25
	v_exp_f32_e32 v104, v23
	v_mul_f32_e32 v23, 0xbe9d265f, v30
	v_exp_f32_e32 v108, v107
	v_mul_f32_e32 v107, 0xbe9d265f, v28
	v_min_f32_e32 v31, 0x42600000, v31
	v_min_f32_e32 v29, 0x42600000, v29
	v_exp_f32_e32 v106, v23
	v_mul_f32_e32 v23, 0xbe9d265f, v27
	v_exp_f32_e32 v110, v107
	v_mul_f32_e32 v107, 0xbe9d265f, v25
	v_exp_f32_e32 v105, v23
	v_mul_f32_e32 v23, 0xbe9d265f, v31
	v_exp_f32_e32 v109, v107
	v_mul_f32_e32 v107, 0xbe9d265f, v29
	v_exp_f32_e32 v111, v107
	v_exp_f32_e32 v107, v23
	v_pk_add_f32 v[104:105], v[104:105], 1.0 op_sel_hi:[1,0]
	v_pk_fma_f32 v[102:103], v[102:103], s[24:25], v[18:19] op_sel_hi:[1,0,1]
	v_rcp_f32_e32 v104, v104
	v_pk_add_f32 v[106:107], v[106:107], 1.0 op_sel_hi:[1,0]
	v_rcp_f32_e32 v105, v105
	v_rcp_f32_e32 v106, v106
	v_rcp_f32_e32 v107, v107
	v_pk_fma_f32 v[98:99], v[98:99], s[24:25], v[14:15] op_sel_hi:[1,0,1]
	v_med3_f32 v102, v102, s76, v213
	v_med3_f32 v98, v98, s76, v213
	v_med3_f32 v103, v103, s76, v213
	v_med3_f32 v99, v99, s76, v213
	v_med3_f32 v32, v32, s76, v213
	v_med3_f32 v33, v33, s76, v213
	v_pk_add_f32 v[108:109], v[108:109], 1.0 op_sel_hi:[1,0]
	v_pk_add_f32 v[110:111], v[110:111], 1.0 op_sel_hi:[1,0]
	v_pk_mul_f32 v[26:27], v[26:27], v[102:103]
	v_pk_mul_f32 v[30:31], v[30:31], v[98:99]
	v_rcp_f32_e32 v108, v108
	v_rcp_f32_e32 v110, v110
	v_rcp_f32_e32 v109, v109
	v_rcp_f32_e32 v111, v111
	v_pk_mul_f32 v[24:25], v[24:25], v[32:33]
	v_pk_mul_f32 v[26:27], v[26:27], v[104:105]
	v_pk_mul_f32 v[30:31], v[30:31], v[106:107]
	v_mov_b32_e32 v32, v163
	v_mov_b32_e32 v33, v163
	v_pk_fma_f32 v[100:101], v[100:101], s[24:25], v[12:13] op_sel_hi:[1,0,1]
	v_cvt_pk_fp8_f32 v32, v26, v27
	v_cvt_pk_fp8_f32 v33, v30, v31
	v_med3_f32 v100, v100, s76, v213
	v_med3_f32 v101, v101, s76, v213
	v_pk_mul_f32 v[26:27], v[28:29], v[100:101]
	v_pk_mul_f32 v[24:25], v[24:25], v[108:109]
	v_pk_mul_f32 v[26:27], v[26:27], v[110:111]
	v_or_b32_e32 v22, 48, v22
	v_cvt_pk_fp8_f32 v32, v24, v25 op_sel:[0,0,1]
	v_cvt_pk_fp8_f32 v33, v26, v27 op_sel:[0,0,1]
	v_ashrrev_i32_e32 v23, 31, v22
	v_lshlrev_b64 v[22:23], 11, v[22:23]
	v_lshl_add_u64 v[22:23], s[14:15], 0, v[22:23]
	v_pk_fma_f32 v[26:27], v[90:91], s[22:23], v[6:7] op_sel_hi:[1,0,1]
	v_lshl_add_u64 v[20:21], v[22:23], 0, v[20:21]
	v_pk_fma_f32 v[22:23], v[94:95], s[22:23], v[10:11] op_sel_hi:[1,0,1]
	v_min_f32_e32 v26, 0x42600000, v26
	global_store_dwordx2 v[20:21], v[32:33], off
	v_pk_fma_f32 v[32:33], v[84:85], s[24:25], v[12:13] op_sel_hi:[1,0,1]
	v_min_f32_e32 v22, 0x42600000, v22
	v_min_f32_e32 v23, 0x42600000, v23
	v_min_f32_e32 v27, 0x42600000, v27
	v_mul_f32_e32 v85, 0xbe9d265f, v26
	v_pk_fma_f32 v[30:31], v[86:87], s[24:25], v[18:19] op_sel_hi:[1,0,1]
	v_mul_f32_e32 v84, 0xbe9d265f, v22
	v_exp_f32_e32 v86, v85
	v_mul_f32_e32 v85, 0xbe9d265f, v23
	v_mul_f32_e32 v87, 0xbe9d265f, v27
	v_pk_fma_f32 v[24:25], v[92:93], s[22:23], v[4:5] op_sel_hi:[1,0,1]
	v_exp_f32_e32 v84, v84
	v_exp_f32_e32 v85, v85
	v_exp_f32_e32 v87, v87
	v_pk_fma_f32 v[20:21], v[96:97], s[22:23], v[8:9] op_sel_hi:[1,0,1]
	v_min_f32_e32 v24, 0x42600000, v24
	v_pk_fma_f32 v[28:29], v[88:89], s[24:25], v[16:17] op_sel_hi:[1,0,1]
	v_min_f32_e32 v20, 0x42600000, v20
	v_min_f32_e32 v21, 0x42600000, v21
	v_min_f32_e32 v25, 0x42600000, v25
	v_mul_f32_e32 v89, 0xbe9d265f, v24
	v_mul_f32_e32 v88, 0xbe9d265f, v20
	v_exp_f32_e32 v90, v89
	v_mul_f32_e32 v89, 0xbe9d265f, v21
	v_mul_f32_e32 v91, 0xbe9d265f, v25
	v_exp_f32_e32 v88, v88
	v_exp_f32_e32 v89, v89
	v_exp_f32_e32 v91, v91
	v_pk_add_f32 v[84:85], v[84:85], 1.0 op_sel_hi:[1,0]
	v_pk_add_f32 v[86:87], v[86:87], 1.0 op_sel_hi:[1,0]
	v_rcp_f32_e32 v84, v84
	v_rcp_f32_e32 v86, v86
	v_rcp_f32_e32 v85, v85
	v_rcp_f32_e32 v87, v87
	v_pk_fma_f32 v[82:83], v[82:83], s[24:25], v[14:15] op_sel_hi:[1,0,1]
	v_med3_f32 v30, v30, s76, v213
	v_med3_f32 v82, v82, s76, v213
	v_med3_f32 v31, v31, s76, v213
	v_med3_f32 v83, v83, s76, v213
	v_med3_f32 v28, v28, s76, v213
	v_med3_f32 v29, v29, s76, v213
	v_pk_add_f32 v[88:89], v[88:89], 1.0 op_sel_hi:[1,0]
	v_pk_add_f32 v[90:91], v[90:91], 1.0 op_sel_hi:[1,0]
	v_pk_mul_f32 v[22:23], v[22:23], v[30:31]
	v_pk_mul_f32 v[26:27], v[26:27], v[82:83]
	v_rcp_f32_e32 v88, v88
	v_rcp_f32_e32 v90, v90
	v_rcp_f32_e32 v89, v89
	v_rcp_f32_e32 v91, v91
	v_pk_mul_f32 v[20:21], v[20:21], v[28:29]
	v_pk_mul_f32 v[22:23], v[22:23], v[84:85]
	v_pk_mul_f32 v[26:27], v[26:27], v[86:87]
	v_mov_b32_e32 v28, v163
	v_mov_b32_e32 v29, v163
	v_cvt_pk_fp8_f32 v28, v22, v23
	v_cvt_pk_fp8_f32 v29, v26, v27
	v_med3_f32 v32, v32, s76, v213
	v_med3_f32 v33, v33, s76, v213
	v_pk_mul_f32 v[22:23], v[24:25], v[32:33]
	v_pk_mul_f32 v[20:21], v[20:21], v[88:89]
	v_pk_mul_f32 v[22:23], v[22:23], v[90:91]
	v_pk_fma_f32 v[26:27], v[74:75], s[22:23], v[6:7] op_sel_hi:[1,0,1]
	v_cvt_pk_fp8_f32 v28, v20, v21 op_sel:[0,0,1]
	v_cvt_pk_fp8_f32 v29, v22, v23 op_sel:[0,0,1]
	v_pk_fma_f32 v[22:23], v[78:79], s[22:23], v[10:11] op_sel_hi:[1,0,1]
	v_min_f32_e32 v26, 0x42600000, v26
	v_pk_fma_f32 v[32:33], v[68:69], s[24:25], v[12:13] op_sel_hi:[1,0,1]
	v_min_f32_e32 v22, 0x42600000, v22
	v_min_f32_e32 v23, 0x42600000, v23
	v_min_f32_e32 v27, 0x42600000, v27
	v_mul_f32_e32 v69, 0xbe9d265f, v26
	v_add_co_u32_e32 v20, vcc, s77, v2
	v_pk_fma_f32 v[30:31], v[70:71], s[24:25], v[18:19] op_sel_hi:[1,0,1]
	v_mul_f32_e32 v68, 0xbe9d265f, v22
	v_exp_f32_e32 v70, v69
	v_mul_f32_e32 v69, 0xbe9d265f, v23
	v_mul_f32_e32 v71, 0xbe9d265f, v27
	v_addc_co_u32_e32 v21, vcc, 0, v3, vcc
	v_pk_fma_f32 v[24:25], v[76:77], s[22:23], v[4:5] op_sel_hi:[1,0,1]
	v_exp_f32_e32 v68, v68
	v_exp_f32_e32 v69, v69
	v_exp_f32_e32 v71, v71
	global_store_dwordx2 v[20:21], v[28:29], off
	v_pk_fma_f32 v[20:21], v[80:81], s[22:23], v[8:9] op_sel_hi:[1,0,1]
	v_min_f32_e32 v24, 0x42600000, v24
	v_pk_fma_f32 v[28:29], v[72:73], s[24:25], v[16:17] op_sel_hi:[1,0,1]
	v_min_f32_e32 v20, 0x42600000, v20
	v_min_f32_e32 v21, 0x42600000, v21
	v_min_f32_e32 v25, 0x42600000, v25
	v_mul_f32_e32 v73, 0xbe9d265f, v24
	v_mul_f32_e32 v72, 0xbe9d265f, v20
	v_exp_f32_e32 v74, v73
	v_mul_f32_e32 v73, 0xbe9d265f, v21
	v_mul_f32_e32 v75, 0xbe9d265f, v25
	v_exp_f32_e32 v72, v72
	v_exp_f32_e32 v73, v73
	v_exp_f32_e32 v75, v75
	v_pk_add_f32 v[68:69], v[68:69], 1.0 op_sel_hi:[1,0]
	v_pk_add_f32 v[70:71], v[70:71], 1.0 op_sel_hi:[1,0]
	v_rcp_f32_e32 v68, v68
	v_rcp_f32_e32 v70, v70
	v_rcp_f32_e32 v69, v69
	v_rcp_f32_e32 v71, v71
	v_pk_fma_f32 v[66:67], v[66:67], s[24:25], v[14:15] op_sel_hi:[1,0,1]
	v_med3_f32 v30, v30, s76, v213
	v_med3_f32 v66, v66, s76, v213
	v_med3_f32 v31, v31, s76, v213
	v_med3_f32 v67, v67, s76, v213
	v_med3_f32 v28, v28, s76, v213
	v_med3_f32 v29, v29, s76, v213
	v_pk_add_f32 v[72:73], v[72:73], 1.0 op_sel_hi:[1,0]
	v_pk_add_f32 v[74:75], v[74:75], 1.0 op_sel_hi:[1,0]
	v_pk_mul_f32 v[22:23], v[22:23], v[30:31]
	v_pk_mul_f32 v[26:27], v[26:27], v[66:67]
	v_rcp_f32_e32 v72, v72
	v_rcp_f32_e32 v74, v74
	v_rcp_f32_e32 v73, v73
	v_rcp_f32_e32 v75, v75
	v_pk_mul_f32 v[20:21], v[20:21], v[28:29]
	v_pk_mul_f32 v[22:23], v[22:23], v[68:69]
	v_pk_mul_f32 v[26:27], v[26:27], v[70:71]
	v_mov_b32_e32 v28, v163
	v_mov_b32_e32 v29, v163
	v_cvt_pk_fp8_f32 v28, v22, v23
	v_cvt_pk_fp8_f32 v29, v26, v27
	v_med3_f32 v32, v32, s76, v213
	v_med3_f32 v33, v33, s76, v213
	v_pk_mul_f32 v[22:23], v[24:25], v[32:33]
	v_pk_mul_f32 v[20:21], v[20:21], v[72:73]
	v_pk_mul_f32 v[22:23], v[22:23], v[74:75]
	v_pk_fma_f32 v[26:27], v[58:59], s[22:23], v[6:7] op_sel_hi:[1,0,1]
	v_cvt_pk_fp8_f32 v28, v20, v21 op_sel:[0,0,1]
	v_cvt_pk_fp8_f32 v29, v22, v23 op_sel:[0,0,1]
	v_pk_fma_f32 v[22:23], v[62:63], s[22:23], v[10:11] op_sel_hi:[1,0,1]
	v_min_f32_e32 v26, 0x42600000, v26
	v_pk_fma_f32 v[32:33], v[52:53], s[24:25], v[12:13] op_sel_hi:[1,0,1]
	v_min_f32_e32 v22, 0x42600000, v22
	v_min_f32_e32 v23, 0x42600000, v23
	v_min_f32_e32 v27, 0x42600000, v27
	v_mul_f32_e32 v53, 0xbe9d265f, v26
	v_add_co_u32_e32 v20, vcc, s78, v2
	v_pk_fma_f32 v[30:31], v[54:55], s[24:25], v[18:19] op_sel_hi:[1,0,1]
	v_mul_f32_e32 v52, 0xbe9d265f, v22
	v_exp_f32_e32 v54, v53
	v_mul_f32_e32 v53, 0xbe9d265f, v23
	v_mul_f32_e32 v55, 0xbe9d265f, v27
	v_addc_co_u32_e32 v21, vcc, 0, v3, vcc
	v_pk_fma_f32 v[24:25], v[60:61], s[22:23], v[4:5] op_sel_hi:[1,0,1]
	v_exp_f32_e32 v52, v52
	v_exp_f32_e32 v53, v53
	v_exp_f32_e32 v55, v55
	global_store_dwordx2 v[20:21], v[28:29], off
	v_pk_fma_f32 v[20:21], v[64:65], s[22:23], v[8:9] op_sel_hi:[1,0,1]
	v_min_f32_e32 v24, 0x42600000, v24
	v_pk_fma_f32 v[28:29], v[56:57], s[24:25], v[16:17] op_sel_hi:[1,0,1]
	v_min_f32_e32 v20, 0x42600000, v20
	v_min_f32_e32 v21, 0x42600000, v21
	v_min_f32_e32 v25, 0x42600000, v25
	v_mul_f32_e32 v57, 0xbe9d265f, v24
	v_mul_f32_e32 v56, 0xbe9d265f, v20
	v_exp_f32_e32 v58, v57
	v_mul_f32_e32 v57, 0xbe9d265f, v21
	v_mul_f32_e32 v59, 0xbe9d265f, v25
	v_exp_f32_e32 v56, v56
	v_exp_f32_e32 v57, v57
	v_exp_f32_e32 v59, v59
	v_pk_add_f32 v[52:53], v[52:53], 1.0 op_sel_hi:[1,0]
	v_pk_add_f32 v[54:55], v[54:55], 1.0 op_sel_hi:[1,0]
	v_rcp_f32_e32 v52, v52
	v_rcp_f32_e32 v54, v54
	v_rcp_f32_e32 v53, v53
	v_rcp_f32_e32 v55, v55
	v_pk_fma_f32 v[50:51], v[50:51], s[24:25], v[14:15] op_sel_hi:[1,0,1]
	v_med3_f32 v30, v30, s76, v213
	v_med3_f32 v50, v50, s76, v213
	v_med3_f32 v31, v31, s76, v213
	v_med3_f32 v51, v51, s76, v213
	v_med3_f32 v28, v28, s76, v213
	v_med3_f32 v29, v29, s76, v213
	v_pk_add_f32 v[56:57], v[56:57], 1.0 op_sel_hi:[1,0]
	v_pk_add_f32 v[58:59], v[58:59], 1.0 op_sel_hi:[1,0]
	v_pk_mul_f32 v[22:23], v[22:23], v[30:31]
	v_pk_mul_f32 v[26:27], v[26:27], v[50:51]
	v_rcp_f32_e32 v56, v56
	v_rcp_f32_e32 v58, v58
	v_rcp_f32_e32 v57, v57
	v_rcp_f32_e32 v59, v59
	v_pk_mul_f32 v[20:21], v[20:21], v[28:29]
	v_pk_mul_f32 v[22:23], v[22:23], v[52:53]
	v_pk_mul_f32 v[26:27], v[26:27], v[54:55]
	v_mov_b32_e32 v28, v163
	v_mov_b32_e32 v29, v163
	v_cvt_pk_fp8_f32 v28, v22, v23
	v_cvt_pk_fp8_f32 v29, v26, v27
	v_med3_f32 v32, v32, s76, v213
	v_med3_f32 v33, v33, s76, v213
	v_pk_mul_f32 v[22:23], v[24:25], v[32:33]
	v_pk_mul_f32 v[20:21], v[20:21], v[56:57]
	v_pk_mul_f32 v[22:23], v[22:23], v[58:59]
	v_cvt_pk_fp8_f32 v28, v20, v21 op_sel:[0,0,1]
	v_cvt_pk_fp8_f32 v29, v22, v23 op_sel:[0,0,1]
	v_add_co_u32_e32 v20, vcc, s79, v2
	v_pk_fma_f32 v[6:7], v[42:43], s[22:23], v[6:7] op_sel_hi:[1,0,1]
	s_nop 0
	v_addc_co_u32_e32 v21, vcc, 0, v3, vcc
	v_pk_fma_f32 v[10:11], v[46:47], s[22:23], v[10:11] op_sel_hi:[1,0,1]
	v_min_f32_e32 v6, 0x42600000, v6
	global_store_dwordx2 v[20:21], v[28:29], off
	v_min_f32_e32 v10, 0x42600000, v10
	v_min_f32_e32 v11, 0x42600000, v11
	v_min_f32_e32 v7, 0x42600000, v7
	v_mul_f32_e32 v21, 0xbe9d265f, v6
	v_mul_f32_e32 v20, 0xbe9d265f, v10
	v_exp_f32_e32 v22, v21
	v_mul_f32_e32 v21, 0xbe9d265f, v11
	v_mul_f32_e32 v23, 0xbe9d265f, v7
	v_pk_fma_f32 v[4:5], v[44:45], s[22:23], v[4:5] op_sel_hi:[1,0,1]
	v_exp_f32_e32 v20, v20
	v_exp_f32_e32 v21, v21
	v_exp_f32_e32 v23, v23
	v_pk_fma_f32 v[8:9], v[48:49], s[22:23], v[8:9] op_sel_hi:[1,0,1]
	v_min_f32_e32 v4, 0x42600000, v4
	v_min_f32_e32 v8, 0x42600000, v8
	v_min_f32_e32 v9, 0x42600000, v9
	v_min_f32_e32 v5, 0x42600000, v5
	v_mul_f32_e32 v25, 0xbe9d265f, v4
	v_mul_f32_e32 v24, 0xbe9d265f, v8
	v_exp_f32_e32 v26, v25
	v_mul_f32_e32 v25, 0xbe9d265f, v9
	v_mul_f32_e32 v27, 0xbe9d265f, v5
	v_exp_f32_e32 v24, v24
	v_exp_f32_e32 v25, v25
	v_exp_f32_e32 v27, v27
	v_pk_add_f32 v[20:21], v[20:21], 1.0 op_sel_hi:[1,0]
	v_pk_add_f32 v[22:23], v[22:23], 1.0 op_sel_hi:[1,0]
	v_rcp_f32_e32 v20, v20
	v_rcp_f32_e32 v22, v22
	v_rcp_f32_e32 v21, v21
	v_rcp_f32_e32 v23, v23
	v_pk_fma_f32 v[18:19], v[38:39], s[24:25], v[18:19] op_sel_hi:[1,0,1]
	v_pk_fma_f32 v[14:15], v[34:35], s[24:25], v[14:15] op_sel_hi:[1,0,1]
	v_med3_f32 v18, v18, s76, v213
	v_med3_f32 v14, v14, s76, v213
	v_med3_f32 v19, v19, s76, v213
	v_med3_f32 v15, v15, s76, v213
	v_pk_add_f32 v[24:25], v[24:25], 1.0 op_sel_hi:[1,0]
	v_pk_add_f32 v[26:27], v[26:27], 1.0 op_sel_hi:[1,0]
	v_pk_mul_f32 v[10:11], v[10:11], v[18:19]
	v_pk_mul_f32 v[6:7], v[6:7], v[14:15]
	v_rcp_f32_e32 v24, v24
	v_rcp_f32_e32 v26, v26
	v_rcp_f32_e32 v25, v25
	v_rcp_f32_e32 v27, v27
	v_pk_mul_f32 v[10:11], v[10:11], v[20:21]
	v_pk_mul_f32 v[6:7], v[6:7], v[22:23]
	v_mov_b32_e32 v14, v163
	v_mov_b32_e32 v15, v163
	v_pk_fma_f32 v[16:17], v[40:41], s[24:25], v[16:17] op_sel_hi:[1,0,1]
	v_pk_fma_f32 v[12:13], v[36:37], s[24:25], v[12:13] op_sel_hi:[1,0,1]
	v_cvt_pk_fp8_f32 v14, v10, v11
	v_cvt_pk_fp8_f32 v15, v6, v7
	v_med3_f32 v16, v16, s76, v213
	v_med3_f32 v12, v12, s76, v213
	v_med3_f32 v17, v17, s76, v213
	v_med3_f32 v13, v13, s76, v213
	v_pk_mul_f32 v[8:9], v[8:9], v[16:17]
	v_pk_mul_f32 v[4:5], v[4:5], v[12:13]
	v_pk_mul_f32 v[8:9], v[8:9], v[24:25]
	v_pk_mul_f32 v[4:5], v[4:5], v[26:27]
	v_cvt_pk_fp8_f32 v14, v8, v9 op_sel:[0,0,1]
	v_cvt_pk_fp8_f32 v15, v4, v5 op_sel:[0,0,1]
	v_add_co_u32_e32 v2, vcc, 0x58000, v2
	s_nop 1
	v_addc_co_u32_e32 v3, vcc, 0, v3, vcc
	s_andn2_b64 vcc, exec, s[0:1]
	s_mov_b64 s[0:1], -1
	global_store_dwordx2 v[2:3], v[14:15], off
	s_cbranch_vccnz .LBB0_771
	s_andn2_b64 vcc, exec, s[12:13]
	s_cbranch_vccnz .LBB0_770
	s_branch .LBB0_770

.LBB0_853:
	s_lshl_b32 s0, s23, 3
	s_cmp_ge_i32 s69, s0
	v_readfirstlane_b32 s18, v0
	s_cbranch_scc1 .LBB0_872
	v_lshrrev_b32_e32 v1, 5, v0
	v_lshrrev_b32_e32 v2, 4, v0
	v_and_b32_e32 v5, 4, v1
	v_lshrrev_b32_e32 v1, 3, v0
	v_and_b32_e32 v3, 7, v0
	v_and_b32_e32 v4, 4, v2
	v_and_b32_e32 v6, 2, v1
	v_bitop3_b32 v6, v6, v3, v4 bitop3:0x36
	v_lshrrev_b32_e32 v7, 2, v0
	s_add_u32 s8, s2, 0x3e800000
	v_lshlrev_b32_e32 v204, 4, v6
	v_and_b32_e32 v6, 35, v1
	v_and_b32_e32 v7, 24, v7
	s_addc_u32 s9, s3, 0
	v_or3_b32 v6, v6, v7, v5
	s_add_u32 s25, s2, 0x22800000
	v_lshl_or_b32 v162, v6, 11, v204
	v_bitop3_b32 v6, v1, 2, 64 bitop3:0xc8
	s_addc_u32 s33, s3, 0
	v_bitop3_b32 v3, v6, v3, v4 bitop3:0x36
	s_movk_i32 s1, 0x63
	s_waitcnt lgkmcnt(0)
	s_ashr_i32 s52, s69, 31
	v_lshlrev_b32_e32 v206, 4, v3
	v_bitop3_b32 v3, v1, s1, 64 bitop3:0xc8
	s_lshr_b32 s1, s52, 29
	s_add_i32 s1, s69, s1
	s_lshr_b32 s19, s18, 6
	s_ashr_i32 s10, s1, 3
	s_and_b32 s1, s1, -8
	s_add_i32 s50, s23, 1
	s_lshr_b32 s20, s18, 8
	s_lshl_b32 s51, s19, 10
	s_sub_i32 s1, s69, s1
	s_cmp_lt_i32 s1, 0
	s_cselect_b32 s11, s50, s23
	s_mul_i32 s1, s11, s1
	s_add_i32 s1, s1, s10
	s_ashr_i32 s10, s1, 31
	s_lshr_b32 s10, s10, 26
	s_add_i32 s10, s1, s10
	s_ashr_i32 s11, s10, 6
	s_lshl_b32 s11, s11, 3
	s_sub_i32 s12, s23, s11
	s_min_i32 s12, s12, 8
	s_abs_i32 s13, s12
	v_cvt_f32_u32_e32 v4, s13
	v_or3_b32 v3, v3, v7, v5
	v_lshl_or_b32 v164, v3, 11, v206
	s_sub_i32 s15, 0, s13
	v_rcp_iflag_f32_e32 v3, v4
	s_andn2_b32 s10, s10, 63
	s_sub_i32 s1, s1, s10
	s_abs_i32 s14, s1
	v_mul_f32_e32 v3, 0x4f7ffffe, v3
	v_cvt_u32_f32_e32 v3, v3
	s_xor_b32 s10, s1, s12
	s_ashr_i32 s10, s10, 31
	v_or_b32_e32 v205, 64, v1
	v_readfirstlane_b32 s16, v3
	s_mul_i32 s15, s15, s16
	s_mul_hi_u32 s15, s16, s15
	s_add_i32 s16, s16, s15
	s_mul_hi_u32 s15, s14, s16
	s_mul_i32 s16, s15, s13
	s_sub_i32 s14, s14, s16
	s_add_i32 s16, s15, 1
	s_sub_i32 s17, s14, s13
	s_cmp_ge_u32 s14, s13
	s_cselect_b32 s15, s16, s15
	s_cselect_b32 s14, s17, s14
	s_add_i32 s16, s15, 1
	s_cmp_ge_u32 s14, s13
	s_cselect_b32 s13, s16, s15
	s_xor_b32 s13, s13, s10
	s_sub_i32 s40, s13, s10
	s_mul_i32 s10, s40, s12
	s_sub_i32 s1, s1, s10
	s_add_i32 s80, s11, s1
	s_add_i32 s1, s80, 0
	s_add_i32 s1, s1, 0x22200
	v_mov_b32_e32 v3, s1
	ds_read_u8 v3, v3
	v_lshl_or_b32 v207, v1, 11, v204
	v_lshl_or_b32 v208, v205, 11, v206
	v_mov_b32_e32 v167, 0
	v_mov_b32_e32 v163, v167
	s_waitcnt lgkmcnt(0)
	v_readfirstlane_b32 s42, v3
	s_ashr_i32 s43, s42, 31
	s_lshl_b64 s[10:11], s[42:43], 22
	s_add_u32 s1, s25, s10
	s_addc_u32 s12, s33, s11
	s_ashr_i32 s41, s40, 31
	s_lshl_b64 s[10:11], s[40:41], 19
	s_add_u32 s44, s1, s10
	s_addc_u32 s45, s12, s11
	v_mov_b32_e32 v3, 0x7f7f7f7f
	s_lshl_b32 s10, s80, 8
	s_add_i32 s41, s51, 0
	s_bitset1_b32 s10, 7
	s_add_i32 m0, s41, 0x10000
	s_lshl_b32 s1, s80, 19
	v_or_b32_e32 v3, s10, v1
	global_load_lds_dwordx4 v162, s[44:45]
	s_add_i32 m0, s41, 0x12000
	v_lshl_or_b32 v172, v3, 11, v204
	v_or_b32_e32 v3, s10, v205
	s_add_u32 s10, s44, 0x40000
	global_load_lds_dwordx4 v164, s[44:45]
	s_addc_u32 s11, s45, 0
	s_add_i32 m0, s41, 0x14000
	v_or_b32_e32 v166, s1, v207
	global_load_lds_dwordx4 v162, s[10:11]
	s_add_i32 m0, s41, 0x16000
	s_add_i32 s53, s41, 0x2000
	global_load_lds_dwordx4 v164, s[10:11]
	s_mov_b32 m0, s41
	v_or_b32_e32 v170, s1, v208
	global_load_lds_dwordx4 v166, s[8:9]
	s_mov_b32 m0, s53
	s_add_i32 s54, s41, 0x4000
	global_load_lds_dwordx4 v170, s[8:9]
	s_mov_b32 m0, s54
	s_add_i32 s55, s41, 0x6000
	v_lshl_or_b32 v174, v3, 11, v206
	v_lshl_add_u64 v[4:5], s[44:45], 0, v[162:163]
	global_load_lds_dwordx4 v172, s[8:9]
	s_mov_b32 m0, s55
	s_mov_b64 s[10:11], 0x80
	v_mov_b32_e32 v165, v167
	global_load_lds_dwordx4 v174, s[8:9]
	s_add_i32 m0, s41, 0x18000
	v_lshl_add_u64 v[4:5], v[4:5], 0, s[10:11]
	v_lshl_add_u64 v[6:7], s[44:45], 0, v[164:165]
	global_load_lds_dwordx4 v[4:5], off
	s_add_i32 m0, s41, 0x1a000
	v_lshl_add_u64 v[4:5], v[6:7], 0, s[10:11]
	s_add_u32 s12, s44, 0x40080
	global_load_lds_dwordx4 v[4:5], off
	s_addc_u32 s13, s45, 0
	s_add_i32 m0, s41, 0x1c000
	s_mov_b64 s[84:85], s[70:71]
	global_load_lds_dwordx4 v162, s[12:13]
	s_add_i32 m0, s41, 0x1e000
	s_cmp_eq_u32 s20, 1
	global_load_lds_dwordx4 v164, s[12:13]
	s_waitcnt vmcnt(6)
	s_mov_b32 s64, 0
	s_mov_b64 s[12:13], 0x40000
	s_cselect_b64 s[14:15], -1, 0
	s_cmp_lg_u32 s20, 1
	s_barrier
	s_cbranch_scc1 .LBB0_856
.LBB0_856:
	s_add_u32 s16, s2, 0x50800000
	v_lshrrev_b32_e32 v5, 1, v0
	s_addc_u32 s17, s3, 0
	v_and_b32_e32 v3, 15, v0
	v_and_b32_e32 v2, 3, v2
	v_and_b32_e32 v4, 2, v0
	v_and_b32_e32 v5, 4, v5
	s_lshl_b32 s19, s19, 5
	v_bitop3_b32 v4, v5, v2, v4 bitop3:0x36
	s_ashr_i32 s65, s94, 31
	s_ashr_i32 s1, s0, 31
	v_lshl_or_b32 v209, s20, 6, v3
	s_and_b32 s20, s19, 0x60
	v_lshlrev_b32_e32 v4, 4, v4
	v_lshlrev_b32_e32 v5, 7, v209
	v_or_b32_e32 v3, s20, v3
	s_cmpk_lt_u32 s18, 0x100
	v_or_b32_e32 v6, v5, v4
	v_lshlrev_b32_e32 v3, 7, v3
	v_bitop3_b32 v5, v5, 64, v4 bitop3:0x36
	s_cselect_b64 s[18:19], -1, 0
	v_lshl_or_b32 v212, v2, 3, s20
	s_add_u32 s20, s2, 0x3e800080
	v_or_b32_e32 v210, v3, v4
	v_bitop3_b32 v211, v3, 64, v4 bitop3:0x36
	s_addc_u32 s21, s3, 0
	v_mov_b64_e32 v[168:169], s[0:1]
	s_add_i32 s66, 0, 0x10000
	s_add_i32 s67, 0, 0x10800
	s_add_i32 s68, 0, 0x14000
	s_add_i32 s69, 0, 0x14800
	v_add_u32_e32 v213, 0, v6
	v_add_u32_e32 v214, 0, v5
	s_add_i32 s70, 0, 0x18000
	s_add_i32 s71, 0, 0x18800
	s_add_i32 s72, 0, 0x1c000
	s_add_i32 s73, 0, 0x1c800
	s_mov_b32 s22, 0x42800000
	s_mov_b32 s24, 0x3b000000
	s_mov_b32 s74, 0xc3e00000
	s_mov_b32 s75, 0x40000
	s_mov_b64 s[26:27], 0x48000
	s_mov_b32 s76, 0x48000
	s_mov_b64 s[28:29], 0x50000
	s_mov_b32 s77, 0x50000
	s_mov_b64 s[30:31], 0x58000
	s_mov_b32 s78, 0x58000
	v_mov_b32_e32 v215, 0x43e00000
	s_mov_b64 s[38:39], s[44:45]
	s_branch .LBB0_859

.LBB0_861:
	s_lshl_b32 s37, s79, 8
	s_bitset1_b32 s37, 7
	s_lshl_b32 s35, s79, 19
	v_or_b32_e32 v2, s37, v1
	v_or_b32_e32 v176, s35, v207
	v_lshl_or_b32 v178, v2, 11, v204
	v_or_b32_e32 v180, s35, v208
	v_or_b32_e32 v2, s37, v205
	v_mov_b32_e32 v171, v167
	v_mov_b32_e32 v173, v167
	v_mov_b32_e32 v175, v167
	s_add_u32 s35, s44, 0x100
	v_mov_b32_e32 v34, 0
	v_lshl_or_b32 v182, v2, 11, v206
	v_mov_b32_e32 v177, v167
	v_mov_b32_e32 v181, v167
	v_mov_b32_e32 v179, v167
	v_mov_b32_e32 v183, v167
	v_lshl_add_u64 v[184:185], s[20:21], 0, v[174:175]
	v_lshl_add_u64 v[186:187], s[20:21], 0, v[172:173]
	v_lshl_add_u64 v[188:189], s[20:21], 0, v[170:171]
	v_lshl_add_u64 v[190:191], s[20:21], 0, v[166:167]
	s_addc_u32 s37, s45, 0
	s_mov_b32 s43, -2
	s_mov_b64 s[44:45], 0
	v_mov_b32_e32 v35, v34
	v_mov_b32_e32 v36, v34
	v_mov_b32_e32 v37, v34
	v_mov_b32_e32 v38, v34
	v_mov_b32_e32 v39, v34
	v_mov_b32_e32 v40, v34
	v_mov_b32_e32 v41, v34
	v_mov_b32_e32 v42, v34
	v_mov_b32_e32 v43, v34
	v_mov_b32_e32 v44, v34
	v_mov_b32_e32 v45, v34
	v_mov_b32_e32 v46, v34
	v_mov_b32_e32 v47, v34
	v_mov_b32_e32 v48, v34
	v_mov_b32_e32 v49, v34
	v_mov_b32_e32 v50, v34
	v_mov_b32_e32 v51, v34
	v_mov_b32_e32 v52, v34
	v_mov_b32_e32 v53, v34
	v_mov_b32_e32 v54, v34
	v_mov_b32_e32 v55, v34
	v_mov_b32_e32 v56, v34
	v_mov_b32_e32 v57, v34
	v_mov_b32_e32 v58, v34
	v_mov_b32_e32 v59, v34
	v_mov_b32_e32 v60, v34
	v_mov_b32_e32 v61, v34
	v_mov_b32_e32 v62, v34
	v_mov_b32_e32 v63, v34
	v_mov_b32_e32 v64, v34
	v_mov_b32_e32 v65, v34
	v_mov_b32_e32 v90, v34
	v_mov_b32_e32 v91, v34
	v_mov_b32_e32 v92, v34
	v_mov_b32_e32 v93, v34
	v_mov_b32_e32 v98, v34
	v_mov_b32_e32 v99, v34
	v_mov_b32_e32 v100, v34
	v_mov_b32_e32 v101, v34
	v_mov_b32_e32 v106, v34
	v_mov_b32_e32 v107, v34
	v_mov_b32_e32 v108, v34
	v_mov_b32_e32 v109, v34
	v_mov_b32_e32 v110, v34
	v_mov_b32_e32 v111, v34
	v_mov_b32_e32 v112, v34
	v_mov_b32_e32 v113, v34
	v_mov_b32_e32 v114, v34
	v_mov_b32_e32 v115, v34
	v_mov_b32_e32 v116, v34
	v_mov_b32_e32 v117, v34
	v_mov_b32_e32 v118, v34
	v_mov_b32_e32 v119, v34
	v_mov_b32_e32 v120, v34
	v_mov_b32_e32 v121, v34
	v_mov_b32_e32 v122, v34
	v_mov_b32_e32 v123, v34
	v_mov_b32_e32 v124, v34
	v_mov_b32_e32 v125, v34
	v_mov_b32_e32 v126, v34
	v_mov_b32_e32 v127, v34
	v_mov_b32_e32 v128, v34
	v_mov_b32_e32 v129, v34
	v_mov_b32_e32 v66, v34
	v_mov_b32_e32 v67, v34
	v_mov_b32_e32 v68, v34
	v_mov_b32_e32 v69, v34
	v_mov_b32_e32 v70, v34
	v_mov_b32_e32 v71, v34
	v_mov_b32_e32 v72, v34
	v_mov_b32_e32 v73, v34
	v_mov_b32_e32 v74, v34
	v_mov_b32_e32 v75, v34
	v_mov_b32_e32 v76, v34
	v_mov_b32_e32 v77, v34
	v_mov_b32_e32 v78, v34
	v_mov_b32_e32 v79, v34
	v_mov_b32_e32 v80, v34
	v_mov_b32_e32 v81, v34
	v_mov_b32_e32 v82, v34
	v_mov_b32_e32 v83, v34
	v_mov_b32_e32 v84, v34
	v_mov_b32_e32 v85, v34
	v_mov_b32_e32 v86, v34
	v_mov_b32_e32 v87, v34
	v_mov_b32_e32 v88, v34
	v_mov_b32_e32 v89, v34
	v_mov_b32_e32 v94, v34
	v_mov_b32_e32 v95, v34
	v_mov_b32_e32 v96, v34
	v_mov_b32_e32 v97, v34
	v_mov_b32_e32 v102, v34
	v_mov_b32_e32 v103, v34
	v_mov_b32_e32 v104, v34
	v_mov_b32_e32 v105, v34
	v_mov_b32_e32 v130, v34
	v_mov_b32_e32 v131, v34
	v_mov_b32_e32 v132, v34
	v_mov_b32_e32 v133, v34
	v_mov_b32_e32 v134, v34
	v_mov_b32_e32 v135, v34
	v_mov_b32_e32 v136, v34
	v_mov_b32_e32 v137, v34
	v_mov_b32_e32 v138, v34
	v_mov_b32_e32 v139, v34
	v_mov_b32_e32 v140, v34
	v_mov_b32_e32 v141, v34
	v_mov_b32_e32 v142, v34
	v_mov_b32_e32 v143, v34
	v_mov_b32_e32 v144, v34
	v_mov_b32_e32 v145, v34
	v_mov_b32_e32 v146, v34
	v_mov_b32_e32 v147, v34
	v_mov_b32_e32 v148, v34
	v_mov_b32_e32 v149, v34
	v_mov_b32_e32 v150, v34
	v_mov_b32_e32 v151, v34
	v_mov_b32_e32 v152, v34
	v_mov_b32_e32 v153, v34
	v_mov_b32_e32 v154, v34
	v_mov_b32_e32 v155, v34
	v_mov_b32_e32 v156, v34
	v_mov_b32_e32 v157, v34
	v_mov_b32_e32 v158, v34
	v_mov_b32_e32 v159, v34
	v_mov_b32_e32 v160, v34
	v_mov_b32_e32 v161, v34
	s_andn2_b64 vcc, exec, s[14:15]
	s_cbranch_vccnz .Lp7_entry
	s_barrier
.Lp7_entry:
	s_branch .LBB0_863
.LBB0_862:
	s_add_u32 s48, s2, s44
	v_add_u32_e32 v2, s66, v210
	s_addc_u32 s49, s3, s45
	v_add_u32_e32 v3, s66, v211
	ds_read_b128 v[18:21], v2
	ds_read_b128 v[22:25], v3
	v_add_u32_e32 v2, s67, v210
	s_add_u32 s81, s48, 0x3e800100
	v_add_u32_e32 v3, s67, v211
	ds_read_b128 v[26:29], v2
	ds_read_b128 v[30:33], v3
	v_add_u32_e32 v2, s68, v210
	v_add_u32_e32 v6, s68, v211
	v_add_u32_e32 v10, s69, v210
	v_add_u32_e32 v14, s69, v211
	s_addc_u32 s82, s49, 0
	ds_read_b128 v[2:5], v2
	ds_read_b128 v[6:9], v6
	ds_read_b128 v[10:13], v10
	ds_read_b128 v[14:17], v14
	s_and_b64 s[48:49], s[46:47], exec
	s_cselect_b32 s49, s9, s82
	s_cselect_b32 s48, s8, s81
	s_add_u32 s81, s35, s44
	s_addc_u32 s82, s37, s45
	s_and_b64 s[46:47], s[46:47], exec
	s_cselect_b32 s47, s39, s82
	s_cselect_b32 s46, s38, s81
	v_lshl_add_u64 v[200:201], v[190:191], 0, s[44:45]
	s_add_i32 m0, s41, 0x8000
	ds_read_b128 v[220:223], v213
	ds_read_b128 v[228:231], v213 offset:2048
	ds_read_b128 v[224:227], v214
	ds_read_b128 v[232:235], v214 offset:2048
	ds_read_b128 v[236:239], v213 offset:4096
	ds_read_b128 v[244:247], v213 offset:6144
	ds_read_b128 v[240:243], v214 offset:4096
	ds_read_b128 v[248:251], v214 offset:6144
	global_load_lds_dwordx4 v[200:201], off
	v_lshl_add_u64 v[200:201], v[188:189], 0, s[44:45]
	s_add_i32 m0, s41, 0xa000
	s_nop 0
	global_load_lds_dwordx4 v[200:201], off
	v_lshl_add_u64 v[200:201], v[186:187], 0, s[44:45]
	s_add_i32 m0, s41, 0xc000
	s_nop 0
	global_load_lds_dwordx4 v[200:201], off
	v_lshl_add_u64 v[200:201], v[184:185], 0, s[44:45]
	s_add_i32 m0, s41, 0xe000
	s_nop 0
	global_load_lds_dwordx4 v[200:201], off
	s_waitcnt vmcnt(8)
	s_waitcnt lgkmcnt(0)
	s_barrier
	s_setprio 1
	s_waitcnt lgkmcnt(0)
	v_mfma_f32_16x16x128_f8f6f4 v[158:161], v[18:25], v[220:227], v[158:161]
	v_mfma_f32_16x16x128_f8f6f4 v[154:157], v[26:33], v[220:227], v[154:157]
	v_mfma_f32_16x16x128_f8f6f4 v[150:153], v[18:25], v[228:235], v[150:153]
	v_mfma_f32_16x16x128_f8f6f4 v[146:149], v[26:33], v[228:235], v[146:149]
	v_mfma_f32_16x16x128_f8f6f4 v[142:145], v[18:25], v[236:243], v[142:145]
	v_mfma_f32_16x16x128_f8f6f4 v[138:141], v[26:33], v[236:243], v[138:141]
	v_mfma_f32_16x16x128_f8f6f4 v[134:137], v[18:25], v[244:251], v[134:137]
	v_mfma_f32_16x16x128_f8f6f4 v[130:133], v[26:33], v[244:251], v[130:133]
	s_setprio 0
	s_setprio 1
	v_mfma_f32_16x16x128_f8f6f4 v[102:105], v[2:9], v[220:227], v[102:105]
	v_mfma_f32_16x16x128_f8f6f4 v[94:97], v[10:17], v[220:227], v[94:97]
	v_mfma_f32_16x16x128_f8f6f4 v[86:89], v[2:9], v[228:235], v[86:89]
	v_mfma_f32_16x16x128_f8f6f4 v[82:85], v[10:17], v[228:235], v[82:85]
	v_mfma_f32_16x16x128_f8f6f4 v[78:81], v[2:9], v[236:243], v[78:81]
	v_mfma_f32_16x16x128_f8f6f4 v[74:77], v[10:17], v[236:243], v[74:77]
	v_mfma_f32_16x16x128_f8f6f4 v[70:73], v[2:9], v[244:251], v[70:73]
	v_mfma_f32_16x16x128_f8f6f4 v[66:69], v[10:17], v[244:251], v[66:69]
	s_setprio 0
	s_barrier
	s_add_i32 s81, s66, s51
	v_lshl_add_u64 v[200:201], s[46:47], 0, v[162:163]
	s_mov_b32 m0, s81
	ds_read_b128 v[220:223], v213 offset:16384
	ds_read_b128 v[228:231], v213 offset:18432
	ds_read_b128 v[224:227], v214 offset:16384
	ds_read_b128 v[232:235], v214 offset:18432
	ds_read_b128 v[236:239], v213 offset:20480
	ds_read_b128 v[244:247], v213 offset:22528
	ds_read_b128 v[240:243], v214 offset:20480
	ds_read_b128 v[248:251], v214 offset:22528
	global_load_lds_dwordx4 v[200:201], off
	s_add_i32 m0, s81, 0x2000
	s_add_u32 s82, s46, 0x40000
	v_lshl_add_u64 v[202:203], s[46:47], 0, v[164:165]
	s_addc_u32 s83, s47, 0
	s_add_i32 s81, s68, s51
	global_load_lds_dwordx4 v[202:203], off
	v_lshl_add_u64 v[252:253], s[82:83], 0, v[162:163]
	s_mov_b32 m0, s81
	s_nop 0
	global_load_lds_dwordx4 v[252:253], off
	v_lshl_add_u64 v[252:253], s[82:83], 0, v[164:165]
	s_add_i32 m0, s81, 0x2000
	s_nop 0
	global_load_lds_dwordx4 v[252:253], off
	s_waitcnt vmcnt(6)
	s_waitcnt lgkmcnt(0)
	s_barrier
	s_setprio 1
	s_waitcnt lgkmcnt(0)
	v_mfma_f32_16x16x128_f8f6f4 v[126:129], v[18:25], v[220:227], v[126:129]
	v_mfma_f32_16x16x128_f8f6f4 v[122:125], v[26:33], v[220:227], v[122:125]
	v_mfma_f32_16x16x128_f8f6f4 v[118:121], v[18:25], v[228:235], v[118:121]
	v_mfma_f32_16x16x128_f8f6f4 v[114:117], v[26:33], v[228:235], v[114:117]
	v_mfma_f32_16x16x128_f8f6f4 v[110:113], v[18:25], v[236:243], v[110:113]
	v_mfma_f32_16x16x128_f8f6f4 v[106:109], v[26:33], v[236:243], v[106:109]
	v_mfma_f32_16x16x128_f8f6f4 v[98:101], v[18:25], v[244:251], v[98:101]
	v_mfma_f32_16x16x128_f8f6f4 v[90:93], v[26:33], v[244:251], v[90:93]
	s_setprio 0
	s_setprio 1
	v_mfma_f32_16x16x128_f8f6f4 v[62:65], v[2:9], v[220:227], v[62:65]
	v_mfma_f32_16x16x128_f8f6f4 v[58:61], v[10:17], v[220:227], v[58:61]
	v_mfma_f32_16x16x128_f8f6f4 v[54:57], v[2:9], v[228:235], v[54:57]
	v_mfma_f32_16x16x128_f8f6f4 v[50:53], v[10:17], v[228:235], v[50:53]
	v_mfma_f32_16x16x128_f8f6f4 v[46:49], v[2:9], v[236:243], v[46:49]
	v_mfma_f32_16x16x128_f8f6f4 v[42:45], v[10:17], v[236:243], v[42:45]
	v_mfma_f32_16x16x128_f8f6f4 v[38:41], v[2:9], v[244:251], v[38:41]
	v_mfma_f32_16x16x128_f8f6f4 v[34:37], v[10:17], v[244:251], v[34:37]
	s_setprio 0
	s_barrier
	v_add_u32_e32 v2, s70, v210
	v_add_u32_e32 v6, s70, v211
	v_add_u32_e32 v10, s71, v210
	v_add_u32_e32 v14, s71, v211
	v_add_u32_e32 v18, s72, v210
	v_add_u32_e32 v22, s72, v211
	v_add_u32_e32 v26, s73, v210
	v_add_u32_e32 v30, s73, v211
	ds_read_b128 v[2:5], v2
	ds_read_b128 v[6:9], v6
	ds_read_b128 v[10:13], v10
	ds_read_b128 v[14:17], v14
	ds_read_b128 v[18:21], v18
	ds_read_b128 v[22:25], v22
	ds_read_b128 v[26:29], v26
	ds_read_b128 v[30:33], v30
	s_mov_b32 m0, s41
	v_lshl_add_u64 v[198:199], s[48:49], 0, v[198:199]
	ds_read_b128 v[220:223], v213 offset:32768
	ds_read_b128 v[228:231], v213 offset:34816
	ds_read_b128 v[224:227], v214 offset:32768
	ds_read_b128 v[232:235], v214 offset:34816
	ds_read_b128 v[236:239], v213 offset:36864
	ds_read_b128 v[244:247], v213 offset:38912
	ds_read_b128 v[240:243], v214 offset:36864
	ds_read_b128 v[248:251], v214 offset:38912
	global_load_lds_dwordx4 v[198:199], off
	v_lshl_add_u64 v[196:197], s[48:49], 0, v[196:197]
	s_mov_b32 m0, s53
	v_lshl_add_u64 v[194:195], s[48:49], 0, v[194:195]
	global_load_lds_dwordx4 v[196:197], off
	s_mov_b32 m0, s54
	v_lshl_add_u64 v[192:193], s[48:49], 0, v[192:193]
	global_load_lds_dwordx4 v[194:195], off
	s_mov_b32 m0, s55
	s_nop 0
	global_load_lds_dwordx4 v[192:193], off
	s_waitcnt vmcnt(8)
	s_waitcnt lgkmcnt(0)
	s_barrier
	s_setprio 1
	s_waitcnt lgkmcnt(0)
	v_mfma_f32_16x16x128_f8f6f4 v[158:161], v[2:9], v[220:227], v[158:161]
	v_mfma_f32_16x16x128_f8f6f4 v[154:157], v[10:17], v[220:227], v[154:157]
	v_mfma_f32_16x16x128_f8f6f4 v[150:153], v[2:9], v[228:235], v[150:153]
	v_mfma_f32_16x16x128_f8f6f4 v[146:149], v[10:17], v[228:235], v[146:149]
	v_mfma_f32_16x16x128_f8f6f4 v[142:145], v[2:9], v[236:243], v[142:145]
	v_mfma_f32_16x16x128_f8f6f4 v[138:141], v[10:17], v[236:243], v[138:141]
	v_mfma_f32_16x16x128_f8f6f4 v[134:137], v[2:9], v[244:251], v[134:137]
	v_mfma_f32_16x16x128_f8f6f4 v[130:133], v[10:17], v[244:251], v[130:133]
	s_setprio 0
	s_setprio 1
	v_mfma_f32_16x16x128_f8f6f4 v[102:105], v[18:25], v[220:227], v[102:105]
	v_mfma_f32_16x16x128_f8f6f4 v[94:97], v[26:33], v[220:227], v[94:97]
	v_mfma_f32_16x16x128_f8f6f4 v[86:89], v[18:25], v[228:235], v[86:89]
	v_mfma_f32_16x16x128_f8f6f4 v[82:85], v[26:33], v[228:235], v[82:85]
	v_mfma_f32_16x16x128_f8f6f4 v[78:81], v[18:25], v[236:243], v[78:81]
	v_mfma_f32_16x16x128_f8f6f4 v[74:77], v[26:33], v[236:243], v[74:77]
	v_mfma_f32_16x16x128_f8f6f4 v[70:73], v[18:25], v[244:251], v[70:73]
	v_mfma_f32_16x16x128_f8f6f4 v[66:69], v[26:33], v[244:251], v[66:69]
	s_setprio 0
	s_barrier
	s_add_i32 s48, s70, s51
	v_lshl_add_u64 v[200:201], v[200:201], 0, s[10:11]
	s_mov_b32 m0, s48
	ds_read_b128 v[192:195], v213 offset:49152
	ds_read_b128 v[220:223], v213 offset:51200
	ds_read_b128 v[196:199], v214 offset:49152
	ds_read_b128 v[224:227], v214 offset:51200
	ds_read_b128 v[228:231], v213 offset:53248
	ds_read_b128 v[236:239], v213 offset:55296
	ds_read_b128 v[232:235], v214 offset:53248
	ds_read_b128 v[240:243], v214 offset:55296
	global_load_lds_dwordx4 v[200:201], off
	s_add_i32 m0, s48, 0x2000
	s_add_u32 s46, s46, 0x40080
	v_lshl_add_u64 v[200:201], v[202:203], 0, s[10:11]
	s_addc_u32 s47, s47, 0
	s_add_i32 s48, s72, s51
	global_load_lds_dwordx4 v[200:201], off
	v_lshl_add_u64 v[200:201], s[46:47], 0, v[162:163]
	s_mov_b32 m0, s48
	s_nop 0
	global_load_lds_dwordx4 v[200:201], off
	v_lshl_add_u64 v[200:201], s[46:47], 0, v[164:165]
	s_add_i32 m0, s48, 0x2000
	s_nop 0
	global_load_lds_dwordx4 v[200:201], off
	s_waitcnt vmcnt(6)
	s_waitcnt lgkmcnt(0)
	s_barrier
	s_setprio 1
	s_waitcnt lgkmcnt(0)
	v_mfma_f32_16x16x128_f8f6f4 v[126:129], v[2:9], v[192:199], v[126:129]
	v_mfma_f32_16x16x128_f8f6f4 v[122:125], v[10:17], v[192:199], v[122:125]
	v_mfma_f32_16x16x128_f8f6f4 v[118:121], v[2:9], v[220:227], v[118:121]
	v_mfma_f32_16x16x128_f8f6f4 v[114:117], v[10:17], v[220:227], v[114:117]
	v_mfma_f32_16x16x128_f8f6f4 v[110:113], v[2:9], v[228:235], v[110:113]
	v_mfma_f32_16x16x128_f8f6f4 v[106:109], v[10:17], v[228:235], v[106:109]
	v_mfma_f32_16x16x128_f8f6f4 v[98:101], v[2:9], v[236:243], v[98:101]
	v_mfma_f32_16x16x128_f8f6f4 v[90:93], v[10:17], v[236:243], v[90:93]
	s_setprio 0
	s_setprio 1
	v_mfma_f32_16x16x128_f8f6f4 v[62:65], v[18:25], v[192:199], v[62:65]
	v_mfma_f32_16x16x128_f8f6f4 v[58:61], v[26:33], v[192:199], v[58:61]
	v_mfma_f32_16x16x128_f8f6f4 v[54:57], v[18:25], v[220:227], v[54:57]
	v_mfma_f32_16x16x128_f8f6f4 v[50:53], v[26:33], v[220:227], v[50:53]
	v_mfma_f32_16x16x128_f8f6f4 v[46:49], v[18:25], v[228:235], v[46:49]
	v_mfma_f32_16x16x128_f8f6f4 v[42:45], v[26:33], v[228:235], v[42:45]
	v_mfma_f32_16x16x128_f8f6f4 v[38:41], v[18:25], v[236:243], v[38:41]
	v_mfma_f32_16x16x128_f8f6f4 v[34:37], v[26:33], v[236:243], v[34:37]
	s_setprio 0
	s_barrier
	s_add_i32 s43, s43, 2
	s_add_u32 s44, s44, 0x100
	s_addc_u32 s45, s45, 0
	s_cmp_gt_u32 s43, 13
	s_cbranch_scc1 .LBB0_866

.LBB0_866:
	s_ashr_i32 s43, s42, 31
	s_lshl_b64 s[42:43], s[42:43], 13
	v_lshl_or_b32 v18, s40, 8, v212
	s_add_u32 s42, s56, s42
	s_addc_u32 s43, s57, s43
	v_ashrrev_i32_e32 v19, 31, v18
	v_lshl_add_u64 v[2:3], v[18:19], 2, s[42:43]
	global_load_dwordx4 v[10:13], v[2:3], off
	global_load_dwordx4 v[14:17], v[2:3], off offset:16
	s_and_b64 vcc, exec, s[18:19]
	s_cbranch_vccz .LBB0_868
	s_barrier
.LBB0_868:
	s_nop 15
	s_nop 15
	v_lshl_add_u32 v20, s80, 8, v209
	v_ashrrev_i32_e32 v21, 31, v20
	v_or_b32_e32 v4, 16, v20
	v_or_b32_e32 v6, 32, v20
	v_lshlrev_b64 v[8:9], 11, v[20:21]
	v_ashrrev_i32_e32 v5, 31, v4
	v_ashrrev_i32_e32 v7, 31, v6
	v_lshl_add_u64 v[8:9], s[16:17], 0, v[8:9]
	v_lshlrev_b64 v[30:31], 11, v[4:5]
	v_lshlrev_b64 v[6:7], 11, v[6:7]
	v_lshl_add_u64 v[4:5], v[8:9], 0, v[18:19]
	v_lshl_add_u64 v[8:9], s[16:17], 0, v[30:31]
	v_lshl_add_u64 v[30:31], s[16:17], 0, v[6:7]
	v_lshl_add_u64 v[6:7], v[8:9], 0, v[18:19]
	v_lshl_add_u64 v[8:9], v[30:31], 0, v[18:19]
	v_mov_b32_e32 v22, 0
	v_mov_b32_e32 v23, 0
	v_mov_b32_e32 v24, 0
	v_mov_b32_e32 v25, 0
	v_mov_b32_e32 v26, 0
	v_mov_b32_e32 v27, 0
	v_mov_b32_e32 v28, 0
	s_waitcnt vmcnt(0)
	v_pk_mul_f32 v[30:31], v[10:11], s[22:23] op_sel_hi:[1,0]
	s_nop 0
	v_pk_fma_f32 v[32:33], v[158:159], s[24:25], v[30:31] op_sel_hi:[1,0,1]
	v_pk_mul_f32 v[12:13], v[12:13], s[22:23] op_sel_hi:[1,0]
	v_med3_f32 v21, v32, s74, v215
	v_med3_f32 v29, v33, s74, v215
	v_cvt_pk_fp8_f32 v22, v21, v29
	v_pk_mul_f32 v[14:15], v[14:15], s[22:23] op_sel_hi:[1,0]
	v_pk_fma_f32 v[10:11], v[160:161], s[24:25], v[12:13] op_sel_hi:[1,0,1]
	v_pk_fma_f32 v[130:131], v[130:131], s[24:25], v[14:15] op_sel_hi:[1,0,1]
	v_med3_f32 v10, v10, s74, v215
	v_med3_f32 v11, v11, s74, v215
	v_pk_fma_f32 v[154:155], v[154:155], s[24:25], v[14:15] op_sel_hi:[1,0,1]
	v_med3_f32 v130, v130, s74, v215
	v_cvt_pk_fp8_f32 v22, v10, v11 op_sel:[0,0,1]
	v_med3_f32 v10, v131, s74, v215
	v_mov_b32_e32 v29, 0
	v_pk_fma_f32 v[150:151], v[150:151], s[24:25], v[30:31] op_sel_hi:[1,0,1]
	v_pk_fma_f32 v[146:147], v[146:147], s[24:25], v[14:15] op_sel_hi:[1,0,1]
	v_med3_f32 v32, v154, s74, v215
	v_med3_f32 v33, v155, s74, v215
	v_cvt_pk_fp8_f32 v29, v130, v10
	v_pk_mul_f32 v[16:17], v[16:17], s[22:23] op_sel_hi:[1,0]
	v_pk_fma_f32 v[142:143], v[142:143], s[24:25], v[30:31] op_sel_hi:[1,0,1]
	v_pk_fma_f32 v[138:139], v[138:139], s[24:25], v[14:15] op_sel_hi:[1,0,1]
	v_med3_f32 v150, v150, s74, v215
	v_med3_f32 v151, v151, s74, v215
	v_med3_f32 v146, v146, s74, v215
	v_med3_f32 v147, v147, s74, v215
	v_cvt_pk_fp8_f32 v23, v32, v33
	v_pk_fma_f32 v[132:133], v[132:133], s[24:25], v[16:17] op_sel_hi:[1,0,1]
	v_med3_f32 v142, v142, s74, v215
	v_med3_f32 v143, v143, s74, v215
	v_med3_f32 v138, v138, s74, v215
	v_med3_f32 v139, v139, s74, v215
	v_cvt_pk_fp8_f32 v24, v150, v151
	v_cvt_pk_fp8_f32 v25, v146, v147
	v_pk_fma_f32 v[156:157], v[156:157], s[24:25], v[16:17] op_sel_hi:[1,0,1]
	v_cvt_pk_fp8_f32 v26, v142, v143
	v_cvt_pk_fp8_f32 v27, v138, v139
	v_med3_f32 v10, v132, s74, v215
	v_med3_f32 v11, v133, s74, v215
	v_pk_fma_f32 v[152:153], v[152:153], s[24:25], v[12:13] op_sel_hi:[1,0,1]
	v_pk_fma_f32 v[148:149], v[148:149], s[24:25], v[16:17] op_sel_hi:[1,0,1]
	v_med3_f32 v154, v156, s74, v215
	v_med3_f32 v155, v157, s74, v215
	v_cvt_pk_fp8_f32 v29, v10, v11 op_sel:[0,0,1]
	v_or_b32_e32 v10, 48, v20
	v_pk_fma_f32 v[144:145], v[144:145], s[24:25], v[12:13] op_sel_hi:[1,0,1]
	v_pk_fma_f32 v[140:141], v[140:141], s[24:25], v[16:17] op_sel_hi:[1,0,1]
	v_med3_f32 v152, v152, s74, v215
	v_med3_f32 v153, v153, s74, v215
	v_med3_f32 v148, v148, s74, v215
	v_med3_f32 v149, v149, s74, v215
	v_cvt_pk_fp8_f32 v23, v154, v155 op_sel:[0,0,1]
	v_ashrrev_i32_e32 v11, 31, v10
	v_med3_f32 v144, v144, s74, v215
	v_med3_f32 v145, v145, s74, v215
	v_med3_f32 v140, v140, s74, v215
	v_med3_f32 v141, v141, s74, v215
	v_cvt_pk_fp8_f32 v24, v152, v153 op_sel:[0,0,1]
	v_cvt_pk_fp8_f32 v25, v148, v149 op_sel:[0,0,1]
	v_lshlrev_b64 v[10:11], 11, v[10:11]
	v_cvt_pk_fp8_f32 v26, v144, v145 op_sel:[0,0,1]
	v_cvt_pk_fp8_f32 v27, v140, v141 op_sel:[0,0,1]
	v_lshl_add_u64 v[10:11], s[16:17], 0, v[10:11]
	v_lshl_add_u64 v[10:11], v[10:11], 0, v[18:19]
	v_pk_fma_f32 v[18:19], v[128:129], s[24:25], v[12:13] op_sel_hi:[1,0,1]
	v_pk_fma_f32 v[20:21], v[126:127], s[24:25], v[30:31] op_sel_hi:[1,0,1]
	global_store_dwordx2 v[4:5], v[22:23], off
	global_store_dwordx2 v[6:7], v[24:25], off
	global_store_dwordx2 v[8:9], v[26:27], off
	v_pk_fma_f32 v[24:25], v[122:123], s[24:25], v[14:15] op_sel_hi:[1,0,1]
	v_med3_f32 v20, v20, s74, v215
	v_med3_f32 v21, v21, s74, v215
	v_med3_f32 v26, v18, s74, v215
	v_mov_b32_e32 v18, 0
	v_med3_f32 v27, v19, s74, v215
	v_cvt_pk_fp8_f32 v18, v20, v21
	v_med3_f32 v20, v24, s74, v215
	v_med3_f32 v21, v25, s74, v215
	v_mov_b32_e32 v19, 0
	v_cvt_pk_fp8_f32 v19, v20, v21
	v_pk_fma_f32 v[22:23], v[124:125], s[24:25], v[16:17] op_sel_hi:[1,0,1]
	v_cvt_pk_fp8_f32 v18, v26, v27 op_sel:[0,0,1]
	v_med3_f32 v20, v22, s74, v215
	v_med3_f32 v21, v23, s74, v215
	v_cvt_pk_fp8_f32 v19, v20, v21 op_sel:[0,0,1]
	v_add_co_u32_e32 v20, vcc, s75, v4
	v_pk_fma_f32 v[24:25], v[114:115], s[24:25], v[14:15] op_sel_hi:[1,0,1]
	s_nop 0
	v_addc_co_u32_e32 v21, vcc, 0, v5, vcc
	global_store_dwordx2 v[20:21], v[18:19], off
	v_pk_fma_f32 v[18:19], v[120:121], s[24:25], v[12:13] op_sel_hi:[1,0,1]
	v_pk_fma_f32 v[20:21], v[118:119], s[24:25], v[30:31] op_sel_hi:[1,0,1]
	v_med3_f32 v26, v18, s74, v215
	v_med3_f32 v20, v20, s74, v215
	v_med3_f32 v21, v21, s74, v215
	v_mov_b32_e32 v18, 0
	v_med3_f32 v27, v19, s74, v215
	v_cvt_pk_fp8_f32 v18, v20, v21
	v_med3_f32 v20, v24, s74, v215
	v_med3_f32 v21, v25, s74, v215
	v_mov_b32_e32 v19, 0
	v_cvt_pk_fp8_f32 v19, v20, v21
	v_pk_fma_f32 v[22:23], v[116:117], s[24:25], v[16:17] op_sel_hi:[1,0,1]
	v_cvt_pk_fp8_f32 v18, v26, v27 op_sel:[0,0,1]
	v_med3_f32 v20, v22, s74, v215
	v_med3_f32 v21, v23, s74, v215
	v_cvt_pk_fp8_f32 v19, v20, v21 op_sel:[0,0,1]
	v_add_co_u32_e32 v20, vcc, s76, v4
	v_pk_fma_f32 v[24:25], v[106:107], s[24:25], v[14:15] op_sel_hi:[1,0,1]
	s_nop 0
	v_addc_co_u32_e32 v21, vcc, 0, v5, vcc
	global_store_dwordx2 v[20:21], v[18:19], off
	v_pk_fma_f32 v[18:19], v[112:113], s[24:25], v[12:13] op_sel_hi:[1,0,1]
	v_pk_fma_f32 v[20:21], v[110:111], s[24:25], v[30:31] op_sel_hi:[1,0,1]
	v_med3_f32 v26, v18, s74, v215
	v_med3_f32 v20, v20, s74, v215
	v_med3_f32 v21, v21, s74, v215
	v_mov_b32_e32 v18, 0
	v_med3_f32 v27, v19, s74, v215
	v_cvt_pk_fp8_f32 v18, v20, v21
	v_med3_f32 v20, v24, s74, v215
	v_med3_f32 v21, v25, s74, v215
	v_mov_b32_e32 v19, 0
	v_cvt_pk_fp8_f32 v19, v20, v21
	v_pk_fma_f32 v[22:23], v[108:109], s[24:25], v[16:17] op_sel_hi:[1,0,1]
	v_cvt_pk_fp8_f32 v18, v26, v27 op_sel:[0,0,1]
	v_med3_f32 v20, v22, s74, v215
	v_med3_f32 v21, v23, s74, v215
	v_cvt_pk_fp8_f32 v19, v20, v21 op_sel:[0,0,1]
	v_add_co_u32_e32 v20, vcc, s77, v4
	v_pk_fma_f32 v[136:137], v[136:137], s[24:25], v[12:13] op_sel_hi:[1,0,1]
	s_nop 0
	v_addc_co_u32_e32 v21, vcc, 0, v5, vcc
	v_pk_fma_f32 v[134:135], v[134:135], s[24:25], v[30:31] op_sel_hi:[1,0,1]
	global_store_dwordx2 v[20:21], v[18:19], off
	v_pk_fma_f32 v[12:13], v[100:101], s[24:25], v[12:13] op_sel_hi:[1,0,1]
	v_pk_fma_f32 v[18:19], v[98:99], s[24:25], v[30:31] op_sel_hi:[1,0,1]
	v_pk_fma_f32 v[14:15], v[90:91], s[24:25], v[14:15] op_sel_hi:[1,0,1]
	v_med3_f32 v134, v134, s74, v215
	v_med3_f32 v135, v135, s74, v215
	v_med3_f32 v18, v18, s74, v215
	v_med3_f32 v19, v19, s74, v215
	v_med3_f32 v20, v12, s74, v215
	v_med3_f32 v21, v13, s74, v215
	v_mov_b32_e32 v12, 0
	v_med3_f32 v14, v14, s74, v215
	v_med3_f32 v15, v15, s74, v215
	v_mov_b32_e32 v13, 0
	v_cvt_pk_fp8_f32 v28, v134, v135
	v_cvt_pk_fp8_f32 v12, v18, v19
	v_cvt_pk_fp8_f32 v13, v14, v15
	v_pk_fma_f32 v[16:17], v[92:93], s[24:25], v[16:17] op_sel_hi:[1,0,1]
	v_med3_f32 v136, v136, s74, v215
	v_med3_f32 v137, v137, s74, v215
	v_med3_f32 v14, v16, s74, v215
	v_med3_f32 v15, v17, s74, v215
	v_cvt_pk_fp8_f32 v28, v136, v137 op_sel:[0,0,1]
	v_cvt_pk_fp8_f32 v12, v20, v21 op_sel:[0,0,1]
	v_cvt_pk_fp8_f32 v13, v14, v15 op_sel:[0,0,1]
	v_add_co_u32_e32 v14, vcc, s78, v4
	global_store_dwordx2 v[10:11], v[28:29], off
	s_nop 0
	v_addc_co_u32_e32 v15, vcc, 0, v5, vcc
	global_store_dwordx2 v[14:15], v[12:13], off
	global_load_dwordx4 v[12:15], v[2:3], off offset:512
	s_nop 0
	global_load_dwordx4 v[16:19], v[2:3], off offset:528
	v_lshl_add_u64 v[2:3], v[4:5], 0, s[12:13]
	v_lshl_add_u64 v[20:21], v[4:5], 0, s[26:27]
	v_lshl_add_u64 v[22:23], v[4:5], 0, s[28:29]
	v_lshl_add_u64 v[24:25], v[4:5], 0, s[30:31]
	s_andn2_b64 vcc, exec, s[0:1]
	s_mov_b64 s[0:1], -1
	s_waitcnt vmcnt(1)
	v_pk_mul_f32 v[14:15], v[14:15], s[22:23] op_sel_hi:[1,0]
	v_pk_mul_f32 v[12:13], v[12:13], s[22:23] op_sel_hi:[1,0]
	s_waitcnt vmcnt(0)
	v_pk_mul_f32 v[16:17], v[16:17], s[22:23] op_sel_hi:[1,0]
	v_pk_fma_f32 v[26:27], v[104:105], s[24:25], v[14:15] op_sel_hi:[1,0,1]
	v_pk_fma_f32 v[28:29], v[102:103], s[24:25], v[12:13] op_sel_hi:[1,0,1]
	v_pk_fma_f32 v[32:33], v[94:95], s[24:25], v[16:17] op_sel_hi:[1,0,1]
	v_med3_f32 v28, v28, s74, v215
	v_med3_f32 v29, v29, s74, v215
	v_med3_f32 v90, v26, s74, v215
	v_mov_b32_e32 v26, 0
	v_med3_f32 v91, v27, s74, v215
	v_cvt_pk_fp8_f32 v26, v28, v29
	v_med3_f32 v28, v32, s74, v215
	v_med3_f32 v29, v33, s74, v215
	v_mov_b32_e32 v27, 0
	v_cvt_pk_fp8_f32 v27, v28, v29
	v_pk_mul_f32 v[18:19], v[18:19], s[22:23] op_sel_hi:[1,0]
	v_pk_fma_f32 v[82:83], v[82:83], s[24:25], v[16:17] op_sel_hi:[1,0,1]
	v_pk_fma_f32 v[30:31], v[96:97], s[24:25], v[18:19] op_sel_hi:[1,0,1]
	v_pk_fma_f32 v[32:33], v[84:85], s[24:25], v[18:19] op_sel_hi:[1,0,1]
	v_med3_f32 v28, v30, s74, v215
	v_med3_f32 v29, v31, s74, v215
	v_cvt_pk_fp8_f32 v27, v28, v29 op_sel:[0,0,1]
	v_pk_fma_f32 v[28:29], v[88:89], s[24:25], v[14:15] op_sel_hi:[1,0,1]
	v_pk_fma_f32 v[30:31], v[86:87], s[24:25], v[12:13] op_sel_hi:[1,0,1]
	v_med3_f32 v84, v28, s74, v215
	v_med3_f32 v30, v30, s74, v215
	v_med3_f32 v31, v31, s74, v215
	v_mov_b32_e32 v28, 0
	v_med3_f32 v85, v29, s74, v215
	v_cvt_pk_fp8_f32 v28, v30, v31
	v_med3_f32 v30, v82, s74, v215
	v_med3_f32 v31, v83, s74, v215
	v_mov_b32_e32 v29, 0
	v_cvt_pk_fp8_f32 v29, v30, v31
	v_med3_f32 v30, v32, s74, v215
	v_med3_f32 v31, v33, s74, v215
	v_pk_fma_f32 v[32:33], v[78:79], s[24:25], v[12:13] op_sel_hi:[1,0,1]
	v_cvt_pk_fp8_f32 v29, v30, v31 op_sel:[0,0,1]
	v_pk_fma_f32 v[30:31], v[80:81], s[24:25], v[14:15] op_sel_hi:[1,0,1]
	v_pk_fma_f32 v[74:75], v[74:75], s[24:25], v[16:17] op_sel_hi:[1,0,1]
	v_med3_f32 v32, v32, s74, v215
	v_med3_f32 v33, v33, s74, v215
	v_med3_f32 v78, v30, s74, v215
	v_mov_b32_e32 v30, 0
	v_med3_f32 v79, v31, s74, v215
	v_cvt_pk_fp8_f32 v30, v32, v33
	v_med3_f32 v32, v74, s74, v215
	v_med3_f32 v33, v75, s74, v215
	v_mov_b32_e32 v31, 0
	v_cvt_pk_fp8_f32 v31, v32, v33
	v_pk_fma_f32 v[76:77], v[76:77], s[24:25], v[18:19] op_sel_hi:[1,0,1]
	v_pk_fma_f32 v[70:71], v[70:71], s[24:25], v[12:13] op_sel_hi:[1,0,1]
	v_med3_f32 v32, v76, s74, v215
	v_med3_f32 v33, v77, s74, v215
	v_cvt_pk_fp8_f32 v31, v32, v33 op_sel:[0,0,1]
	v_pk_fma_f32 v[32:33], v[72:73], s[24:25], v[14:15] op_sel_hi:[1,0,1]
	v_pk_fma_f32 v[66:67], v[66:67], s[24:25], v[16:17] op_sel_hi:[1,0,1]
	v_med3_f32 v70, v70, s74, v215
	v_med3_f32 v71, v71, s74, v215
	v_med3_f32 v72, v32, s74, v215
	v_med3_f32 v73, v33, s74, v215
	v_mov_b32_e32 v32, 0
	v_med3_f32 v66, v66, s74, v215
	v_med3_f32 v67, v67, s74, v215
	v_mov_b32_e32 v33, 0
	v_cvt_pk_fp8_f32 v32, v70, v71
	v_cvt_pk_fp8_f32 v33, v66, v67
	v_cvt_pk_fp8_f32 v26, v90, v91 op_sel:[0,0,1]
	v_cvt_pk_fp8_f32 v28, v84, v85 op_sel:[0,0,1]
	v_pk_fma_f32 v[68:69], v[68:69], s[24:25], v[18:19] op_sel_hi:[1,0,1]
	v_cvt_pk_fp8_f32 v30, v78, v79 op_sel:[0,0,1]
	v_med3_f32 v66, v68, s74, v215
	v_med3_f32 v67, v69, s74, v215
	v_cvt_pk_fp8_f32 v32, v72, v73 op_sel:[0,0,1]
	v_cvt_pk_fp8_f32 v33, v66, v67 op_sel:[0,0,1]
	global_store_dwordx2 v[4:5], v[26:27], off offset:128
	global_store_dwordx2 v[6:7], v[28:29], off offset:128
	global_store_dwordx2 v[8:9], v[30:31], off offset:128
	global_store_dwordx2 v[10:11], v[32:33], off offset:128
	v_pk_fma_f32 v[4:5], v[64:65], s[24:25], v[14:15] op_sel_hi:[1,0,1]
	v_pk_fma_f32 v[6:7], v[62:63], s[24:25], v[12:13] op_sel_hi:[1,0,1]
	v_pk_fma_f32 v[10:11], v[58:59], s[24:25], v[16:17] op_sel_hi:[1,0,1]
	v_med3_f32 v6, v6, s74, v215
	v_med3_f32 v7, v7, s74, v215
	v_med3_f32 v26, v4, s74, v215
	v_mov_b32_e32 v4, 0
	v_med3_f32 v27, v5, s74, v215
	v_cvt_pk_fp8_f32 v4, v6, v7
	v_med3_f32 v6, v10, s74, v215
	v_med3_f32 v7, v11, s74, v215
	v_mov_b32_e32 v5, 0
	v_cvt_pk_fp8_f32 v5, v6, v7
	v_pk_fma_f32 v[8:9], v[60:61], s[24:25], v[18:19] op_sel_hi:[1,0,1]
	v_cvt_pk_fp8_f32 v4, v26, v27 op_sel:[0,0,1]
	v_med3_f32 v6, v8, s74, v215
	v_med3_f32 v7, v9, s74, v215
	v_cvt_pk_fp8_f32 v5, v6, v7 op_sel:[0,0,1]
	v_pk_fma_f32 v[6:7], v[56:57], s[24:25], v[14:15] op_sel_hi:[1,0,1]
	v_pk_fma_f32 v[8:9], v[54:55], s[24:25], v[12:13] op_sel_hi:[1,0,1]
	v_pk_fma_f32 v[26:27], v[50:51], s[24:25], v[16:17] op_sel_hi:[1,0,1]
	v_med3_f32 v8, v8, s74, v215
	v_med3_f32 v9, v9, s74, v215
	v_med3_f32 v28, v6, s74, v215
	v_mov_b32_e32 v6, 0
	v_med3_f32 v29, v7, s74, v215
	v_cvt_pk_fp8_f32 v6, v8, v9
	v_med3_f32 v8, v26, s74, v215
	v_med3_f32 v9, v27, s74, v215
	v_mov_b32_e32 v7, 0
	v_cvt_pk_fp8_f32 v7, v8, v9
	v_pk_fma_f32 v[10:11], v[52:53], s[24:25], v[18:19] op_sel_hi:[1,0,1]
	v_cvt_pk_fp8_f32 v6, v28, v29 op_sel:[0,0,1]
	v_med3_f32 v8, v10, s74, v215
	v_med3_f32 v9, v11, s74, v215
	v_cvt_pk_fp8_f32 v7, v8, v9 op_sel:[0,0,1]
	v_pk_fma_f32 v[8:9], v[48:49], s[24:25], v[14:15] op_sel_hi:[1,0,1]
	v_pk_fma_f32 v[10:11], v[46:47], s[24:25], v[12:13] op_sel_hi:[1,0,1]
	v_pk_fma_f32 v[28:29], v[42:43], s[24:25], v[16:17] op_sel_hi:[1,0,1]
	v_med3_f32 v10, v10, s74, v215
	v_med3_f32 v11, v11, s74, v215
	v_med3_f32 v30, v8, s74, v215
	v_mov_b32_e32 v8, 0
	v_med3_f32 v31, v9, s74, v215
	v_cvt_pk_fp8_f32 v8, v10, v11
	v_med3_f32 v10, v28, s74, v215
	v_med3_f32 v11, v29, s74, v215
	v_mov_b32_e32 v9, 0
	v_cvt_pk_fp8_f32 v9, v10, v11
	v_pk_fma_f32 v[26:27], v[44:45], s[24:25], v[18:19] op_sel_hi:[1,0,1]
	v_pk_fma_f32 v[12:13], v[38:39], s[24:25], v[12:13] op_sel_hi:[1,0,1]
	v_med3_f32 v10, v26, s74, v215
	v_med3_f32 v11, v27, s74, v215
	v_cvt_pk_fp8_f32 v9, v10, v11 op_sel:[0,0,1]
	v_pk_fma_f32 v[10:11], v[40:41], s[24:25], v[14:15] op_sel_hi:[1,0,1]
	v_pk_fma_f32 v[14:15], v[36:37], s[24:25], v[18:19] op_sel_hi:[1,0,1]
	v_pk_fma_f32 v[16:17], v[34:35], s[24:25], v[16:17] op_sel_hi:[1,0,1]
	v_med3_f32 v12, v12, s74, v215
	v_med3_f32 v13, v13, s74, v215
	v_med3_f32 v18, v10, s74, v215
	v_mov_b32_e32 v10, 0
	v_med3_f32 v19, v11, s74, v215
	v_cvt_pk_fp8_f32 v10, v12, v13
	v_med3_f32 v12, v16, s74, v215
	v_med3_f32 v13, v17, s74, v215
	v_mov_b32_e32 v11, 0
	v_cvt_pk_fp8_f32 v11, v12, v13
	v_cvt_pk_fp8_f32 v8, v30, v31 op_sel:[0,0,1]
	v_med3_f32 v12, v14, s74, v215
	v_med3_f32 v13, v15, s74, v215
	v_cvt_pk_fp8_f32 v10, v18, v19 op_sel:[0,0,1]
	v_cvt_pk_fp8_f32 v11, v12, v13 op_sel:[0,0,1]
	global_store_dwordx2 v[2:3], v[4:5], off offset:128
	global_store_dwordx2 v[20:21], v[6:7], off offset:128
	global_store_dwordx2 v[22:23], v[8:9], off offset:128
	global_store_dwordx2 v[24:25], v[10:11], off offset:128
	s_cbranch_vccnz .LBB0_858
	s_andn2_b64 vcc, exec, s[14:15]
	s_cbranch_vccnz .LBB0_857
	s_branch .LBB0_857
